# v31 + f32->fp8 weight-conversion inner loops unrolled by two items (loads of item B issued before convert/store of item A), bit-identical
# speedup vs baseline: 1.0118x; 1.0047x over previous
; __device__ __forceinline__ void cv_load(const float* W, int N, int nblk, int item, int lane, f32x4 (&tv)[16]) {
;     const int kb = item / nblk, nb = item - kb * nblk; const float* p = W + (size_t)(64 * kb + 16 * (lane >> 4)) * N + 64 * nb + 4 * (lane & 15);
; #pragma unroll
;     for (int i = 0; i < 16; ++i) tv[i] = __builtin_nontemporal_load((const f32x4*)(p + (size_t)i * N));
; }
; template <int MODE> __device__ __forceinline__ void cv_run4(const float* W, int K, int N, unsigned char* WT, int item0, int lane) {
;     const int nblk = N / 64; f32x4 ta[16];
; #pragma unroll 1
;     for (int j = 0; j < 4; ++j) { cv_load(W, N, nblk, item0 + j, lane, ta); cv_finish<MODE>(ta, K, nblk, WT, item0 + j, lane); }
.LBB0_729:
	s_lshr_b32 s21, s10, 5
	s_lshl_b32 s22, s21, 11
	v_lshl_or_b32 v132, s21, 6, v1
	s_sub_i32 s21, s11, s22
	v_subrev_u32_e32 v21, s22, v4
	v_lshlrev_b64 v[22:23], 13, v[132:133]
	s_add_i32 s22, s12, s21
	v_lshl_add_u64 v[22:23], s[4:5], 0, v[22:23]
	s_ashr_i32 s23, s22, 31
	v_lshlrev_b32_e32 v2, 2, v130
	v_mov_b32_e32 v3, v133
	v_lshl_add_u64 v[22:23], s[22:23], 2, v[22:23]
	s_movk_i32 s13, 0x2000
	v_lshl_add_u64 v[2:3], v[22:23], 0, v[2:3]
	v_add_co_u32_e32 v34, vcc, s13, v2
	s_movk_i32 s14, 0x6000
	s_nop 0
	v_addc_co_u32_e32 v35, vcc, 0, v3, vcc
	v_add_co_u32_e32 v36, vcc, s1, v2
	s_mov_b32 s15, 0xa000
	s_nop 0
	v_addc_co_u32_e32 v37, vcc, 0, v3, vcc
	v_add_co_u32_e32 v38, vcc, s14, v2
	s_mov_b32 s16, 0xe000
	s_nop 0
	v_addc_co_u32_e32 v39, vcc, 0, v3, vcc
	v_add_co_u32_e32 v40, vcc, s78, v2
	s_mov_b32 s17, 0x12000
	s_nop 0
	v_addc_co_u32_e32 v41, vcc, 0, v3, vcc
	v_add_co_u32_e32 v42, vcc, s15, v2
	s_mov_b32 s18, 0x16000
	s_nop 0
	v_addc_co_u32_e32 v43, vcc, 0, v3, vcc
	v_add_co_u32_e32 v46, vcc, s79, v2
	s_mov_b32 s19, 0x1a000
	s_nop 0
	v_addc_co_u32_e32 v47, vcc, 0, v3, vcc
	v_add_co_u32_e32 v50, vcc, s16, v2
	v_add_u32_e32 v24, s12, v21
	s_nop 0
	v_addc_co_u32_e32 v51, vcc, 0, v3, vcc
	v_add_co_u32_e32 v54, vcc, s86, v2
	v_ashrrev_i32_e32 v25, 31, v24
	s_nop 0
	v_addc_co_u32_e32 v55, vcc, 0, v3, vcc
	v_add_co_u32_e32 v58, vcc, s17, v2
	v_add_u32_e32 v28, 1, v24
	s_nop 0
	v_addc_co_u32_e32 v59, vcc, 0, v3, vcc
	v_add_co_u32_e32 v62, vcc, s87, v2
	v_add_u32_e32 v30, 2, v24
	s_nop 0
	v_addc_co_u32_e32 v63, vcc, 0, v3, vcc
	v_add_co_u32_e32 v66, vcc, s18, v2
	v_add_u32_e32 v32, 3, v24
	s_nop 0
	v_addc_co_u32_e32 v67, vcc, 0, v3, vcc
	v_add_co_u32_e32 v70, vcc, s85, v2
	s_mov_b32 s20, 0x1e000
	s_nop 0
	v_addc_co_u32_e32 v71, vcc, 0, v3, vcc
	v_add_co_u32_e32 v74, vcc, s19, v2
	v_lshl_add_u64 v[26:27], s[6:7], 0, v[132:133]
	s_nop 0
	v_addc_co_u32_e32 v75, vcc, 0, v3, vcc
	v_add_co_u32_e32 v78, vcc, s82, v2
	v_lshlrev_b64 v[24:25], 11, v[24:25]
	v_ashrrev_i32_e32 v29, 31, v28
	v_ashrrev_i32_e32 v31, 31, v30
	v_ashrrev_i32_e32 v33, 31, v32
	v_addc_co_u32_e32 v79, vcc, 0, v3, vcc
	v_lshl_add_u64 v[86:87], v[26:27], 0, v[24:25]
	v_lshlrev_b64 v[28:29], 11, v[28:29]
	v_lshlrev_b64 v[30:31], 11, v[30:31]
	v_lshlrev_b64 v[32:33], 11, v[32:33]
	global_load_dwordx4 v[22:25], v[2:3], off nt
	v_add_co_u32_e32 v2, vcc, s20, v2
	v_lshl_add_u64 v[88:89], v[26:27], 0, v[28:29]
	s_nop 0
	v_addc_co_u32_e32 v3, vcc, 0, v3, vcc
	v_lshl_add_u64 v[90:91], v[26:27], 0, v[30:31]
	v_lshl_add_u64 v[92:93], v[26:27], 0, v[32:33]
	global_load_dwordx4 v[26:29], v[34:35], off nt
	global_load_dwordx4 v[30:33], v[36:37], off nt
	s_nop 0
	global_load_dwordx4 v[34:37], v[38:39], off nt
	s_nop 0
	global_load_dwordx4 v[38:41], v[40:41], off nt
	s_nop 0
	global_load_dwordx4 v[42:45], v[42:43], off nt
	s_nop 0
	global_load_dwordx4 v[46:49], v[46:47], off nt
	s_nop 0
	global_load_dwordx4 v[50:53], v[50:51], off nt
	s_nop 0
	global_load_dwordx4 v[54:57], v[54:55], off nt
	s_nop 0
	global_load_dwordx4 v[58:61], v[58:59], off nt
	s_nop 0
	global_load_dwordx4 v[62:65], v[62:63], off nt
	s_nop 0
	global_load_dwordx4 v[66:69], v[66:67], off nt
	s_nop 0
	global_load_dwordx4 v[70:73], v[70:71], off nt
	s_nop 0
	global_load_dwordx4 v[74:77], v[74:75], off nt
	s_nop 0
	global_load_dwordx4 v[78:81], v[78:79], off nt
	s_nop 0
	global_load_dwordx4 v[82:85], v[2:3], off nt
	v_mov_b32_e32 v5, v133
	v_mov_b32_e32 v6, v133
	v_mov_b32_e32 v7, v133
	v_mov_b32_e32 v8, v133
	v_mov_b32_e32 v9, v133
	v_mov_b32_e32 v10, v133
	v_mov_b32_e32 v11, v133
	v_mov_b32_e32 v12, v133
	v_mov_b32_e32 v13, v133
	v_mov_b32_e32 v14, v133
	v_mov_b32_e32 v15, v133
	v_mov_b32_e32 v16, v133
	v_mov_b32_e32 v17, v133
	v_mov_b32_e32 v18, v133
	v_mov_b32_e32 v19, v133
	v_mov_b32_e32 v20, v133
	s_add_i32 s10, s10, 1
	s_add_i32 s12, s12, 64
	v_mov_b32_e32 v211, v133
	s_lshr_b32 s21, s10, 5
	s_lshl_b32 s22, s21, 11
	v_lshl_or_b32 v210, s21, 6, v1
	s_sub_i32 s21, s11, s22
	v_subrev_u32_e32 v115, s22, v4
	v_lshlrev_b64 v[116:117], 13, v[210:211]
	s_add_i32 s22, s12, s21
	v_lshl_add_u64 v[116:117], s[4:5], 0, v[116:117]
	s_ashr_i32 s23, s22, 31
	v_lshlrev_b32_e32 v98, 2, v130
	v_mov_b32_e32 v99, v211
	v_lshl_add_u64 v[116:117], s[22:23], 2, v[116:117]
	s_movk_i32 s13, 0x2000
	v_lshl_add_u64 v[98:99], v[116:117], 0, v[98:99]
	v_add_co_u32_e32 v136, vcc, s13, v98
	s_movk_i32 s14, 0x6000
	s_nop 0
	v_addc_co_u32_e32 v137, vcc, 0, v99, vcc
	v_add_co_u32_e32 v138, vcc, s1, v98
	s_mov_b32 s15, 0xa000
	s_nop 0
	v_addc_co_u32_e32 v139, vcc, 0, v99, vcc
	v_add_co_u32_e32 v140, vcc, s14, v98
	s_mov_b32 s16, 0xe000
	s_nop 0
	v_addc_co_u32_e32 v141, vcc, 0, v99, vcc
	v_add_co_u32_e32 v142, vcc, s78, v98
	s_mov_b32 s17, 0x12000
	s_nop 0
	v_addc_co_u32_e32 v143, vcc, 0, v99, vcc
	v_add_co_u32_e32 v152, vcc, s15, v98
	s_mov_b32 s18, 0x16000
	s_nop 0
	v_addc_co_u32_e32 v153, vcc, 0, v99, vcc
	v_add_co_u32_e32 v156, vcc, s79, v98
	s_mov_b32 s19, 0x1a000
	s_nop 0
	v_addc_co_u32_e32 v157, vcc, 0, v99, vcc
	v_add_co_u32_e32 v160, vcc, s16, v98
	v_add_u32_e32 v118, s12, v115
	s_nop 0
	v_addc_co_u32_e32 v161, vcc, 0, v99, vcc
	v_add_co_u32_e32 v164, vcc, s86, v98
	v_ashrrev_i32_e32 v119, 31, v118
	s_nop 0
	v_addc_co_u32_e32 v165, vcc, 0, v99, vcc
	v_add_co_u32_e32 v174, vcc, s17, v98
	v_add_u32_e32 v122, 1, v118
	s_nop 0
	v_addc_co_u32_e32 v175, vcc, 0, v99, vcc
	v_add_co_u32_e32 v178, vcc, s87, v98
	v_add_u32_e32 v124, 2, v118
	s_nop 0
	v_addc_co_u32_e32 v179, vcc, 0, v99, vcc
	v_add_co_u32_e32 v182, vcc, s18, v98
	v_add_u32_e32 v126, 3, v118
	s_nop 0
	v_addc_co_u32_e32 v183, vcc, 0, v99, vcc
	v_add_co_u32_e32 v186, vcc, s85, v98
; __device__ __forceinline__ void cv_load(const float* W, int N, int nblk, int item, int lane, f32x4 (&tv)[16]) {
;     const int kb = item / nblk, nb = item - kb * nblk; const float* p = W + (size_t)(64 * kb + 16 * (lane >> 4)) * N + 64 * nb + 4 * (lane & 15);
; #pragma unroll
;     for (int i = 0; i < 16; ++i) tv[i] = __builtin_nontemporal_load((const f32x4*)(p + (size_t)i * N));
; }
; template <int MODE> __device__ __forceinline__ void cv_finish(const f32x4 (&tv)[16], int K, int nblk, unsigned char* WT, int item, int lane) {
;     const int kb = item / nblk, nb = item - kb * nblk, k0 = 64 * kb + 16 * (lane >> 4), n0 = 64 * nb + 4 * (lane & 15);
;     unsigned D[16];
; #pragma unroll
;     for (int i = 0; i < 16; ++i) { const f32x2 a = (f32x2){tv[i].x, tv[i].y} * (f32x2){1024.f, 1024.f}, b = (f32x2){tv[i].z, tv[i].w} * (f32x2){1024.f, 1024.f};
;         D[i] = pk4_fp8(a.x, a.y, b.x, b.y); }
	s_mov_b32 s20, 0x1e000
	s_nop 0
	v_addc_co_u32_e32 v187, vcc, 0, v99, vcc
	v_add_co_u32_e32 v190, vcc, s19, v98
	v_lshl_add_u64 v[120:121], s[6:7], 0, v[210:211]
	s_nop 0
	v_addc_co_u32_e32 v191, vcc, 0, v99, vcc
	v_add_co_u32_e32 v194, vcc, s82, v98
	v_lshlrev_b64 v[118:119], 11, v[118:119]
	v_ashrrev_i32_e32 v123, 31, v122
	v_ashrrev_i32_e32 v125, 31, v124
	v_ashrrev_i32_e32 v127, 31, v126
	v_addc_co_u32_e32 v195, vcc, 0, v99, vcc
	v_lshl_add_u64 v[128:129], v[120:121], 0, v[118:119]
	v_lshlrev_b64 v[122:123], 11, v[122:123]
	v_lshlrev_b64 v[124:125], 11, v[124:125]
	v_lshlrev_b64 v[126:127], 11, v[126:127]
	global_load_dwordx4 v[116:119], v[98:99], off nt
	v_add_co_u32_e32 v98, vcc, s20, v98
	v_lshl_add_u64 v[168:169], v[120:121], 0, v[122:123]
	s_nop 0
	v_addc_co_u32_e32 v99, vcc, 0, v99, vcc
	v_lshl_add_u64 v[202:203], v[120:121], 0, v[124:125]
	v_lshl_add_u64 v[204:205], v[120:121], 0, v[126:127]
	global_load_dwordx4 v[120:123], v[136:137], off nt
	global_load_dwordx4 v[124:127], v[138:139], off nt
	s_nop 0
	global_load_dwordx4 v[136:139], v[140:141], off nt
	s_nop 0
	global_load_dwordx4 v[140:143], v[142:143], off nt
	s_nop 0
	global_load_dwordx4 v[152:155], v[152:153], off nt
	s_nop 0
	global_load_dwordx4 v[156:159], v[156:157], off nt
	s_nop 0
	global_load_dwordx4 v[160:163], v[160:161], off nt
	s_nop 0
	global_load_dwordx4 v[164:167], v[164:165], off nt
	s_nop 0
	global_load_dwordx4 v[174:177], v[174:175], off nt
	s_nop 0
	global_load_dwordx4 v[178:181], v[178:179], off nt
	s_nop 0
	global_load_dwordx4 v[182:185], v[182:183], off nt
	s_nop 0
	global_load_dwordx4 v[186:189], v[186:187], off nt
	s_nop 0
	global_load_dwordx4 v[190:193], v[190:191], off nt
	s_nop 0
	global_load_dwordx4 v[194:197], v[194:195], off nt
	s_nop 0
	global_load_dwordx4 v[198:201], v[98:99], off nt
	v_mov_b32_e32 v97, v211
	v_mov_b32_e32 v100, v211
	v_mov_b32_e32 v101, v211
	v_mov_b32_e32 v102, v211
	v_mov_b32_e32 v103, v211
	v_mov_b32_e32 v104, v211
	v_mov_b32_e32 v105, v211
	v_mov_b32_e32 v106, v211
	v_mov_b32_e32 v107, v211
	v_mov_b32_e32 v108, v211
	v_mov_b32_e32 v109, v211
	v_mov_b32_e32 v110, v211
	v_mov_b32_e32 v111, v211
	v_mov_b32_e32 v112, v211
	v_mov_b32_e32 v113, v211
	v_mov_b32_e32 v114, v211
	s_add_i32 s10, s10, 1
	s_add_i32 s12, s12, 64
	s_cmpk_eq_i32 s12, 0x100
	s_waitcnt vmcnt(31)
	v_pk_mul_f32 v[2:3], v[22:23], s[84:85] op_sel_hi:[1,0]
	v_pk_mul_f32 v[22:23], v[24:25], s[84:85] op_sel_hi:[1,0]
	v_med3_f32 v21, v2, s96, v150
	v_med3_f32 v94, v3, s96, v150
	v_med3_f32 v95, v22, s96, v150
	v_med3_f32 v96, v23, s96, v150
	s_waitcnt vmcnt(30)
	v_pk_mul_f32 v[2:3], v[26:27], s[84:85] op_sel_hi:[1,0]
	v_pk_mul_f32 v[22:23], v[28:29], s[84:85] op_sel_hi:[1,0]
	s_waitcnt vmcnt(29)
	v_pk_mul_f32 v[24:25], v[30:31], s[84:85] op_sel_hi:[1,0]
	v_pk_mul_f32 v[26:27], v[32:33], s[84:85] op_sel_hi:[1,0]
	s_waitcnt vmcnt(28)
	v_pk_mul_f32 v[28:29], v[34:35], s[84:85] op_sel_hi:[1,0]
	v_pk_mul_f32 v[30:31], v[36:37], s[84:85] op_sel_hi:[1,0]
	s_waitcnt vmcnt(27)
	v_pk_mul_f32 v[32:33], v[38:39], s[84:85] op_sel_hi:[1,0]
	v_pk_mul_f32 v[34:35], v[40:41], s[84:85] op_sel_hi:[1,0]
	s_waitcnt vmcnt(26)
	v_pk_mul_f32 v[36:37], v[42:43], s[84:85] op_sel_hi:[1,0]
	v_pk_mul_f32 v[38:39], v[44:45], s[84:85] op_sel_hi:[1,0]
	s_waitcnt vmcnt(25)
	v_pk_mul_f32 v[40:41], v[46:47], s[84:85] op_sel_hi:[1,0]
	v_pk_mul_f32 v[42:43], v[48:49], s[84:85] op_sel_hi:[1,0]
	s_waitcnt vmcnt(24)
	v_pk_mul_f32 v[44:45], v[50:51], s[84:85] op_sel_hi:[1,0]
	v_pk_mul_f32 v[46:47], v[52:53], s[84:85] op_sel_hi:[1,0]
	s_waitcnt vmcnt(23)
	v_pk_mul_f32 v[48:49], v[54:55], s[84:85] op_sel_hi:[1,0]
	v_pk_mul_f32 v[50:51], v[56:57], s[84:85] op_sel_hi:[1,0]
	s_waitcnt vmcnt(22)
	v_pk_mul_f32 v[52:53], v[58:59], s[84:85] op_sel_hi:[1,0]
	v_pk_mul_f32 v[54:55], v[60:61], s[84:85] op_sel_hi:[1,0]
	s_waitcnt vmcnt(21)
	v_pk_mul_f32 v[56:57], v[62:63], s[84:85] op_sel_hi:[1,0]
	v_pk_mul_f32 v[58:59], v[64:65], s[84:85] op_sel_hi:[1,0]
	s_waitcnt vmcnt(20)
	v_pk_mul_f32 v[60:61], v[66:67], s[84:85] op_sel_hi:[1,0]
	v_pk_mul_f32 v[62:63], v[68:69], s[84:85] op_sel_hi:[1,0]
	s_waitcnt vmcnt(19)
	v_pk_mul_f32 v[64:65], v[70:71], s[84:85] op_sel_hi:[1,0]
	v_pk_mul_f32 v[66:67], v[72:73], s[84:85] op_sel_hi:[1,0]
	s_waitcnt vmcnt(18)
	v_pk_mul_f32 v[68:69], v[74:75], s[84:85] op_sel_hi:[1,0]
	v_pk_mul_f32 v[70:71], v[76:77], s[84:85] op_sel_hi:[1,0]
	s_waitcnt vmcnt(17)
	v_pk_mul_f32 v[72:73], v[78:79], s[84:85] op_sel_hi:[1,0]
	v_pk_mul_f32 v[74:75], v[80:81], s[84:85] op_sel_hi:[1,0]
	s_waitcnt vmcnt(16)
; template <int MODE> __device__ __forceinline__ void cv_finish(const f32x4 (&tv)[16], int K, int nblk, unsigned char* WT, int item, int lane) {
;     const int kb = item / nblk, nb = item - kb * nblk, k0 = 64 * kb + 16 * (lane >> 4), n0 = 64 * nb + 4 * (lane & 15);
;     unsigned D[16];
; #pragma unroll
;     for (int i = 0; i < 16; ++i) { const f32x2 a = (f32x2){tv[i].x, tv[i].y} * (f32x2){1024.f, 1024.f}, b = (f32x2){tv[i].z, tv[i].w} * (f32x2){1024.f, 1024.f};
;         D[i] = pk4_fp8(a.x, a.y, b.x, b.y); }
;     unsigned O[4][4];
; #pragma unroll
;     for (int q = 0; q < 4; ++q) { const unsigned a = D[4 * q], b = D[4 * q + 1], c = D[4 * q + 2], d = D[4 * q + 3];
;         const unsigned t0 = __builtin_amdgcn_perm(b, a, 0x05010400u), t1 = __builtin_amdgcn_perm(b, a, 0x07030602u), u0 = __builtin_amdgcn_perm(d, c, 0x05010400u), u1 = __builtin_amdgcn_perm(d, c, 0x07030602u);
;         O[0][q] = __builtin_amdgcn_perm(u0, t0, 0x05040100u); O[1][q] = __builtin_amdgcn_perm(u0, t0, 0x07060302u); O[2][q] = __builtin_amdgcn_perm(u1, t1, 0x05040100u); O[3][q] = __builtin_amdgcn_perm(u1, t1, 0x07060302u); }
; #pragma unroll
;     for (int j = 0; j < 4; ++j) { u32x4 o; o.x = O[j][0]; o.y = O[j][1]; o.z = O[j][2]; o.w = O[j][3];
;         __builtin_nontemporal_store(o, (u32x4*)(WT + (size_t)drow<MODE>(n0 + j) * K + k0)); }
; }
	v_pk_mul_f32 v[76:77], v[82:83], s[84:85] op_sel_hi:[1,0]
	v_cvt_pk_fp8_f32 v5, v21, v94
	v_med3_f32 v2, v2, s96, v150
	v_med3_f32 v3, v3, s96, v150
	v_med3_f32 v21, v22, s96, v150
	v_med3_f32 v22, v23, s96, v150
	v_med3_f32 v23, v24, s96, v150
	v_med3_f32 v24, v25, s96, v150
	v_med3_f32 v25, v26, s96, v150
	v_med3_f32 v26, v27, s96, v150
	v_med3_f32 v27, v28, s96, v150
	v_med3_f32 v28, v29, s96, v150
	v_med3_f32 v29, v30, s96, v150
	v_med3_f32 v30, v31, s96, v150
	v_med3_f32 v31, v32, s96, v150
	v_med3_f32 v32, v33, s96, v150
	v_med3_f32 v33, v34, s96, v150
	v_med3_f32 v34, v35, s96, v150
	v_med3_f32 v35, v36, s96, v150
	v_med3_f32 v36, v37, s96, v150
	v_med3_f32 v37, v38, s96, v150
	v_med3_f32 v38, v39, s96, v150
	v_med3_f32 v39, v40, s96, v150
	v_med3_f32 v40, v41, s96, v150
	v_med3_f32 v41, v42, s96, v150
	v_med3_f32 v42, v43, s96, v150
	v_med3_f32 v43, v44, s96, v150
	v_med3_f32 v44, v45, s96, v150
	v_med3_f32 v45, v46, s96, v150
	v_med3_f32 v46, v47, s96, v150
	v_med3_f32 v47, v48, s96, v150
	v_med3_f32 v48, v49, s96, v150
	v_med3_f32 v49, v50, s96, v150
	v_med3_f32 v50, v51, s96, v150
	v_med3_f32 v51, v52, s96, v150
	v_med3_f32 v52, v53, s96, v150
	v_med3_f32 v53, v54, s96, v150
	v_med3_f32 v54, v55, s96, v150
	v_med3_f32 v55, v56, s96, v150
	v_med3_f32 v56, v57, s96, v150
	v_med3_f32 v57, v58, s96, v150
	v_med3_f32 v58, v59, s96, v150
	v_med3_f32 v59, v60, s96, v150
	v_med3_f32 v60, v61, s96, v150
	v_med3_f32 v61, v62, s96, v150
	v_med3_f32 v62, v63, s96, v150
	v_med3_f32 v63, v64, s96, v150
	v_med3_f32 v64, v65, s96, v150
	v_med3_f32 v65, v66, s96, v150
	v_med3_f32 v66, v67, s96, v150
	v_med3_f32 v67, v68, s96, v150
	v_med3_f32 v68, v69, s96, v150
	v_med3_f32 v69, v70, s96, v150
	v_med3_f32 v70, v71, s96, v150
	v_med3_f32 v71, v72, s96, v150
	v_med3_f32 v72, v73, s96, v150
	v_med3_f32 v73, v74, s96, v150
	v_med3_f32 v74, v75, s96, v150
	v_med3_f32 v75, v76, s96, v150
	v_med3_f32 v76, v77, s96, v150
	v_cvt_pk_fp8_f32 v6, v2, v3
	v_cvt_pk_fp8_f32 v7, v23, v24
	v_cvt_pk_fp8_f32 v8, v27, v28
	v_cvt_pk_fp8_f32 v9, v31, v32
	v_cvt_pk_fp8_f32 v10, v35, v36
	v_cvt_pk_fp8_f32 v11, v39, v40
	v_cvt_pk_fp8_f32 v12, v43, v44
	v_cvt_pk_fp8_f32 v13, v47, v48
	v_cvt_pk_fp8_f32 v14, v51, v52
	v_cvt_pk_fp8_f32 v15, v55, v56
	v_cvt_pk_fp8_f32 v16, v59, v60
	v_cvt_pk_fp8_f32 v17, v63, v64
	v_cvt_pk_fp8_f32 v18, v67, v68
	v_cvt_pk_fp8_f32 v19, v71, v72
	v_cvt_pk_fp8_f32 v20, v75, v76
	v_pk_mul_f32 v[78:79], v[84:85], s[84:85] op_sel_hi:[1,0]
	v_cvt_pk_fp8_f32 v5, v95, v96 op_sel:[0,0,1]
	v_med3_f32 v77, v78, s96, v150
	v_med3_f32 v78, v79, s96, v150
	v_cvt_pk_fp8_f32 v6, v21, v22 op_sel:[0,0,1]
	v_cvt_pk_fp8_f32 v7, v25, v26 op_sel:[0,0,1]
	v_cvt_pk_fp8_f32 v8, v29, v30 op_sel:[0,0,1]
	v_cvt_pk_fp8_f32 v9, v33, v34 op_sel:[0,0,1]
	v_cvt_pk_fp8_f32 v10, v37, v38 op_sel:[0,0,1]
	v_cvt_pk_fp8_f32 v11, v41, v42 op_sel:[0,0,1]
	v_cvt_pk_fp8_f32 v12, v45, v46 op_sel:[0,0,1]
	v_cvt_pk_fp8_f32 v13, v49, v50 op_sel:[0,0,1]
	v_cvt_pk_fp8_f32 v14, v53, v54 op_sel:[0,0,1]
	v_cvt_pk_fp8_f32 v15, v57, v58 op_sel:[0,0,1]
	v_cvt_pk_fp8_f32 v16, v61, v62 op_sel:[0,0,1]
	v_cvt_pk_fp8_f32 v17, v65, v66 op_sel:[0,0,1]
	v_cvt_pk_fp8_f32 v18, v69, v70 op_sel:[0,0,1]
	v_cvt_pk_fp8_f32 v19, v73, v74 op_sel:[0,0,1]
	v_cvt_pk_fp8_f32 v20, v77, v78 op_sel:[0,0,1]
	v_perm_b32 v2, v6, v5, s97
	v_perm_b32 v3, v6, v5, s70
	v_perm_b32 v5, v8, v7, s97
	v_perm_b32 v7, v8, v7, s70
	v_perm_b32 v8, v10, v9, s97
	v_perm_b32 v9, v10, v9, s70
	v_perm_b32 v21, v12, v11, s97
	v_perm_b32 v12, v12, v11, s70
	v_perm_b32 v22, v14, v13, s97
	v_perm_b32 v23, v16, v15, s97
	v_perm_b32 v25, v18, v17, s97
	v_perm_b32 v26, v18, v17, s70
	v_perm_b32 v17, v20, v19, s97
	v_perm_b32 v13, v14, v13, s70
	v_perm_b32 v24, v16, v15, s70
	v_perm_b32 v27, v20, v19, s70
	v_perm_b32 v6, v5, v2, s71
	v_perm_b32 v14, v7, v3, s71
	v_perm_b32 v18, v7, v3, s72
	v_perm_b32 v7, v21, v8, s71
	v_perm_b32 v11, v21, v8, s72
	v_perm_b32 v15, v12, v9, s71
	v_perm_b32 v19, v12, v9, s72
	v_perm_b32 v8, v23, v22, s71
	v_perm_b32 v9, v17, v25, s71
	v_perm_b32 v10, v5, v2, s72
	v_perm_b32 v12, v23, v22, s72
	v_perm_b32 v16, v24, v13, s71
	v_perm_b32 v20, v24, v13, s72
	v_perm_b32 v13, v17, v25, s72
	v_perm_b32 v17, v27, v26, s71
	v_perm_b32 v21, v27, v26, s72
	global_store_dwordx4 v[86:87], v[6:9], off nt
	global_store_dwordx4 v[88:89], v[10:13], off nt
	global_store_dwordx4 v[90:91], v[14:17], off nt
	global_store_dwordx4 v[92:93], v[18:21], off nt
	s_waitcnt vmcnt(19)
	v_pk_mul_f32 v[98:99], v[116:117], s[84:85] op_sel_hi:[1,0]
	v_pk_mul_f32 v[116:117], v[118:119], s[84:85] op_sel_hi:[1,0]
	v_med3_f32 v115, v98, s96, v150
	v_med3_f32 v206, v99, s96, v150
	v_med3_f32 v145, v116, s96, v150
	v_med3_f32 v208, v117, s96, v150
	s_waitcnt vmcnt(18)
	v_pk_mul_f32 v[98:99], v[120:121], s[84:85] op_sel_hi:[1,0]
	v_pk_mul_f32 v[116:117], v[122:123], s[84:85] op_sel_hi:[1,0]
	s_waitcnt vmcnt(17)
	v_pk_mul_f32 v[118:119], v[124:125], s[84:85] op_sel_hi:[1,0]
	v_pk_mul_f32 v[120:121], v[126:127], s[84:85] op_sel_hi:[1,0]
	s_waitcnt vmcnt(16)
	v_pk_mul_f32 v[122:123], v[136:137], s[84:85] op_sel_hi:[1,0]
	v_pk_mul_f32 v[124:125], v[138:139], s[84:85] op_sel_hi:[1,0]
	s_waitcnt vmcnt(15)
	v_pk_mul_f32 v[126:127], v[140:141], s[84:85] op_sel_hi:[1,0]
	v_pk_mul_f32 v[136:137], v[142:143], s[84:85] op_sel_hi:[1,0]
	s_waitcnt vmcnt(14)
	v_pk_mul_f32 v[138:139], v[152:153], s[84:85] op_sel_hi:[1,0]
	v_pk_mul_f32 v[140:141], v[154:155], s[84:85] op_sel_hi:[1,0]
	s_waitcnt vmcnt(13)
	v_pk_mul_f32 v[142:143], v[156:157], s[84:85] op_sel_hi:[1,0]
	v_pk_mul_f32 v[152:153], v[158:159], s[84:85] op_sel_hi:[1,0]
	s_waitcnt vmcnt(12)
; template <int MODE> __device__ __forceinline__ void cv_finish(const f32x4 (&tv)[16], int K, int nblk, unsigned char* WT, int item, int lane) {
;     const int kb = item / nblk, nb = item - kb * nblk, k0 = 64 * kb + 16 * (lane >> 4), n0 = 64 * nb + 4 * (lane & 15);
;     unsigned D[16];
; #pragma unroll
;     for (int i = 0; i < 16; ++i) { const f32x2 a = (f32x2){tv[i].x, tv[i].y} * (f32x2){1024.f, 1024.f}, b = (f32x2){tv[i].z, tv[i].w} * (f32x2){1024.f, 1024.f};
;         D[i] = pk4_fp8(a.x, a.y, b.x, b.y); }
;     unsigned O[4][4];
; #pragma unroll
;     for (int q = 0; q < 4; ++q) { const unsigned a = D[4 * q], b = D[4 * q + 1], c = D[4 * q + 2], d = D[4 * q + 3];
;         const unsigned t0 = __builtin_amdgcn_perm(b, a, 0x05010400u), t1 = __builtin_amdgcn_perm(b, a, 0x07030602u), u0 = __builtin_amdgcn_perm(d, c, 0x05010400u), u1 = __builtin_amdgcn_perm(d, c, 0x07030602u);
;         O[0][q] = __builtin_amdgcn_perm(u0, t0, 0x05040100u); O[1][q] = __builtin_amdgcn_perm(u0, t0, 0x07060302u); O[2][q] = __builtin_amdgcn_perm(u1, t1, 0x05040100u); O[3][q] = __builtin_amdgcn_perm(u1, t1, 0x07060302u); }
; #pragma unroll
;     for (int j = 0; j < 4; ++j) { u32x4 o; o.x = O[j][0]; o.y = O[j][1]; o.z = O[j][2]; o.w = O[j][3];
;         __builtin_nontemporal_store(o, (u32x4*)(WT + (size_t)drow<MODE>(n0 + j) * K + k0)); }
; }
	v_pk_mul_f32 v[154:155], v[160:161], s[84:85] op_sel_hi:[1,0]
	v_pk_mul_f32 v[156:157], v[162:163], s[84:85] op_sel_hi:[1,0]
	s_waitcnt vmcnt(11)
	v_pk_mul_f32 v[158:159], v[164:165], s[84:85] op_sel_hi:[1,0]
	v_pk_mul_f32 v[160:161], v[166:167], s[84:85] op_sel_hi:[1,0]
	s_waitcnt vmcnt(10)
	v_pk_mul_f32 v[162:163], v[174:175], s[84:85] op_sel_hi:[1,0]
	v_pk_mul_f32 v[164:165], v[176:177], s[84:85] op_sel_hi:[1,0]
	s_waitcnt vmcnt(9)
	v_pk_mul_f32 v[166:167], v[178:179], s[84:85] op_sel_hi:[1,0]
	v_pk_mul_f32 v[174:175], v[180:181], s[84:85] op_sel_hi:[1,0]
	s_waitcnt vmcnt(8)
	v_pk_mul_f32 v[176:177], v[182:183], s[84:85] op_sel_hi:[1,0]
	v_pk_mul_f32 v[178:179], v[184:185], s[84:85] op_sel_hi:[1,0]
	s_waitcnt vmcnt(7)
	v_pk_mul_f32 v[180:181], v[186:187], s[84:85] op_sel_hi:[1,0]
	v_pk_mul_f32 v[182:183], v[188:189], s[84:85] op_sel_hi:[1,0]
	s_waitcnt vmcnt(6)
	v_pk_mul_f32 v[184:185], v[190:191], s[84:85] op_sel_hi:[1,0]
	v_pk_mul_f32 v[186:187], v[192:193], s[84:85] op_sel_hi:[1,0]
	s_waitcnt vmcnt(5)
	v_pk_mul_f32 v[188:189], v[194:195], s[84:85] op_sel_hi:[1,0]
	v_pk_mul_f32 v[190:191], v[196:197], s[84:85] op_sel_hi:[1,0]
	s_waitcnt vmcnt(4)
	v_pk_mul_f32 v[192:193], v[198:199], s[84:85] op_sel_hi:[1,0]
	v_cvt_pk_fp8_f32 v97, v115, v206
	v_med3_f32 v98, v98, s96, v150
	v_med3_f32 v99, v99, s96, v150
	v_med3_f32 v115, v116, s96, v150
	v_med3_f32 v116, v117, s96, v150
	v_med3_f32 v117, v118, s96, v150
	v_med3_f32 v118, v119, s96, v150
	v_med3_f32 v119, v120, s96, v150
	v_med3_f32 v120, v121, s96, v150
	v_med3_f32 v121, v122, s96, v150
	v_med3_f32 v122, v123, s96, v150
	v_med3_f32 v123, v124, s96, v150
	v_med3_f32 v124, v125, s96, v150
	v_med3_f32 v125, v126, s96, v150
	v_med3_f32 v126, v127, s96, v150
	v_med3_f32 v127, v136, s96, v150
	v_med3_f32 v136, v137, s96, v150
	v_med3_f32 v137, v138, s96, v150
	v_med3_f32 v138, v139, s96, v150
	v_med3_f32 v139, v140, s96, v150
	v_med3_f32 v140, v141, s96, v150
	v_med3_f32 v141, v142, s96, v150
	v_med3_f32 v142, v143, s96, v150
	v_med3_f32 v143, v152, s96, v150
	v_med3_f32 v152, v153, s96, v150
	v_med3_f32 v153, v154, s96, v150
	v_med3_f32 v154, v155, s96, v150
	v_med3_f32 v155, v156, s96, v150
	v_med3_f32 v156, v157, s96, v150
	v_med3_f32 v157, v158, s96, v150
	v_med3_f32 v158, v159, s96, v150
	v_med3_f32 v159, v160, s96, v150
	v_med3_f32 v160, v161, s96, v150
	v_med3_f32 v161, v162, s96, v150
	v_med3_f32 v162, v163, s96, v150
	v_med3_f32 v163, v164, s96, v150
	v_med3_f32 v164, v165, s96, v150
	v_med3_f32 v165, v166, s96, v150
	v_med3_f32 v166, v167, s96, v150
	v_med3_f32 v167, v174, s96, v150
	v_med3_f32 v174, v175, s96, v150
	v_med3_f32 v175, v176, s96, v150
	v_med3_f32 v176, v177, s96, v150
	v_med3_f32 v177, v178, s96, v150
	v_med3_f32 v178, v179, s96, v150
	v_med3_f32 v179, v180, s96, v150
	v_med3_f32 v180, v181, s96, v150
	v_med3_f32 v181, v182, s96, v150
	v_med3_f32 v182, v183, s96, v150
	v_med3_f32 v183, v184, s96, v150
	v_med3_f32 v184, v185, s96, v150
	v_med3_f32 v185, v186, s96, v150
	v_med3_f32 v186, v187, s96, v150
	v_med3_f32 v187, v188, s96, v150
	v_med3_f32 v188, v189, s96, v150
	v_med3_f32 v189, v190, s96, v150
	v_med3_f32 v190, v191, s96, v150
	v_med3_f32 v191, v192, s96, v150
	v_med3_f32 v192, v193, s96, v150
	v_cvt_pk_fp8_f32 v100, v98, v99
	v_cvt_pk_fp8_f32 v101, v117, v118
	v_cvt_pk_fp8_f32 v102, v121, v122
	v_cvt_pk_fp8_f32 v103, v125, v126
	v_cvt_pk_fp8_f32 v104, v137, v138
	v_cvt_pk_fp8_f32 v105, v141, v142
	v_cvt_pk_fp8_f32 v106, v153, v154
	v_cvt_pk_fp8_f32 v107, v157, v158
	v_cvt_pk_fp8_f32 v108, v161, v162
	v_cvt_pk_fp8_f32 v109, v165, v166
	v_cvt_pk_fp8_f32 v110, v175, v176
	v_cvt_pk_fp8_f32 v111, v179, v180
	v_cvt_pk_fp8_f32 v112, v183, v184
	v_cvt_pk_fp8_f32 v113, v187, v188
	v_cvt_pk_fp8_f32 v114, v191, v192
	v_pk_mul_f32 v[194:195], v[200:201], s[84:85] op_sel_hi:[1,0]
	v_cvt_pk_fp8_f32 v97, v145, v208 op_sel:[0,0,1]
	v_med3_f32 v193, v194, s96, v150
	v_med3_f32 v194, v195, s96, v150
	v_cvt_pk_fp8_f32 v100, v115, v116 op_sel:[0,0,1]
	v_cvt_pk_fp8_f32 v101, v119, v120 op_sel:[0,0,1]
	v_cvt_pk_fp8_f32 v102, v123, v124 op_sel:[0,0,1]
	v_cvt_pk_fp8_f32 v103, v127, v136 op_sel:[0,0,1]
	v_cvt_pk_fp8_f32 v104, v139, v140 op_sel:[0,0,1]
	v_cvt_pk_fp8_f32 v105, v143, v152 op_sel:[0,0,1]
	v_cvt_pk_fp8_f32 v106, v155, v156 op_sel:[0,0,1]
	v_cvt_pk_fp8_f32 v107, v159, v160 op_sel:[0,0,1]
	v_cvt_pk_fp8_f32 v108, v163, v164 op_sel:[0,0,1]
	v_cvt_pk_fp8_f32 v109, v167, v174 op_sel:[0,0,1]
	v_cvt_pk_fp8_f32 v110, v177, v178 op_sel:[0,0,1]
	v_cvt_pk_fp8_f32 v111, v181, v182 op_sel:[0,0,1]
	v_cvt_pk_fp8_f32 v112, v185, v186 op_sel:[0,0,1]
	v_cvt_pk_fp8_f32 v113, v189, v190 op_sel:[0,0,1]
	v_cvt_pk_fp8_f32 v114, v193, v194 op_sel:[0,0,1]
	v_perm_b32 v98, v100, v97, s97
	v_perm_b32 v99, v100, v97, s70
	v_perm_b32 v97, v102, v101, s97
	v_perm_b32 v101, v102, v101, s70
	v_perm_b32 v102, v104, v103, s97
	v_perm_b32 v103, v104, v103, s70
	v_perm_b32 v115, v106, v105, s97
	v_perm_b32 v106, v106, v105, s70
	v_perm_b32 v116, v108, v107, s97
	v_perm_b32 v117, v110, v109, s97
	v_perm_b32 v119, v112, v111, s97
	v_perm_b32 v120, v112, v111, s70
	v_perm_b32 v111, v114, v113, s97
	v_perm_b32 v107, v108, v107, s70
	v_perm_b32 v118, v110, v109, s70
	v_perm_b32 v121, v114, v113, s70
	v_perm_b32 v100, v97, v98, s71
	v_perm_b32 v108, v101, v99, s71
	v_perm_b32 v112, v101, v99, s72
	v_perm_b32 v101, v115, v102, s71
	v_perm_b32 v105, v115, v102, s72
	v_perm_b32 v109, v106, v103, s71
	v_perm_b32 v113, v106, v103, s72
	v_perm_b32 v102, v117, v116, s71
	v_perm_b32 v103, v111, v119, s71
	v_perm_b32 v104, v97, v98, s72
	v_perm_b32 v106, v117, v116, s72
	v_perm_b32 v110, v118, v107, s71
	v_perm_b32 v114, v118, v107, s72
	v_perm_b32 v107, v111, v119, s72
	v_perm_b32 v111, v121, v120, s71
	v_perm_b32 v115, v121, v120, s72
	global_store_dwordx4 v[128:129], v[100:103], off nt
	global_store_dwordx4 v[168:169], v[104:107], off nt
	global_store_dwordx4 v[202:203], v[108:111], off nt
	global_store_dwordx4 v[204:205], v[112:115], off nt
	s_cbranch_scc0 .LBB0_729
	s_mov_b64 s[4:5], 0

; template <int MODE> __device__ __forceinline__ int drow(int n) {
;     if (MODE == 1) { const int h = n / 192, nl = n - h * 192; return nl < 128 ? n : h * 192 + 128 + ((nl - 128) & 31) * 2 + ((nl - 128) >> 5); }
;     if (MODE == 2) { return n < FF ? ((n >> 7) * 256 + (n & 127)) : (((n - FF) >> 7) * 256 + 128 + ((n - FF) & 127)); }
; __device__ __forceinline__ void cv_load(const float* W, int N, int nblk, int item, int lane, f32x4 (&tv)[16]) {
;     const int kb = item / nblk, nb = item - kb * nblk; const float* p = W + (size_t)(64 * kb + 16 * (lane >> 4)) * N + 64 * nb + 4 * (lane & 15);
; #pragma unroll
;     for (int i = 0; i < 16; ++i) tv[i] = __builtin_nontemporal_load((const f32x4*)(p + (size_t)i * N));
; }
.LBB0_734:
	s_ashr_i32 s8, s10, 31
	s_lshr_b32 s8, s8, 26
	s_add_i32 s8, s10, s8
	s_ashr_i32 s13, s8, 6
	s_andn2_b32 s8, s8, 63
	v_or_b32_e32 v66, s8, v1
	v_ashrrev_i32_e32 v67, 31, v66
	s_lshl_b32 s8, s13, 12
	v_lshlrev_b64 v[2:3], 14, v[66:67]
	s_sub_i32 s8, s11, s8
	v_lshl_add_u64 v[2:3], s[4:5], 0, v[2:3]
	s_ashr_i32 s9, s8, 31
	v_lshl_add_u64 v[2:3], s[8:9], 2, v[2:3]
	v_lshlrev_b32_e32 v132, 2, v130
	v_lshl_add_u64 v[2:3], v[2:3], 0, v[132:133]
	v_add_co_u32_e32 v4, vcc, s1, v2
	s_mov_b32 s9, 0x20000
	s_nop 0
	v_addc_co_u32_e32 v5, vcc, 0, v3, vcc
	global_load_dwordx4 v[62:65], v[2:3], off nt
	global_load_dwordx4 v[58:61], v[4:5], off nt
	v_add_co_u32_e32 v4, vcc, s78, v2
	v_add_u32_e32 v72, s8, v130
	s_nop 0
	v_addc_co_u32_e32 v5, vcc, 0, v3, vcc
	v_add_co_u32_e32 v6, vcc, s79, v2
	v_add_u32_e32 v68, s12, v70
	s_nop 0
	v_addc_co_u32_e32 v7, vcc, 0, v3, vcc
	global_load_dwordx4 v[54:57], v[4:5], off nt
	global_load_dwordx4 v[50:53], v[6:7], off nt
	v_add_co_u32_e32 v4, vcc, s86, v2
	s_lshl_b32 s8, s13, 13
	s_nop 0
	v_addc_co_u32_e32 v5, vcc, 0, v3, vcc
	v_add_co_u32_e32 v6, vcc, s87, v2
	v_subrev_u32_e32 v71, s8, v68
	s_nop 0
	v_addc_co_u32_e32 v7, vcc, 0, v3, vcc
	global_load_dwordx4 v[46:49], v[4:5], off nt
	global_load_dwordx4 v[42:45], v[6:7], off nt
	v_add_co_u32_e32 v4, vcc, s85, v2
	s_nop 1
	v_addc_co_u32_e32 v5, vcc, 0, v3, vcc
	v_add_co_u32_e32 v6, vcc, s82, v2
	s_nop 1
	v_addc_co_u32_e32 v7, vcc, 0, v3, vcc
	global_load_dwordx4 v[38:41], v[4:5], off nt
	global_load_dwordx4 v[34:37], v[6:7], off nt
	v_add_co_u32_e32 v4, vcc, s9, v2
	s_mov_b32 s9, 0x24000
	s_nop 0
	v_addc_co_u32_e32 v5, vcc, 0, v3, vcc
	v_add_co_u32_e32 v6, vcc, s9, v2
	s_mov_b32 s9, 0x28000
	s_nop 0
	v_addc_co_u32_e32 v7, vcc, 0, v3, vcc
	global_load_dwordx4 v[30:33], v[4:5], off nt
	global_load_dwordx4 v[26:29], v[6:7], off nt
	v_add_co_u32_e32 v4, vcc, s9, v2
	s_mov_b32 s9, 0x2c000
	s_nop 0
	v_addc_co_u32_e32 v5, vcc, 0, v3, vcc
	v_add_co_u32_e32 v6, vcc, s9, v2
	s_mov_b32 s9, 0x30000
	s_nop 0
	v_addc_co_u32_e32 v7, vcc, 0, v3, vcc
	global_load_dwordx4 v[22:25], v[4:5], off nt
	global_load_dwordx4 v[18:21], v[6:7], off nt
	v_add_co_u32_e32 v4, vcc, s9, v2
	s_mov_b32 s9, 0x34000
	s_nop 0
	v_addc_co_u32_e32 v5, vcc, 0, v3, vcc
	v_add_co_u32_e32 v6, vcc, s9, v2
	s_nop 1
	v_addc_co_u32_e32 v7, vcc, 0, v3, vcc
	global_load_dwordx4 v[14:17], v[4:5], off nt
	global_load_dwordx4 v[10:13], v[6:7], off nt
	v_add_co_u32_e32 v4, vcc, 0x38000, v2
	s_nop 1
	v_addc_co_u32_e32 v5, vcc, 0, v3, vcc
	v_add_co_u32_e32 v2, vcc, 0x3c000, v2
	s_nop 1
	v_addc_co_u32_e32 v3, vcc, 0, v3, vcc
	global_load_dwordx4 v[6:9], v[4:5], off nt
	s_nop 0
	global_load_dwordx4 v[2:5], v[2:3], off nt
	s_addk_i32 s12, 0x80
	s_add_i32 s11, s11, 64
	s_add_i32 s10, s10, 1
	s_ashr_i32 s8, s10, 31
	s_lshr_b32 s8, s8, 26
	s_add_i32 s8, s10, s8
	s_ashr_i32 s13, s8, 6
	s_andn2_b32 s8, s8, 63
	v_or_b32_e32 v156, s8, v1
	v_ashrrev_i32_e32 v157, 31, v156
	s_lshl_b32 s8, s13, 12
	v_lshlrev_b64 v[78:79], 14, v[156:157]
	s_sub_i32 s8, s11, s8
	v_lshl_add_u64 v[78:79], s[4:5], 0, v[78:79]
	s_ashr_i32 s9, s8, 31
	v_lshl_add_u64 v[78:79], s[8:9], 2, v[78:79]
	v_lshlrev_b32_e32 v132, 2, v130
	v_lshl_add_u64 v[78:79], v[78:79], 0, v[132:133]
	v_add_co_u32_e32 v80, vcc, s1, v78
	s_mov_b32 s9, 0x20000
	s_nop 0
	v_addc_co_u32_e32 v81, vcc, 0, v79, vcc
	global_load_dwordx4 v[152:155], v[78:79], off nt
	global_load_dwordx4 v[140:143], v[80:81], off nt
	v_add_co_u32_e32 v80, vcc, s78, v78
	v_add_u32_e32 v160, s8, v130
	s_nop 0
	v_addc_co_u32_e32 v81, vcc, 0, v79, vcc
	v_add_co_u32_e32 v82, vcc, s79, v78
	v_add_u32_e32 v158, s12, v70
	s_nop 0
	v_addc_co_u32_e32 v83, vcc, 0, v79, vcc
	global_load_dwordx4 v[136:139], v[80:81], off nt
	global_load_dwordx4 v[126:129], v[82:83], off nt
	v_add_co_u32_e32 v80, vcc, s86, v78
	s_lshl_b32 s8, s13, 13
	s_nop 0
	v_addc_co_u32_e32 v81, vcc, 0, v79, vcc
	v_add_co_u32_e32 v82, vcc, s87, v78
	v_subrev_u32_e32 v73, s8, v158
	s_nop 0
	v_addc_co_u32_e32 v83, vcc, 0, v79, vcc
	global_load_dwordx4 v[122:125], v[80:81], off nt
	global_load_dwordx4 v[118:121], v[82:83], off nt
	v_add_co_u32_e32 v80, vcc, s85, v78
	s_nop 1
	v_addc_co_u32_e32 v81, vcc, 0, v79, vcc
	v_add_co_u32_e32 v82, vcc, s82, v78
	s_nop 1
	v_addc_co_u32_e32 v83, vcc, 0, v79, vcc
	global_load_dwordx4 v[114:117], v[80:81], off nt
	global_load_dwordx4 v[110:113], v[82:83], off nt
	v_add_co_u32_e32 v80, vcc, s9, v78
	s_mov_b32 s9, 0x24000
	s_nop 0
	v_addc_co_u32_e32 v81, vcc, 0, v79, vcc
	v_add_co_u32_e32 v82, vcc, s9, v78
	s_mov_b32 s9, 0x28000
	s_nop 0
	v_addc_co_u32_e32 v83, vcc, 0, v79, vcc
	global_load_dwordx4 v[106:109], v[80:81], off nt
	global_load_dwordx4 v[102:105], v[82:83], off nt
	v_add_co_u32_e32 v80, vcc, s9, v78
	s_mov_b32 s9, 0x2c000
	s_nop 0
	v_addc_co_u32_e32 v81, vcc, 0, v79, vcc
	v_add_co_u32_e32 v82, vcc, s9, v78
	s_mov_b32 s9, 0x30000
	s_nop 0
	v_addc_co_u32_e32 v83, vcc, 0, v79, vcc
	global_load_dwordx4 v[98:101], v[80:81], off nt
	global_load_dwordx4 v[94:97], v[82:83], off nt
	v_add_co_u32_e32 v80, vcc, s9, v78
	s_mov_b32 s9, 0x34000
	s_nop 0
	v_addc_co_u32_e32 v81, vcc, 0, v79, vcc
	v_add_co_u32_e32 v82, vcc, s9, v78
	s_nop 1
	v_addc_co_u32_e32 v83, vcc, 0, v79, vcc
	global_load_dwordx4 v[90:93], v[80:81], off nt
	global_load_dwordx4 v[86:89], v[82:83], off nt
	v_add_co_u32_e32 v80, vcc, 0x38000, v78
	s_nop 1
	v_addc_co_u32_e32 v81, vcc, 0, v79, vcc
	v_add_co_u32_e32 v78, vcc, 0x3c000, v78
	s_nop 1
	v_addc_co_u32_e32 v79, vcc, 0, v79, vcc
	global_load_dwordx4 v[82:85], v[80:81], off nt
	s_nop 0
	global_load_dwordx4 v[78:81], v[78:79], off nt
	s_addk_i32 s12, 0x80
	s_add_i32 s11, s11, 64
	s_add_i32 s10, s10, 1
	v_cmp_lt_i32_e32 vcc, s73, v72
	s_and_saveexec_b64 s[8:9], vcc
	s_xor_b64 s[8:9], exec, s[8:9]
	v_add_u32_e32 v68, 0x7ffff000, v71
	v_and_b32_e32 v68, 0x7fffff00, v68
	v_and_b32_e32 v69, 0x7c, v72
	v_or3_b32 v68, v69, v68, s83
	s_andn2_saveexec_b64 s[8:9], s[8:9]
	v_and_b32_e32 v68, 0x7c, v72
	v_and_or_b32 v68, v71, s0, v68
	s_or_b64 exec, exec, s[8:9]
	s_waitcnt vmcnt(31)
; template <int MODE> __device__ __forceinline__ void cv_finish(const f32x4 (&tv)[16], int K, int nblk, unsigned char* WT, int item, int lane) {
;     ...
;     for (int i = 0; i < 16; ++i) { const f32x2 a = (f32x2){tv[i].x, tv[i].y} * (f32x2){1024.f, 1024.f}, b = (f32x2){tv[i].z, tv[i].w} * (f32x2){1024.f, 1024.f};
;         D[i] = pk4_fp8(a.x, a.y, b.x, b.y); }
	v_pk_mul_f32 v[62:63], v[62:63], s[84:85] op_sel_hi:[1,0]
	v_pk_mul_f32 v[64:65], v[64:65], s[84:85] op_sel_hi:[1,0]
	v_med3_f32 v69, v62, s96, v150
	v_med3_f32 v63, v63, s96, v150
	v_mov_b32_e32 v62, v133
	v_cvt_pk_fp8_f32 v62, v69, v63
	v_med3_f32 v63, v64, s96, v150
	v_med3_f32 v64, v65, s96, v150
	s_waitcnt vmcnt(30)
	v_pk_mul_f32 v[58:59], v[58:59], s[84:85] op_sel_hi:[1,0]
	v_cvt_pk_fp8_f32 v62, v63, v64 op_sel:[0,0,1]
	v_med3_f32 v63, v58, s96, v150
	v_med3_f32 v59, v59, s96, v150
	v_mov_b32_e32 v58, v133
	v_cvt_pk_fp8_f32 v58, v63, v59
	v_pk_mul_f32 v[60:61], v[60:61], s[84:85] op_sel_hi:[1,0]
	s_waitcnt vmcnt(29)
	v_pk_mul_f32 v[54:55], v[54:55], s[84:85] op_sel_hi:[1,0]
	v_med3_f32 v59, v60, s96, v150
	v_med3_f32 v60, v61, s96, v150
	v_cvt_pk_fp8_f32 v58, v59, v60 op_sel:[0,0,1]
	v_med3_f32 v59, v54, s96, v150
	v_med3_f32 v55, v55, s96, v150
	v_mov_b32_e32 v54, v133
	v_cvt_pk_fp8_f32 v54, v59, v55
	v_pk_mul_f32 v[56:57], v[56:57], s[84:85] op_sel_hi:[1,0]
	s_waitcnt vmcnt(28)
	v_pk_mul_f32 v[50:51], v[50:51], s[84:85] op_sel_hi:[1,0]
	v_med3_f32 v55, v56, s96, v150
	v_med3_f32 v56, v57, s96, v150
	v_cvt_pk_fp8_f32 v54, v55, v56 op_sel:[0,0,1]
	v_med3_f32 v55, v50, s96, v150
	v_med3_f32 v51, v51, s96, v150
	v_mov_b32_e32 v50, v133
	v_cvt_pk_fp8_f32 v50, v55, v51
	v_pk_mul_f32 v[52:53], v[52:53], s[84:85] op_sel_hi:[1,0]
	s_waitcnt vmcnt(27)
	v_pk_mul_f32 v[46:47], v[46:47], s[84:85] op_sel_hi:[1,0]
	v_med3_f32 v51, v52, s96, v150
	v_med3_f32 v52, v53, s96, v150
	v_cvt_pk_fp8_f32 v50, v51, v52 op_sel:[0,0,1]
	v_med3_f32 v51, v46, s96, v150
	v_med3_f32 v47, v47, s96, v150
	v_mov_b32_e32 v46, v133
	v_cvt_pk_fp8_f32 v46, v51, v47
	v_pk_mul_f32 v[48:49], v[48:49], s[84:85] op_sel_hi:[1,0]
	s_waitcnt vmcnt(26)
	v_pk_mul_f32 v[42:43], v[42:43], s[84:85] op_sel_hi:[1,0]
	v_med3_f32 v47, v48, s96, v150
	v_med3_f32 v48, v49, s96, v150
	v_cvt_pk_fp8_f32 v46, v47, v48 op_sel:[0,0,1]
	v_med3_f32 v47, v42, s96, v150
	v_med3_f32 v43, v43, s96, v150
	v_mov_b32_e32 v42, v133
	v_cvt_pk_fp8_f32 v42, v47, v43
	v_pk_mul_f32 v[44:45], v[44:45], s[84:85] op_sel_hi:[1,0]
	s_waitcnt vmcnt(25)
	v_pk_mul_f32 v[38:39], v[38:39], s[84:85] op_sel_hi:[1,0]
	v_med3_f32 v43, v44, s96, v150
	v_med3_f32 v44, v45, s96, v150
	v_cvt_pk_fp8_f32 v42, v43, v44 op_sel:[0,0,1]
	v_med3_f32 v43, v38, s96, v150
	v_med3_f32 v39, v39, s96, v150
	v_mov_b32_e32 v38, v133
	v_cvt_pk_fp8_f32 v38, v43, v39
	v_pk_mul_f32 v[40:41], v[40:41], s[84:85] op_sel_hi:[1,0]
	s_waitcnt vmcnt(24)
	v_pk_mul_f32 v[34:35], v[34:35], s[84:85] op_sel_hi:[1,0]
	v_med3_f32 v39, v40, s96, v150
	v_med3_f32 v40, v41, s96, v150
	v_cvt_pk_fp8_f32 v38, v39, v40 op_sel:[0,0,1]
	v_med3_f32 v39, v34, s96, v150
	v_med3_f32 v35, v35, s96, v150
	v_mov_b32_e32 v34, v133
	v_cvt_pk_fp8_f32 v34, v39, v35
	v_pk_mul_f32 v[36:37], v[36:37], s[84:85] op_sel_hi:[1,0]
	s_waitcnt vmcnt(23)
	v_pk_mul_f32 v[30:31], v[30:31], s[84:85] op_sel_hi:[1,0]
	v_med3_f32 v35, v36, s96, v150
	v_med3_f32 v36, v37, s96, v150
	v_cvt_pk_fp8_f32 v34, v35, v36 op_sel:[0,0,1]
	v_med3_f32 v35, v30, s96, v150
	v_med3_f32 v31, v31, s96, v150
	v_mov_b32_e32 v30, v133
	v_cvt_pk_fp8_f32 v30, v35, v31
	v_pk_mul_f32 v[32:33], v[32:33], s[84:85] op_sel_hi:[1,0]
	s_waitcnt vmcnt(22)
	v_pk_mul_f32 v[26:27], v[26:27], s[84:85] op_sel_hi:[1,0]
	v_med3_f32 v31, v32, s96, v150
	v_med3_f32 v32, v33, s96, v150
	v_cvt_pk_fp8_f32 v30, v31, v32 op_sel:[0,0,1]
	v_med3_f32 v31, v26, s96, v150
	v_med3_f32 v27, v27, s96, v150
	v_mov_b32_e32 v26, v133
	v_cvt_pk_fp8_f32 v26, v31, v27
	v_pk_mul_f32 v[28:29], v[28:29], s[84:85] op_sel_hi:[1,0]
	s_waitcnt vmcnt(21)
	v_pk_mul_f32 v[22:23], v[22:23], s[84:85] op_sel_hi:[1,0]
	v_med3_f32 v27, v28, s96, v150
	v_med3_f32 v28, v29, s96, v150
	v_cvt_pk_fp8_f32 v26, v27, v28 op_sel:[0,0,1]
	v_med3_f32 v27, v22, s96, v150
	v_med3_f32 v23, v23, s96, v150
	v_mov_b32_e32 v22, v133
	v_cvt_pk_fp8_f32 v22, v27, v23
	v_pk_mul_f32 v[24:25], v[24:25], s[84:85] op_sel_hi:[1,0]
	s_waitcnt vmcnt(20)
	v_pk_mul_f32 v[18:19], v[18:19], s[84:85] op_sel_hi:[1,0]
	v_med3_f32 v23, v24, s96, v150
	v_med3_f32 v24, v25, s96, v150
	v_cvt_pk_fp8_f32 v22, v23, v24 op_sel:[0,0,1]
	v_med3_f32 v23, v18, s96, v150
	v_med3_f32 v19, v19, s96, v150
	v_mov_b32_e32 v18, v133
	v_cvt_pk_fp8_f32 v18, v23, v19
	v_pk_mul_f32 v[20:21], v[20:21], s[84:85] op_sel_hi:[1,0]
	s_waitcnt vmcnt(19)
	v_pk_mul_f32 v[14:15], v[14:15], s[84:85] op_sel_hi:[1,0]
	v_med3_f32 v19, v20, s96, v150
	v_med3_f32 v20, v21, s96, v150
	v_cvt_pk_fp8_f32 v18, v19, v20 op_sel:[0,0,1]
	v_med3_f32 v19, v14, s96, v150
	v_med3_f32 v15, v15, s96, v150
	v_mov_b32_e32 v14, v133
	v_cvt_pk_fp8_f32 v14, v19, v15
	v_pk_mul_f32 v[16:17], v[16:17], s[84:85] op_sel_hi:[1,0]
	s_waitcnt vmcnt(18)
	v_pk_mul_f32 v[10:11], v[10:11], s[84:85] op_sel_hi:[1,0]
	v_med3_f32 v15, v16, s96, v150
	v_med3_f32 v16, v17, s96, v150
	v_cvt_pk_fp8_f32 v14, v15, v16 op_sel:[0,0,1]
	v_med3_f32 v15, v10, s96, v150
	v_med3_f32 v11, v11, s96, v150
	v_mov_b32_e32 v10, v133
	v_cvt_pk_fp8_f32 v10, v15, v11
	v_pk_mul_f32 v[12:13], v[12:13], s[84:85] op_sel_hi:[1,0]
	s_waitcnt vmcnt(17)
	v_pk_mul_f32 v[6:7], v[6:7], s[84:85] op_sel_hi:[1,0]
	v_med3_f32 v11, v12, s96, v150
	v_med3_f32 v12, v13, s96, v150
	v_cvt_pk_fp8_f32 v10, v11, v12 op_sel:[0,0,1]
	v_med3_f32 v11, v6, s96, v150
	v_med3_f32 v7, v7, s96, v150
	v_mov_b32_e32 v6, v133
	v_cvt_pk_fp8_f32 v6, v11, v7
	v_pk_mul_f32 v[8:9], v[8:9], s[84:85] op_sel_hi:[1,0]
	s_waitcnt vmcnt(16)
; template <int MODE> __device__ __forceinline__ int drow(int n) {
;     if (MODE == 1) { const int h = n / 192, nl = n - h * 192; return nl < 128 ? n : h * 192 + 128 + ((nl - 128) & 31) * 2 + ((nl - 128) >> 5); }
;     if (MODE == 2) { return n < FF ? ((n >> 7) * 256 + (n & 127)) : (((n - FF) >> 7) * 256 + 128 + ((n - FF) & 127)); }
; template <int MODE> __device__ __forceinline__ void cv_finish(const f32x4 (&tv)[16], int K, int nblk, unsigned char* WT, int item, int lane) {
;     ...
;     unsigned O[4][4];
; #pragma unroll
;     for (int q = 0; q < 4; ++q) { const unsigned a = D[4 * q], b = D[4 * q + 1], c = D[4 * q + 2], d = D[4 * q + 3];
;         const unsigned t0 = __builtin_amdgcn_perm(b, a, 0x05010400u), t1 = __builtin_amdgcn_perm(b, a, 0x07030602u), u0 = __builtin_amdgcn_perm(d, c, 0x05010400u), u1 = __builtin_amdgcn_perm(d, c, 0x07030602u);
;         O[0][q] = __builtin_amdgcn_perm(u0, t0, 0x05040100u); O[1][q] = __builtin_amdgcn_perm(u0, t0, 0x07060302u); O[2][q] = __builtin_amdgcn_perm(u1, t1, 0x05040100u); O[3][q] = __builtin_amdgcn_perm(u1, t1, 0x07060302u); }
; #pragma unroll
;     for (int j = 0; j < 4; ++j) { u32x4 o; o.x = O[j][0]; o.y = O[j][1]; o.z = O[j][2]; o.w = O[j][3];
;         __builtin_nontemporal_store(o, (u32x4*)(WT + (size_t)drow<MODE>(n0 + j) * K + k0)); }
; }
	v_pk_mul_f32 v[2:3], v[2:3], s[84:85] op_sel_hi:[1,0]
	v_med3_f32 v7, v8, s96, v150
	v_med3_f32 v8, v9, s96, v150
	v_cvt_pk_fp8_f32 v6, v7, v8 op_sel:[0,0,1]
	v_med3_f32 v2, v2, s96, v150
	v_med3_f32 v3, v3, s96, v150
	v_mov_b32_e32 v7, v133
	v_cvt_pk_fp8_f32 v7, v2, v3
	v_pk_mul_f32 v[2:3], v[4:5], s[84:85] op_sel_hi:[1,0]
	v_ashrrev_i32_e32 v69, 31, v68
	v_med3_f32 v2, v2, s96, v150
	v_med3_f32 v3, v3, s96, v150
	v_cvt_pk_fp8_f32 v7, v2, v3 op_sel:[0,0,1]
	v_perm_b32 v5, v58, v62, s97
	v_perm_b32 v8, v50, v54, s97
	v_perm_b32 v9, v42, v46, s97
	v_perm_b32 v11, v34, v38, s97
	v_perm_b32 v12, v26, v30, s97
	v_perm_b32 v13, v18, v22, s97
	v_perm_b32 v15, v10, v14, s97
	v_perm_b32 v16, v7, v6, s97
	v_lshl_add_u64 v[2:3], s[6:7], 0, v[66:67]
	v_lshlrev_b64 v[20:21], 11, v[68:69]
	v_add_u32_e32 v17, 1, v72
	v_perm_b32 v74, v8, v5, s71
	v_perm_b32 v75, v11, v9, s71
	v_perm_b32 v76, v13, v12, s71
	v_perm_b32 v77, v16, v15, s71
	v_lshl_add_u64 v[20:21], v[2:3], 0, v[20:21]
	v_cmp_lt_i32_e32 vcc, s73, v17
	global_store_dwordx4 v[20:21], v[74:77], off nt
	s_and_saveexec_b64 s[8:9], vcc
	s_xor_b64 s[8:9], exec, s[8:9]
	v_add_u32_e32 v4, 0x7ffff002, v71
	v_and_b32_e32 v4, 0x7fffff00, v4
	v_and_b32_e32 v17, 0x7d, v17
	v_or3_b32 v4, v17, v4, s83
	s_andn2_saveexec_b64 s[8:9], s[8:9]
	v_add_u32_e32 v4, 2, v71
	v_and_b32_e32 v17, 0x7d, v17
	v_and_or_b32 v4, v4, s0, v17
	s_or_b64 exec, exec, s[8:9]
	v_perm_b32 v64, v8, v5, s72
	v_ashrrev_i32_e32 v5, 31, v4
	v_lshlrev_b64 v[4:5], 11, v[4:5]
	v_perm_b32 v65, v11, v9, s72
	v_perm_b32 v66, v13, v12, s72
	v_perm_b32 v67, v16, v15, s72
	v_lshl_add_u64 v[4:5], v[2:3], 0, v[4:5]
	global_store_dwordx4 v[4:5], v[64:67], off nt
	v_add_u32_e32 v5, 2, v72
	v_cmp_lt_i32_e32 vcc, s73, v5
	s_and_saveexec_b64 s[8:9], vcc
	s_xor_b64 s[8:9], exec, s[8:9]
	v_add_u32_e32 v4, 0x7ffff004, v71
	v_and_b32_e32 v4, 0x7fffff00, v4
	v_and_b32_e32 v5, 0x7e, v5
	v_or3_b32 v4, v5, v4, s83
	s_andn2_saveexec_b64 s[8:9], s[8:9]
	v_add_u32_e32 v4, 4, v71
	v_and_b32_e32 v5, 0x7e, v5
	v_and_or_b32 v4, v4, s0, v5
	s_or_b64 exec, exec, s[8:9]
	v_ashrrev_i32_e32 v5, 31, v4
	v_perm_b32 v8, v58, v62, s70
	v_perm_b32 v9, v50, v54, s70
	v_perm_b32 v11, v42, v46, s70
	v_perm_b32 v12, v34, v38, s70
	v_perm_b32 v13, v26, v30, s70
	v_perm_b32 v15, v18, v22, s70
	v_perm_b32 v10, v10, v14, s70
	v_perm_b32 v6, v7, v6, s70
	v_lshlrev_b64 v[4:5], 11, v[4:5]
	v_perm_b32 v16, v9, v8, s71
	v_perm_b32 v17, v12, v11, s71
	v_perm_b32 v18, v15, v13, s71
	v_perm_b32 v19, v6, v10, s71
	v_lshl_add_u64 v[4:5], v[2:3], 0, v[4:5]
	global_store_dwordx4 v[4:5], v[16:19], off nt
	v_add_u32_e32 v5, 3, v72
	v_cmp_lt_i32_e32 vcc, s73, v5
	s_and_saveexec_b64 s[8:9], vcc
	s_xor_b64 s[8:9], exec, s[8:9]
	v_add_u32_e32 v4, 0x7ffff006, v71
	v_and_b32_e32 v4, 0x7fffff00, v4
	v_and_b32_e32 v5, 0x7f, v5
	v_or3_b32 v4, v5, v4, s83
	s_andn2_saveexec_b64 s[8:9], s[8:9]
	v_add_u32_e32 v4, 6, v71
	v_and_b32_e32 v5, 0x7f, v5
	v_and_or_b32 v4, v4, s0, v5
	s_or_b64 exec, exec, s[8:9]
	v_ashrrev_i32_e32 v5, 31, v4
	v_lshlrev_b64 v[4:5], 11, v[4:5]
	v_perm_b32 v16, v9, v8, s72
	v_perm_b32 v17, v12, v11, s72
	v_perm_b32 v18, v15, v13, s72
	v_perm_b32 v19, v6, v10, s72
	v_lshl_add_u64 v[2:3], v[2:3], 0, v[4:5]
	global_store_dwordx4 v[2:3], v[16:19], off nt
	v_cmp_lt_i32_e32 vcc, s73, v160
	s_and_saveexec_b64 s[8:9], vcc
	s_xor_b64 s[8:9], exec, s[8:9]
	v_add_u32_e32 v158, 0x7ffff000, v73
	v_and_b32_e32 v158, 0x7fffff00, v158
	v_and_b32_e32 v159, 0x7c, v160
	v_or3_b32 v158, v159, v158, s83
	s_andn2_saveexec_b64 s[8:9], s[8:9]
	v_and_b32_e32 v158, 0x7c, v160
	v_and_or_b32 v158, v73, s0, v158
	s_or_b64 exec, exec, s[8:9]
	s_waitcnt vmcnt(19)
	v_pk_mul_f32 v[152:153], v[152:153], s[84:85] op_sel_hi:[1,0]
	v_pk_mul_f32 v[154:155], v[154:155], s[84:85] op_sel_hi:[1,0]
	v_med3_f32 v159, v152, s96, v150
	v_med3_f32 v153, v153, s96, v150
	v_mov_b32_e32 v152, v133
	v_cvt_pk_fp8_f32 v152, v159, v153
	v_med3_f32 v153, v154, s96, v150
	v_med3_f32 v154, v155, s96, v150
	s_waitcnt vmcnt(18)
	v_pk_mul_f32 v[140:141], v[140:141], s[84:85] op_sel_hi:[1,0]
	v_cvt_pk_fp8_f32 v152, v153, v154 op_sel:[0,0,1]
	v_med3_f32 v153, v140, s96, v150
	v_med3_f32 v141, v141, s96, v150
	v_mov_b32_e32 v140, v133
	v_cvt_pk_fp8_f32 v140, v153, v141
	v_pk_mul_f32 v[142:143], v[142:143], s[84:85] op_sel_hi:[1,0]
	s_waitcnt vmcnt(17)
	v_pk_mul_f32 v[136:137], v[136:137], s[84:85] op_sel_hi:[1,0]
	v_med3_f32 v141, v142, s96, v150
	v_med3_f32 v142, v143, s96, v150
	v_cvt_pk_fp8_f32 v140, v141, v142 op_sel:[0,0,1]
	v_med3_f32 v141, v136, s96, v150
	v_med3_f32 v137, v137, s96, v150
	v_mov_b32_e32 v136, v133
	v_cvt_pk_fp8_f32 v136, v141, v137
	v_pk_mul_f32 v[138:139], v[138:139], s[84:85] op_sel_hi:[1,0]
	s_waitcnt vmcnt(16)
	v_pk_mul_f32 v[126:127], v[126:127], s[84:85] op_sel_hi:[1,0]
	v_med3_f32 v137, v138, s96, v150
	v_med3_f32 v138, v139, s96, v150
	v_cvt_pk_fp8_f32 v136, v137, v138 op_sel:[0,0,1]
	v_med3_f32 v137, v126, s96, v150
	v_med3_f32 v127, v127, s96, v150
	v_mov_b32_e32 v126, v133
	v_cvt_pk_fp8_f32 v126, v137, v127
	v_pk_mul_f32 v[128:129], v[128:129], s[84:85] op_sel_hi:[1,0]
	s_waitcnt vmcnt(15)
	v_pk_mul_f32 v[122:123], v[122:123], s[84:85] op_sel_hi:[1,0]
	v_med3_f32 v127, v128, s96, v150
	v_med3_f32 v128, v129, s96, v150
	v_cvt_pk_fp8_f32 v126, v127, v128 op_sel:[0,0,1]
	v_med3_f32 v127, v122, s96, v150
	v_med3_f32 v123, v123, s96, v150
	v_mov_b32_e32 v122, v133
	v_cvt_pk_fp8_f32 v122, v127, v123
	v_pk_mul_f32 v[124:125], v[124:125], s[84:85] op_sel_hi:[1,0]
	s_waitcnt vmcnt(14)
; template <int MODE> __device__ __forceinline__ void cv_finish(const f32x4 (&tv)[16], int K, int nblk, unsigned char* WT, int item, int lane) {
;     ...
;     for (int i = 0; i < 16; ++i) { const f32x2 a = (f32x2){tv[i].x, tv[i].y} * (f32x2){1024.f, 1024.f}, b = (f32x2){tv[i].z, tv[i].w} * (f32x2){1024.f, 1024.f};
;         D[i] = pk4_fp8(a.x, a.y, b.x, b.y); }
	v_pk_mul_f32 v[118:119], v[118:119], s[84:85] op_sel_hi:[1,0]
	v_med3_f32 v123, v124, s96, v150
	v_med3_f32 v124, v125, s96, v150
	v_cvt_pk_fp8_f32 v122, v123, v124 op_sel:[0,0,1]
	v_med3_f32 v123, v118, s96, v150
	v_med3_f32 v119, v119, s96, v150
	v_mov_b32_e32 v118, v133
	v_cvt_pk_fp8_f32 v118, v123, v119
	v_pk_mul_f32 v[120:121], v[120:121], s[84:85] op_sel_hi:[1,0]
	s_waitcnt vmcnt(13)
	v_pk_mul_f32 v[114:115], v[114:115], s[84:85] op_sel_hi:[1,0]
	v_med3_f32 v119, v120, s96, v150
	v_med3_f32 v120, v121, s96, v150
	v_cvt_pk_fp8_f32 v118, v119, v120 op_sel:[0,0,1]
	v_med3_f32 v119, v114, s96, v150
	v_med3_f32 v115, v115, s96, v150
	v_mov_b32_e32 v114, v133
	v_cvt_pk_fp8_f32 v114, v119, v115
	v_pk_mul_f32 v[116:117], v[116:117], s[84:85] op_sel_hi:[1,0]
	s_waitcnt vmcnt(12)
	v_pk_mul_f32 v[110:111], v[110:111], s[84:85] op_sel_hi:[1,0]
	v_med3_f32 v115, v116, s96, v150
	v_med3_f32 v116, v117, s96, v150
	v_cvt_pk_fp8_f32 v114, v115, v116 op_sel:[0,0,1]
	v_med3_f32 v115, v110, s96, v150
	v_med3_f32 v111, v111, s96, v150
	v_mov_b32_e32 v110, v133
	v_cvt_pk_fp8_f32 v110, v115, v111
	v_pk_mul_f32 v[112:113], v[112:113], s[84:85] op_sel_hi:[1,0]
	s_waitcnt vmcnt(11)
	v_pk_mul_f32 v[106:107], v[106:107], s[84:85] op_sel_hi:[1,0]
	v_med3_f32 v111, v112, s96, v150
	v_med3_f32 v112, v113, s96, v150
	v_cvt_pk_fp8_f32 v110, v111, v112 op_sel:[0,0,1]
	v_med3_f32 v111, v106, s96, v150
	v_med3_f32 v107, v107, s96, v150
	v_mov_b32_e32 v106, v133
	v_cvt_pk_fp8_f32 v106, v111, v107
	v_pk_mul_f32 v[108:109], v[108:109], s[84:85] op_sel_hi:[1,0]
	s_waitcnt vmcnt(10)
	v_pk_mul_f32 v[102:103], v[102:103], s[84:85] op_sel_hi:[1,0]
	v_med3_f32 v107, v108, s96, v150
	v_med3_f32 v108, v109, s96, v150
	v_cvt_pk_fp8_f32 v106, v107, v108 op_sel:[0,0,1]
	v_med3_f32 v107, v102, s96, v150
	v_med3_f32 v103, v103, s96, v150
	v_mov_b32_e32 v102, v133
	v_cvt_pk_fp8_f32 v102, v107, v103
	v_pk_mul_f32 v[104:105], v[104:105], s[84:85] op_sel_hi:[1,0]
	s_waitcnt vmcnt(9)
	v_pk_mul_f32 v[98:99], v[98:99], s[84:85] op_sel_hi:[1,0]
	v_med3_f32 v103, v104, s96, v150
	v_med3_f32 v104, v105, s96, v150
	v_cvt_pk_fp8_f32 v102, v103, v104 op_sel:[0,0,1]
	v_med3_f32 v103, v98, s96, v150
	v_med3_f32 v99, v99, s96, v150
	v_mov_b32_e32 v98, v133
	v_cvt_pk_fp8_f32 v98, v103, v99
	v_pk_mul_f32 v[100:101], v[100:101], s[84:85] op_sel_hi:[1,0]
	s_waitcnt vmcnt(8)
	v_pk_mul_f32 v[94:95], v[94:95], s[84:85] op_sel_hi:[1,0]
	v_med3_f32 v99, v100, s96, v150
	v_med3_f32 v100, v101, s96, v150
	v_cvt_pk_fp8_f32 v98, v99, v100 op_sel:[0,0,1]
	v_med3_f32 v99, v94, s96, v150
	v_med3_f32 v95, v95, s96, v150
	v_mov_b32_e32 v94, v133
	v_cvt_pk_fp8_f32 v94, v99, v95
	v_pk_mul_f32 v[96:97], v[96:97], s[84:85] op_sel_hi:[1,0]
	s_waitcnt vmcnt(7)
	v_pk_mul_f32 v[90:91], v[90:91], s[84:85] op_sel_hi:[1,0]
	v_med3_f32 v95, v96, s96, v150
	v_med3_f32 v96, v97, s96, v150
	v_cvt_pk_fp8_f32 v94, v95, v96 op_sel:[0,0,1]
	v_med3_f32 v95, v90, s96, v150
	v_med3_f32 v91, v91, s96, v150
	v_mov_b32_e32 v90, v133
	v_cvt_pk_fp8_f32 v90, v95, v91
	v_pk_mul_f32 v[92:93], v[92:93], s[84:85] op_sel_hi:[1,0]
	s_waitcnt vmcnt(6)
	v_pk_mul_f32 v[86:87], v[86:87], s[84:85] op_sel_hi:[1,0]
	v_med3_f32 v91, v92, s96, v150
	v_med3_f32 v92, v93, s96, v150
	v_cvt_pk_fp8_f32 v90, v91, v92 op_sel:[0,0,1]
	v_med3_f32 v91, v86, s96, v150
	v_med3_f32 v87, v87, s96, v150
	v_mov_b32_e32 v86, v133
	v_cvt_pk_fp8_f32 v86, v91, v87
	v_pk_mul_f32 v[88:89], v[88:89], s[84:85] op_sel_hi:[1,0]
	s_waitcnt vmcnt(5)
	v_pk_mul_f32 v[82:83], v[82:83], s[84:85] op_sel_hi:[1,0]
	v_med3_f32 v87, v88, s96, v150
	v_med3_f32 v88, v89, s96, v150
	v_cvt_pk_fp8_f32 v86, v87, v88 op_sel:[0,0,1]
	v_med3_f32 v87, v82, s96, v150
	v_med3_f32 v83, v83, s96, v150
	v_mov_b32_e32 v82, v133
	v_cvt_pk_fp8_f32 v82, v87, v83
	v_pk_mul_f32 v[84:85], v[84:85], s[84:85] op_sel_hi:[1,0]
	s_waitcnt vmcnt(4)
; template <int MODE> __device__ __forceinline__ int drow(int n) {
;     if (MODE == 1) { const int h = n / 192, nl = n - h * 192; return nl < 128 ? n : h * 192 + 128 + ((nl - 128) & 31) * 2 + ((nl - 128) >> 5); }
;     if (MODE == 2) { return n < FF ? ((n >> 7) * 256 + (n & 127)) : (((n - FF) >> 7) * 256 + 128 + ((n - FF) & 127)); }
; template <int MODE> __device__ __forceinline__ void cv_finish(const f32x4 (&tv)[16], int K, int nblk, unsigned char* WT, int item, int lane) {
;     ...
;     unsigned O[4][4];
; #pragma unroll
;     for (int q = 0; q < 4; ++q) { const unsigned a = D[4 * q], b = D[4 * q + 1], c = D[4 * q + 2], d = D[4 * q + 3];
;         const unsigned t0 = __builtin_amdgcn_perm(b, a, 0x05010400u), t1 = __builtin_amdgcn_perm(b, a, 0x07030602u), u0 = __builtin_amdgcn_perm(d, c, 0x05010400u), u1 = __builtin_amdgcn_perm(d, c, 0x07030602u);
;         O[0][q] = __builtin_amdgcn_perm(u0, t0, 0x05040100u); O[1][q] = __builtin_amdgcn_perm(u0, t0, 0x07060302u); O[2][q] = __builtin_amdgcn_perm(u1, t1, 0x05040100u); O[3][q] = __builtin_amdgcn_perm(u1, t1, 0x07060302u); }
; #pragma unroll
;     for (int j = 0; j < 4; ++j) { u32x4 o; o.x = O[j][0]; o.y = O[j][1]; o.z = O[j][2]; o.w = O[j][3];
;         __builtin_nontemporal_store(o, (u32x4*)(WT + (size_t)drow<MODE>(n0 + j) * K + k0)); }
; }
	v_pk_mul_f32 v[78:79], v[78:79], s[84:85] op_sel_hi:[1,0]
	v_med3_f32 v83, v84, s96, v150
	v_med3_f32 v84, v85, s96, v150
	v_cvt_pk_fp8_f32 v82, v83, v84 op_sel:[0,0,1]
	v_med3_f32 v78, v78, s96, v150
	v_med3_f32 v79, v79, s96, v150
	v_mov_b32_e32 v83, v133
	v_cvt_pk_fp8_f32 v83, v78, v79
	v_pk_mul_f32 v[78:79], v[80:81], s[84:85] op_sel_hi:[1,0]
	v_ashrrev_i32_e32 v159, 31, v158
	v_med3_f32 v78, v78, s96, v150
	v_med3_f32 v79, v79, s96, v150
	v_cvt_pk_fp8_f32 v83, v78, v79 op_sel:[0,0,1]
	v_perm_b32 v81, v140, v152, s97
	v_perm_b32 v84, v126, v136, s97
	v_perm_b32 v85, v118, v122, s97
	v_perm_b32 v87, v110, v114, s97
	v_perm_b32 v88, v102, v106, s97
	v_perm_b32 v89, v94, v98, s97
	v_perm_b32 v91, v86, v90, s97
	v_perm_b32 v92, v83, v82, s97
	v_lshl_add_u64 v[78:79], s[6:7], 0, v[156:157]
	v_lshlrev_b64 v[96:97], 11, v[158:159]
	v_add_u32_e32 v93, 1, v160
	v_perm_b32 v162, v84, v81, s71
	v_perm_b32 v163, v87, v85, s71
	v_perm_b32 v164, v89, v88, s71
	v_perm_b32 v165, v92, v91, s71
	v_lshl_add_u64 v[96:97], v[78:79], 0, v[96:97]
	v_cmp_lt_i32_e32 vcc, s73, v93
	global_store_dwordx4 v[96:97], v[162:165], off nt
	s_and_saveexec_b64 s[8:9], vcc
	s_xor_b64 s[8:9], exec, s[8:9]
	v_add_u32_e32 v80, 0x7ffff002, v73
	v_and_b32_e32 v80, 0x7fffff00, v80
	v_and_b32_e32 v93, 0x7d, v93
	v_or3_b32 v80, v93, v80, s83
	s_andn2_saveexec_b64 s[8:9], s[8:9]
	v_add_u32_e32 v80, 2, v73
	v_and_b32_e32 v93, 0x7d, v93
	v_and_or_b32 v80, v80, s0, v93
	s_or_b64 exec, exec, s[8:9]
	v_perm_b32 v154, v84, v81, s72
	v_ashrrev_i32_e32 v81, 31, v80
	v_lshlrev_b64 v[80:81], 11, v[80:81]
	v_perm_b32 v155, v87, v85, s72
	v_perm_b32 v156, v89, v88, s72
	v_perm_b32 v157, v92, v91, s72
	v_lshl_add_u64 v[80:81], v[78:79], 0, v[80:81]
	global_store_dwordx4 v[80:81], v[154:157], off nt
	v_add_u32_e32 v81, 2, v160
	v_cmp_lt_i32_e32 vcc, s73, v81
	s_and_saveexec_b64 s[8:9], vcc
	s_xor_b64 s[8:9], exec, s[8:9]
	v_add_u32_e32 v80, 0x7ffff004, v73
	v_and_b32_e32 v80, 0x7fffff00, v80
	v_and_b32_e32 v81, 0x7e, v81
	v_or3_b32 v80, v81, v80, s83
	s_andn2_saveexec_b64 s[8:9], s[8:9]
	v_add_u32_e32 v80, 4, v73
	v_and_b32_e32 v81, 0x7e, v81
	v_and_or_b32 v80, v80, s0, v81
	s_or_b64 exec, exec, s[8:9]
	v_ashrrev_i32_e32 v81, 31, v80
	v_perm_b32 v84, v140, v152, s70
	v_perm_b32 v85, v126, v136, s70
	v_perm_b32 v87, v118, v122, s70
	v_perm_b32 v88, v110, v114, s70
	v_perm_b32 v89, v102, v106, s70
	v_perm_b32 v91, v94, v98, s70
	v_perm_b32 v86, v86, v90, s70
	v_perm_b32 v82, v83, v82, s70
	v_lshlrev_b64 v[80:81], 11, v[80:81]
	v_perm_b32 v92, v85, v84, s71
	v_perm_b32 v93, v88, v87, s71
	v_perm_b32 v94, v91, v89, s71
	v_perm_b32 v95, v82, v86, s71
	v_lshl_add_u64 v[80:81], v[78:79], 0, v[80:81]
	global_store_dwordx4 v[80:81], v[92:95], off nt
	v_add_u32_e32 v81, 3, v160
	v_cmp_lt_i32_e32 vcc, s73, v81
	s_and_saveexec_b64 s[8:9], vcc
	s_xor_b64 s[8:9], exec, s[8:9]
	v_add_u32_e32 v80, 0x7ffff006, v73
	v_and_b32_e32 v80, 0x7fffff00, v80
	v_and_b32_e32 v81, 0x7f, v81
	v_or3_b32 v80, v81, v80, s83
	s_andn2_saveexec_b64 s[8:9], s[8:9]
	v_add_u32_e32 v80, 6, v73
	v_and_b32_e32 v81, 0x7f, v81
	v_and_or_b32 v80, v80, s0, v81
	s_or_b64 exec, exec, s[8:9]
	v_ashrrev_i32_e32 v81, 31, v80
	v_lshlrev_b64 v[80:81], 11, v[80:81]
	v_perm_b32 v92, v85, v84, s72
	v_perm_b32 v93, v88, v87, s72
	v_perm_b32 v94, v91, v89, s72
	v_perm_b32 v95, v82, v86, s72
	v_lshl_add_u64 v[78:79], v[78:79], 0, v[80:81]
	global_store_dwordx4 v[78:79], v[92:95], off nt
	s_cmpk_eq_i32 s12, 0x200
	s_cbranch_scc0 .LBB0_734
	s_branch .LBB0_719

; __device__ __forceinline__ void cv_load(const float* W, int N, int nblk, int item, int lane, f32x4 (&tv)[16]) {
;     const int kb = item / nblk, nb = item - kb * nblk; const float* p = W + (size_t)(64 * kb + 16 * (lane >> 4)) * N + 64 * nb + 4 * (lane & 15);
; #pragma unroll
;     for (int i = 0; i < 16; ++i) tv[i] = __builtin_nontemporal_load((const f32x4*)(p + (size_t)i * N));
; }
; template <int MODE> __device__ __forceinline__ void cv_run4(const float* W, int K, int N, unsigned char* WT, int item0, int lane) {
;     const int nblk = N / 64; f32x4 ta[16];
; #pragma unroll 1
;     for (int j = 0; j < 4; ++j) { cv_load(W, N, nblk, item0 + j, lane, ta); cv_finish<MODE>(ta, K, nblk, WT, item0 + j, lane); }
.LBB0_761:
	s_lshr_b32 s41, s2, 5
	s_lshl_b32 s42, s41, 11
	v_mov_b32_e32 v3, v67
	v_lshl_or_b32 v2, s41, 6, v1
	s_sub_i32 s41, s39, s42
	v_subrev_u32_e32 v8, s42, v4
	v_lshlrev_b64 v[6:7], 13, v[2:3]
	s_add_i32 s42, s40, s41
	v_lshl_add_u64 v[6:7], s[6:7], 0, v[6:7]
	s_ashr_i32 s43, s42, 31
	v_lshl_add_u64 v[6:7], s[42:43], 2, v[6:7]
	v_lshl_add_u64 v[16:17], v[6:7], 0, v[66:67]
	v_add_co_u32_e32 v18, vcc, s0, v16
	v_add_u32_e32 v8, s40, v8
	s_nop 0
	v_addc_co_u32_e32 v19, vcc, 0, v17, vcc
	v_add_co_u32_e32 v20, vcc, s1, v16
	v_ashrrev_i32_e32 v9, 31, v8
	s_nop 0
	v_addc_co_u32_e32 v21, vcc, 0, v17, vcc
	v_add_co_u32_e32 v22, vcc, s5, v16
	v_add_u32_e32 v10, 1, v8
	s_nop 0
	v_addc_co_u32_e32 v23, vcc, 0, v17, vcc
	v_add_co_u32_e32 v24, vcc, s12, v16
	v_add_u32_e32 v12, 2, v8
	s_nop 0
	v_addc_co_u32_e32 v25, vcc, 0, v17, vcc
	v_add_co_u32_e32 v26, vcc, s13, v16
	v_add_u32_e32 v14, 3, v8
	s_nop 0
	v_addc_co_u32_e32 v27, vcc, 0, v17, vcc
	v_add_co_u32_e32 v30, vcc, s14, v16
	v_lshl_add_u64 v[2:3], s[8:9], 0, v[2:3]
	s_nop 0
	v_addc_co_u32_e32 v31, vcc, 0, v17, vcc
	v_add_co_u32_e32 v34, vcc, s15, v16
	v_lshlrev_b64 v[8:9], 11, v[8:9]
	s_nop 0
	v_addc_co_u32_e32 v35, vcc, 0, v17, vcc
	v_add_co_u32_e32 v38, vcc, s16, v16
	v_ashrrev_i32_e32 v11, 31, v10
	s_nop 0
	v_addc_co_u32_e32 v39, vcc, 0, v17, vcc
	v_add_co_u32_e32 v42, vcc, s17, v16
	v_ashrrev_i32_e32 v13, 31, v12
	s_nop 0
	v_addc_co_u32_e32 v43, vcc, 0, v17, vcc
	v_add_co_u32_e32 v46, vcc, s18, v16
	v_ashrrev_i32_e32 v15, 31, v14
	s_nop 0
	v_addc_co_u32_e32 v47, vcc, 0, v17, vcc
	v_add_co_u32_e32 v50, vcc, s19, v16
	v_lshl_add_u64 v[74:75], v[2:3], 0, v[8:9]
	s_nop 0
	v_addc_co_u32_e32 v51, vcc, 0, v17, vcc
	v_add_co_u32_e32 v54, vcc, s20, v16
	v_lshlrev_b64 v[10:11], 11, v[10:11]
	s_nop 0
	v_addc_co_u32_e32 v55, vcc, 0, v17, vcc
	v_add_co_u32_e32 v58, vcc, s21, v16
	v_lshlrev_b64 v[12:13], 11, v[12:13]
	s_nop 0
	v_addc_co_u32_e32 v59, vcc, 0, v17, vcc
	v_add_co_u32_e32 v62, vcc, s22, v16
	v_lshlrev_b64 v[14:15], 11, v[14:15]
	s_nop 0
	v_addc_co_u32_e32 v63, vcc, 0, v17, vcc
	v_add_co_u32_e32 v68, vcc, s23, v16
	global_load_dwordx4 v[6:9], v[16:17], off nt
	s_nop 0
	v_addc_co_u32_e32 v69, vcc, 0, v17, vcc
	v_lshl_add_u64 v[76:77], v[2:3], 0, v[10:11]
	v_lshl_add_u64 v[78:79], v[2:3], 0, v[12:13]
	v_lshl_add_u64 v[2:3], v[2:3], 0, v[14:15]
	global_load_dwordx4 v[10:13], v[18:19], off nt
	global_load_dwordx4 v[14:17], v[20:21], off nt
	s_nop 0
	global_load_dwordx4 v[18:21], v[22:23], off nt
	s_nop 0
	global_load_dwordx4 v[22:25], v[24:25], off nt
	s_nop 0
	global_load_dwordx4 v[26:29], v[26:27], off nt
	s_nop 0
	global_load_dwordx4 v[30:33], v[30:31], off nt
	s_nop 0
	global_load_dwordx4 v[34:37], v[34:35], off nt
	s_nop 0
	global_load_dwordx4 v[38:41], v[38:39], off nt
	s_nop 0
	global_load_dwordx4 v[42:45], v[42:43], off nt
	s_nop 0
	global_load_dwordx4 v[46:49], v[46:47], off nt
	s_nop 0
	global_load_dwordx4 v[50:53], v[50:51], off nt
	s_nop 0
	global_load_dwordx4 v[54:57], v[54:55], off nt
	s_nop 0
	global_load_dwordx4 v[58:61], v[58:59], off nt
	s_nop 0
	global_load_dwordx4 v[62:65], v[62:63], off nt
	s_nop 0
	global_load_dwordx4 v[68:71], v[68:69], off nt
	v_mov_b32_e32 v5, v67
	v_mov_b32_e32 v73, v67
	v_mov_b32_e32 v80, v67
	v_mov_b32_e32 v81, v67
	v_mov_b32_e32 v82, v67
	v_mov_b32_e32 v83, v67
	v_mov_b32_e32 v84, v67
	v_mov_b32_e32 v85, v67
	v_mov_b32_e32 v86, v67
	v_mov_b32_e32 v87, v67
	v_mov_b32_e32 v88, v67
	v_mov_b32_e32 v89, v67
	v_mov_b32_e32 v90, v67
	v_mov_b32_e32 v91, v67
	v_mov_b32_e32 v92, v67
	v_mov_b32_e32 v93, v67
	s_add_i32 s2, s2, 1
	s_add_i32 s40, s40, 64
	s_lshr_b32 s41, s2, 5
	s_lshl_b32 s42, s41, 11
	v_mov_b32_e32 v99, v67
	v_lshl_or_b32 v98, s41, 6, v1
	s_sub_i32 s41, s39, s42
	v_subrev_u32_e32 v104, s42, v4
	v_lshlrev_b64 v[102:103], 13, v[98:99]
	s_add_i32 s42, s40, s41
	v_lshl_add_u64 v[102:103], s[6:7], 0, v[102:103]
	s_ashr_i32 s43, s42, 31
	v_lshl_add_u64 v[102:103], s[42:43], 2, v[102:103]
	v_lshl_add_u64 v[112:113], v[102:103], 0, v[66:67]
	v_add_co_u32_e32 v114, vcc, s0, v112
	v_add_u32_e32 v104, s40, v104
	s_nop 0
	v_addc_co_u32_e32 v115, vcc, 0, v113, vcc
	v_add_co_u32_e32 v116, vcc, s1, v112
	v_ashrrev_i32_e32 v105, 31, v104
	s_nop 0
	v_addc_co_u32_e32 v117, vcc, 0, v113, vcc
	v_add_co_u32_e32 v118, vcc, s5, v112
	v_add_u32_e32 v106, 1, v104
	s_nop 0
	v_addc_co_u32_e32 v119, vcc, 0, v113, vcc
	v_add_co_u32_e32 v120, vcc, s12, v112
	v_add_u32_e32 v108, 2, v104
	s_nop 0
	v_addc_co_u32_e32 v121, vcc, 0, v113, vcc
	v_add_co_u32_e32 v122, vcc, s13, v112
	v_add_u32_e32 v110, 3, v104
	s_nop 0
	v_addc_co_u32_e32 v123, vcc, 0, v113, vcc
	v_add_co_u32_e32 v126, vcc, s14, v112
	v_lshl_add_u64 v[98:99], s[8:9], 0, v[98:99]
	s_nop 0
	v_addc_co_u32_e32 v127, vcc, 0, v113, vcc
	v_add_co_u32_e32 v132, vcc, s15, v112
	v_lshlrev_b64 v[104:105], 11, v[104:105]
	s_nop 0
	v_addc_co_u32_e32 v133, vcc, 0, v113, vcc
	v_add_co_u32_e32 v136, vcc, s16, v112
	v_ashrrev_i32_e32 v107, 31, v106
	s_nop 0
	v_addc_co_u32_e32 v137, vcc, 0, v113, vcc
	v_add_co_u32_e32 v140, vcc, s17, v112
	v_ashrrev_i32_e32 v109, 31, v108
	s_nop 0
	v_addc_co_u32_e32 v141, vcc, 0, v113, vcc
	v_add_co_u32_e32 v144, vcc, s18, v112
	v_ashrrev_i32_e32 v111, 31, v110
	s_nop 0
	v_addc_co_u32_e32 v145, vcc, 0, v113, vcc
	v_add_co_u32_e32 v148, vcc, s19, v112
	v_lshl_add_u64 v[174:175], v[98:99], 0, v[104:105]
	s_nop 0
	v_addc_co_u32_e32 v149, vcc, 0, v113, vcc
	v_add_co_u32_e32 v152, vcc, s20, v112
	v_lshlrev_b64 v[106:107], 11, v[106:107]
	s_nop 0
	v_addc_co_u32_e32 v153, vcc, 0, v113, vcc
	v_add_co_u32_e32 v156, vcc, s21, v112
	v_lshlrev_b64 v[108:109], 11, v[108:109]
	s_nop 0
	v_addc_co_u32_e32 v157, vcc, 0, v113, vcc
; __device__ __forceinline__ void cv_load(const float* W, int N, int nblk, int item, int lane, f32x4 (&tv)[16]) {
;     const int kb = item / nblk, nb = item - kb * nblk; const float* p = W + (size_t)(64 * kb + 16 * (lane >> 4)) * N + 64 * nb + 4 * (lane & 15);
; #pragma unroll
;     for (int i = 0; i < 16; ++i) tv[i] = __builtin_nontemporal_load((const f32x4*)(p + (size_t)i * N));
; }
; template <int MODE> __device__ __forceinline__ void cv_finish(const f32x4 (&tv)[16], int K, int nblk, unsigned char* WT, int item, int lane) {
;     const int kb = item / nblk, nb = item - kb * nblk, k0 = 64 * kb + 16 * (lane >> 4), n0 = 64 * nb + 4 * (lane & 15);
;     unsigned D[16];
; #pragma unroll
;     for (int i = 0; i < 16; ++i) { const f32x2 a = (f32x2){tv[i].x, tv[i].y} * (f32x2){1024.f, 1024.f}, b = (f32x2){tv[i].z, tv[i].w} * (f32x2){1024.f, 1024.f};
;         D[i] = pk4_fp8(a.x, a.y, b.x, b.y); }
	v_add_co_u32_e32 v160, vcc, s22, v112
	v_lshlrev_b64 v[110:111], 11, v[110:111]
	s_nop 0
	v_addc_co_u32_e32 v161, vcc, 0, v113, vcc
	v_add_co_u32_e32 v164, vcc, s23, v112
	global_load_dwordx4 v[102:105], v[112:113], off nt
	s_nop 0
	v_addc_co_u32_e32 v165, vcc, 0, v113, vcc
	v_lshl_add_u64 v[176:177], v[98:99], 0, v[106:107]
	v_lshl_add_u64 v[178:179], v[98:99], 0, v[108:109]
	v_lshl_add_u64 v[98:99], v[98:99], 0, v[110:111]
	global_load_dwordx4 v[106:109], v[114:115], off nt
	global_load_dwordx4 v[110:113], v[116:117], off nt
	s_nop 0
	global_load_dwordx4 v[114:117], v[118:119], off nt
	s_nop 0
	global_load_dwordx4 v[118:121], v[120:121], off nt
	s_nop 0
	global_load_dwordx4 v[122:125], v[122:123], off nt
	s_nop 0
	global_load_dwordx4 v[126:129], v[126:127], off nt
	s_nop 0
	global_load_dwordx4 v[132:135], v[132:133], off nt
	s_nop 0
	global_load_dwordx4 v[136:139], v[136:137], off nt
	s_nop 0
	global_load_dwordx4 v[140:143], v[140:141], off nt
	s_nop 0
	global_load_dwordx4 v[144:147], v[144:145], off nt
	s_nop 0
	global_load_dwordx4 v[148:151], v[148:149], off nt
	s_nop 0
	global_load_dwordx4 v[152:155], v[152:153], off nt
	s_nop 0
	global_load_dwordx4 v[156:159], v[156:157], off nt
	s_nop 0
	global_load_dwordx4 v[160:163], v[160:161], off nt
	s_nop 0
	global_load_dwordx4 v[164:167], v[164:165], off nt
	v_mov_b32_e32 v101, v67
	v_mov_b32_e32 v169, v67
	v_mov_b32_e32 v100, v67
	v_mov_b32_e32 v171, v67
	v_mov_b32_e32 v168, v67
	v_mov_b32_e32 v173, v67
	v_mov_b32_e32 v180, v67
	v_mov_b32_e32 v181, v67
	v_mov_b32_e32 v182, v67
	v_mov_b32_e32 v183, v67
	v_mov_b32_e32 v184, v67
	v_mov_b32_e32 v185, v67
	v_mov_b32_e32 v186, v67
	v_mov_b32_e32 v187, v67
	v_mov_b32_e32 v188, v67
	v_mov_b32_e32 v189, v67
	s_add_i32 s2, s2, 1
	s_add_i32 s40, s40, 64
	s_cmpk_eq_i32 s40, 0x100
	s_waitcnt vmcnt(31)
	v_pk_mul_f32 v[6:7], v[6:7], s[4:5] op_sel_hi:[1,0]
	s_nop 0
	v_med3_f32 v94, v6, s24, v72
	v_med3_f32 v95, v7, s24, v72
	s_waitcnt vmcnt(30)
	v_pk_mul_f32 v[6:7], v[10:11], s[4:5] op_sel_hi:[1,0]
	s_waitcnt vmcnt(29)
	v_pk_mul_f32 v[10:11], v[14:15], s[4:5] op_sel_hi:[1,0]
	s_waitcnt vmcnt(28)
	v_pk_mul_f32 v[14:15], v[18:19], s[4:5] op_sel_hi:[1,0]
	s_waitcnt vmcnt(27)
	v_pk_mul_f32 v[18:19], v[22:23], s[4:5] op_sel_hi:[1,0]
	s_waitcnt vmcnt(26)
	v_pk_mul_f32 v[22:23], v[26:27], s[4:5] op_sel_hi:[1,0]
	s_waitcnt vmcnt(25)
	v_pk_mul_f32 v[26:27], v[30:31], s[4:5] op_sel_hi:[1,0]
	s_waitcnt vmcnt(24)
	v_pk_mul_f32 v[30:31], v[34:35], s[4:5] op_sel_hi:[1,0]
	s_waitcnt vmcnt(23)
	v_pk_mul_f32 v[34:35], v[38:39], s[4:5] op_sel_hi:[1,0]
	s_waitcnt vmcnt(22)
	v_pk_mul_f32 v[38:39], v[42:43], s[4:5] op_sel_hi:[1,0]
	s_waitcnt vmcnt(21)
	v_pk_mul_f32 v[42:43], v[46:47], s[4:5] op_sel_hi:[1,0]
	s_waitcnt vmcnt(20)
	v_pk_mul_f32 v[46:47], v[50:51], s[4:5] op_sel_hi:[1,0]
	s_waitcnt vmcnt(19)
	v_pk_mul_f32 v[50:51], v[54:55], s[4:5] op_sel_hi:[1,0]
	s_waitcnt vmcnt(18)
	v_pk_mul_f32 v[54:55], v[58:59], s[4:5] op_sel_hi:[1,0]
	s_waitcnt vmcnt(17)
	v_pk_mul_f32 v[58:59], v[62:63], s[4:5] op_sel_hi:[1,0]
	s_waitcnt vmcnt(16)
	v_pk_mul_f32 v[62:63], v[68:69], s[4:5] op_sel_hi:[1,0]
	v_med3_f32 v6, v6, s24, v72
	v_med3_f32 v7, v7, s24, v72
	v_med3_f32 v10, v10, s24, v72
	v_med3_f32 v11, v11, s24, v72
	v_med3_f32 v14, v14, s24, v72
	v_med3_f32 v15, v15, s24, v72
	v_med3_f32 v18, v18, s24, v72
	v_med3_f32 v19, v19, s24, v72
	v_med3_f32 v22, v22, s24, v72
	v_med3_f32 v23, v23, s24, v72
	v_med3_f32 v26, v26, s24, v72
	v_med3_f32 v27, v27, s24, v72
	v_med3_f32 v30, v30, s24, v72
	v_med3_f32 v31, v31, s24, v72
	v_med3_f32 v34, v34, s24, v72
	v_med3_f32 v35, v35, s24, v72
	v_med3_f32 v38, v38, s24, v72
	v_med3_f32 v39, v39, s24, v72
	v_med3_f32 v42, v42, s24, v72
	v_med3_f32 v43, v43, s24, v72
	v_med3_f32 v46, v46, s24, v72
	v_med3_f32 v47, v47, s24, v72
	v_med3_f32 v50, v50, s24, v72
	v_med3_f32 v51, v51, s24, v72
	v_med3_f32 v54, v54, s24, v72
	v_med3_f32 v55, v55, s24, v72
	v_med3_f32 v58, v58, s24, v72
	v_med3_f32 v59, v59, s24, v72
	v_med3_f32 v62, v62, s24, v72
	v_med3_f32 v63, v63, s24, v72
	v_cvt_pk_fp8_f32 v5, v94, v95
	v_cvt_pk_fp8_f32 v73, v6, v7
	v_cvt_pk_fp8_f32 v80, v10, v11
	v_cvt_pk_fp8_f32 v81, v14, v15
	v_cvt_pk_fp8_f32 v82, v18, v19
	v_cvt_pk_fp8_f32 v83, v22, v23
	v_cvt_pk_fp8_f32 v84, v26, v27
	v_cvt_pk_fp8_f32 v85, v30, v31
	v_cvt_pk_fp8_f32 v86, v34, v35
	v_cvt_pk_fp8_f32 v87, v38, v39
	v_cvt_pk_fp8_f32 v88, v42, v43
	v_cvt_pk_fp8_f32 v89, v46, v47
	v_cvt_pk_fp8_f32 v90, v50, v51
	v_cvt_pk_fp8_f32 v91, v54, v55
	v_cvt_pk_fp8_f32 v92, v58, v59
	v_cvt_pk_fp8_f32 v93, v62, v63
	v_pk_mul_f32 v[8:9], v[8:9], s[4:5] op_sel_hi:[1,0]
	s_nop 0
	v_med3_f32 v96, v8, s24, v72
	v_med3_f32 v97, v9, s24, v72
	v_pk_mul_f32 v[8:9], v[12:13], s[4:5] op_sel_hi:[1,0]
	v_pk_mul_f32 v[12:13], v[16:17], s[4:5] op_sel_hi:[1,0]
	v_pk_mul_f32 v[16:17], v[20:21], s[4:5] op_sel_hi:[1,0]
	v_pk_mul_f32 v[20:21], v[24:25], s[4:5] op_sel_hi:[1,0]
	v_pk_mul_f32 v[24:25], v[28:29], s[4:5] op_sel_hi:[1,0]
	v_pk_mul_f32 v[28:29], v[32:33], s[4:5] op_sel_hi:[1,0]
	v_pk_mul_f32 v[32:33], v[36:37], s[4:5] op_sel_hi:[1,0]
	v_pk_mul_f32 v[36:37], v[40:41], s[4:5] op_sel_hi:[1,0]
	v_pk_mul_f32 v[40:41], v[44:45], s[4:5] op_sel_hi:[1,0]
	v_pk_mul_f32 v[44:45], v[48:49], s[4:5] op_sel_hi:[1,0]
	v_pk_mul_f32 v[48:49], v[52:53], s[4:5] op_sel_hi:[1,0]
	v_pk_mul_f32 v[52:53], v[56:57], s[4:5] op_sel_hi:[1,0]
	v_pk_mul_f32 v[56:57], v[60:61], s[4:5] op_sel_hi:[1,0]
	v_pk_mul_f32 v[60:61], v[64:65], s[4:5] op_sel_hi:[1,0]
	v_pk_mul_f32 v[64:65], v[70:71], s[4:5] op_sel_hi:[1,0]
	v_med3_f32 v8, v8, s24, v72
	v_med3_f32 v9, v9, s24, v72
	v_med3_f32 v12, v12, s24, v72
	v_med3_f32 v13, v13, s24, v72
; template <int MODE> __device__ __forceinline__ void cv_finish(const f32x4 (&tv)[16], int K, int nblk, unsigned char* WT, int item, int lane) {
;     const int kb = item / nblk, nb = item - kb * nblk, k0 = 64 * kb + 16 * (lane >> 4), n0 = 64 * nb + 4 * (lane & 15);
;     unsigned D[16];
; #pragma unroll
;     for (int i = 0; i < 16; ++i) { const f32x2 a = (f32x2){tv[i].x, tv[i].y} * (f32x2){1024.f, 1024.f}, b = (f32x2){tv[i].z, tv[i].w} * (f32x2){1024.f, 1024.f};
;         D[i] = pk4_fp8(a.x, a.y, b.x, b.y); }
;     unsigned O[4][4];
; #pragma unroll
;     for (int q = 0; q < 4; ++q) { const unsigned a = D[4 * q], b = D[4 * q + 1], c = D[4 * q + 2], d = D[4 * q + 3];
;         const unsigned t0 = __builtin_amdgcn_perm(b, a, 0x05010400u), t1 = __builtin_amdgcn_perm(b, a, 0x07030602u), u0 = __builtin_amdgcn_perm(d, c, 0x05010400u), u1 = __builtin_amdgcn_perm(d, c, 0x07030602u);
;         O[0][q] = __builtin_amdgcn_perm(u0, t0, 0x05040100u); O[1][q] = __builtin_amdgcn_perm(u0, t0, 0x07060302u); O[2][q] = __builtin_amdgcn_perm(u1, t1, 0x05040100u); O[3][q] = __builtin_amdgcn_perm(u1, t1, 0x07060302u); }
; #pragma unroll
;     for (int j = 0; j < 4; ++j) { u32x4 o; o.x = O[j][0]; o.y = O[j][1]; o.z = O[j][2]; o.w = O[j][3];
;         __builtin_nontemporal_store(o, (u32x4*)(WT + (size_t)drow<MODE>(n0 + j) * K + k0)); }
; }
	v_med3_f32 v16, v16, s24, v72
	v_med3_f32 v17, v17, s24, v72
	v_med3_f32 v20, v20, s24, v72
	v_med3_f32 v21, v21, s24, v72
	v_med3_f32 v24, v24, s24, v72
	v_med3_f32 v25, v25, s24, v72
	v_med3_f32 v28, v28, s24, v72
	v_med3_f32 v29, v29, s24, v72
	v_med3_f32 v32, v32, s24, v72
	v_med3_f32 v33, v33, s24, v72
	v_med3_f32 v36, v36, s24, v72
	v_med3_f32 v37, v37, s24, v72
	v_med3_f32 v40, v40, s24, v72
	v_med3_f32 v41, v41, s24, v72
	v_med3_f32 v44, v44, s24, v72
	v_med3_f32 v45, v45, s24, v72
	v_med3_f32 v48, v48, s24, v72
	v_med3_f32 v49, v49, s24, v72
	v_med3_f32 v52, v52, s24, v72
	v_med3_f32 v53, v53, s24, v72
	v_med3_f32 v56, v56, s24, v72
	v_med3_f32 v57, v57, s24, v72
	v_med3_f32 v60, v60, s24, v72
	v_med3_f32 v61, v61, s24, v72
	v_med3_f32 v64, v64, s24, v72
	v_med3_f32 v65, v65, s24, v72
	v_cvt_pk_fp8_f32 v5, v96, v97 op_sel:[0,0,1]
	v_cvt_pk_fp8_f32 v73, v8, v9 op_sel:[0,0,1]
	v_cvt_pk_fp8_f32 v80, v12, v13 op_sel:[0,0,1]
	v_cvt_pk_fp8_f32 v81, v16, v17 op_sel:[0,0,1]
	v_cvt_pk_fp8_f32 v82, v20, v21 op_sel:[0,0,1]
	v_cvt_pk_fp8_f32 v83, v24, v25 op_sel:[0,0,1]
	v_cvt_pk_fp8_f32 v84, v28, v29 op_sel:[0,0,1]
	v_cvt_pk_fp8_f32 v85, v32, v33 op_sel:[0,0,1]
	v_cvt_pk_fp8_f32 v86, v36, v37 op_sel:[0,0,1]
	v_cvt_pk_fp8_f32 v87, v40, v41 op_sel:[0,0,1]
	v_cvt_pk_fp8_f32 v88, v44, v45 op_sel:[0,0,1]
	v_cvt_pk_fp8_f32 v89, v48, v49 op_sel:[0,0,1]
	v_cvt_pk_fp8_f32 v90, v52, v53 op_sel:[0,0,1]
	v_cvt_pk_fp8_f32 v91, v56, v57 op_sel:[0,0,1]
	v_cvt_pk_fp8_f32 v92, v60, v61 op_sel:[0,0,1]
	v_cvt_pk_fp8_f32 v93, v64, v65 op_sel:[0,0,1]
	v_perm_b32 v7, v73, v5, s25
	v_perm_b32 v5, v73, v5, s26
	v_perm_b32 v8, v81, v80, s25
	v_perm_b32 v9, v81, v80, s26
	v_perm_b32 v11, v83, v82, s25
	v_perm_b32 v13, v85, v84, s25
	v_perm_b32 v17, v87, v86, s25
	v_perm_b32 v21, v89, v88, s25
	v_perm_b32 v23, v91, v90, s25
	v_perm_b32 v25, v93, v92, s25
	v_perm_b32 v12, v83, v82, s26
	v_perm_b32 v16, v85, v84, s26
	v_perm_b32 v20, v87, v86, s26
	v_perm_b32 v22, v89, v88, s26
	v_perm_b32 v24, v91, v90, s26
	v_perm_b32 v26, v93, v92, s26
	v_perm_b32 v6, v8, v7, s27
	v_perm_b32 v10, v8, v7, s28
	v_perm_b32 v14, v9, v5, s27
	v_perm_b32 v18, v9, v5, s28
	v_perm_b32 v7, v13, v11, s27
	v_perm_b32 v8, v21, v17, s27
	v_perm_b32 v9, v25, v23, s27
	v_perm_b32 v11, v13, v11, s28
	v_perm_b32 v15, v16, v12, s27
	v_perm_b32 v19, v16, v12, s28
	v_perm_b32 v12, v21, v17, s28
	v_perm_b32 v16, v22, v20, s27
	v_perm_b32 v20, v22, v20, s28
	v_perm_b32 v13, v25, v23, s28
	v_perm_b32 v17, v26, v24, s27
	v_perm_b32 v21, v26, v24, s28
	global_store_dwordx4 v[74:75], v[6:9], off nt
	global_store_dwordx4 v[76:77], v[10:13], off nt
	global_store_dwordx4 v[78:79], v[14:17], off nt
	global_store_dwordx4 v[2:3], v[18:21], off nt
	s_waitcnt vmcnt(19)
	v_pk_mul_f32 v[102:103], v[102:103], s[4:5] op_sel_hi:[1,0]
	s_nop 0
	v_med3_f32 v190, v102, s24, v72
	v_med3_f32 v191, v103, s24, v72
	s_waitcnt vmcnt(18)
	v_pk_mul_f32 v[102:103], v[106:107], s[4:5] op_sel_hi:[1,0]
	s_waitcnt vmcnt(17)
	v_pk_mul_f32 v[106:107], v[110:111], s[4:5] op_sel_hi:[1,0]
	s_waitcnt vmcnt(16)
	v_pk_mul_f32 v[110:111], v[114:115], s[4:5] op_sel_hi:[1,0]
	s_waitcnt vmcnt(15)
	v_pk_mul_f32 v[114:115], v[118:119], s[4:5] op_sel_hi:[1,0]
	s_waitcnt vmcnt(14)
	v_pk_mul_f32 v[118:119], v[122:123], s[4:5] op_sel_hi:[1,0]
	s_waitcnt vmcnt(13)
	v_pk_mul_f32 v[122:123], v[126:127], s[4:5] op_sel_hi:[1,0]
	s_waitcnt vmcnt(12)
	v_pk_mul_f32 v[126:127], v[132:133], s[4:5] op_sel_hi:[1,0]
	s_waitcnt vmcnt(11)
	v_pk_mul_f32 v[132:133], v[136:137], s[4:5] op_sel_hi:[1,0]
	s_waitcnt vmcnt(10)
	v_pk_mul_f32 v[136:137], v[140:141], s[4:5] op_sel_hi:[1,0]
	s_waitcnt vmcnt(9)
	v_pk_mul_f32 v[140:141], v[144:145], s[4:5] op_sel_hi:[1,0]
	s_waitcnt vmcnt(8)
	v_pk_mul_f32 v[144:145], v[148:149], s[4:5] op_sel_hi:[1,0]
	s_waitcnt vmcnt(7)
	v_pk_mul_f32 v[148:149], v[152:153], s[4:5] op_sel_hi:[1,0]
	s_waitcnt vmcnt(6)
	v_pk_mul_f32 v[152:153], v[156:157], s[4:5] op_sel_hi:[1,0]
	s_waitcnt vmcnt(5)
	v_pk_mul_f32 v[156:157], v[160:161], s[4:5] op_sel_hi:[1,0]
	s_waitcnt vmcnt(4)
; template <int MODE> __device__ __forceinline__ void cv_finish(const f32x4 (&tv)[16], int K, int nblk, unsigned char* WT, int item, int lane) {
;     const int kb = item / nblk, nb = item - kb * nblk, k0 = 64 * kb + 16 * (lane >> 4), n0 = 64 * nb + 4 * (lane & 15);
;     unsigned D[16];
; #pragma unroll
;     for (int i = 0; i < 16; ++i) { const f32x2 a = (f32x2){tv[i].x, tv[i].y} * (f32x2){1024.f, 1024.f}, b = (f32x2){tv[i].z, tv[i].w} * (f32x2){1024.f, 1024.f};
;         D[i] = pk4_fp8(a.x, a.y, b.x, b.y); }
;     unsigned O[4][4];
; #pragma unroll
;     for (int q = 0; q < 4; ++q) { const unsigned a = D[4 * q], b = D[4 * q + 1], c = D[4 * q + 2], d = D[4 * q + 3];
;         const unsigned t0 = __builtin_amdgcn_perm(b, a, 0x05010400u), t1 = __builtin_amdgcn_perm(b, a, 0x07030602u), u0 = __builtin_amdgcn_perm(d, c, 0x05010400u), u1 = __builtin_amdgcn_perm(d, c, 0x07030602u);
;         O[0][q] = __builtin_amdgcn_perm(u0, t0, 0x05040100u); O[1][q] = __builtin_amdgcn_perm(u0, t0, 0x07060302u); O[2][q] = __builtin_amdgcn_perm(u1, t1, 0x05040100u); O[3][q] = __builtin_amdgcn_perm(u1, t1, 0x07060302u); }
; #pragma unroll
;     for (int j = 0; j < 4; ++j) { u32x4 o; o.x = O[j][0]; o.y = O[j][1]; o.z = O[j][2]; o.w = O[j][3];
;         __builtin_nontemporal_store(o, (u32x4*)(WT + (size_t)drow<MODE>(n0 + j) * K + k0)); }
; }
	v_pk_mul_f32 v[160:161], v[164:165], s[4:5] op_sel_hi:[1,0]
	v_med3_f32 v102, v102, s24, v72
	v_med3_f32 v103, v103, s24, v72
	v_med3_f32 v106, v106, s24, v72
	v_med3_f32 v107, v107, s24, v72
	v_med3_f32 v110, v110, s24, v72
	v_med3_f32 v111, v111, s24, v72
	v_med3_f32 v114, v114, s24, v72
	v_med3_f32 v115, v115, s24, v72
	v_med3_f32 v118, v118, s24, v72
	v_med3_f32 v119, v119, s24, v72
	v_med3_f32 v122, v122, s24, v72
	v_med3_f32 v123, v123, s24, v72
	v_med3_f32 v126, v126, s24, v72
	v_med3_f32 v127, v127, s24, v72
	v_med3_f32 v132, v132, s24, v72
	v_med3_f32 v133, v133, s24, v72
	v_med3_f32 v136, v136, s24, v72
	v_med3_f32 v137, v137, s24, v72
	v_med3_f32 v140, v140, s24, v72
	v_med3_f32 v141, v141, s24, v72
	v_med3_f32 v144, v144, s24, v72
	v_med3_f32 v145, v145, s24, v72
	v_med3_f32 v148, v148, s24, v72
	v_med3_f32 v149, v149, s24, v72
	v_med3_f32 v152, v152, s24, v72
	v_med3_f32 v153, v153, s24, v72
	v_med3_f32 v156, v156, s24, v72
	v_med3_f32 v157, v157, s24, v72
	v_med3_f32 v160, v160, s24, v72
	v_med3_f32 v161, v161, s24, v72
	v_cvt_pk_fp8_f32 v101, v190, v191
	v_cvt_pk_fp8_f32 v169, v102, v103
	v_cvt_pk_fp8_f32 v100, v106, v107
	v_cvt_pk_fp8_f32 v171, v110, v111
	v_cvt_pk_fp8_f32 v168, v114, v115
	v_cvt_pk_fp8_f32 v173, v118, v119
	v_cvt_pk_fp8_f32 v180, v122, v123
	v_cvt_pk_fp8_f32 v181, v126, v127
	v_cvt_pk_fp8_f32 v182, v132, v133
	v_cvt_pk_fp8_f32 v183, v136, v137
	v_cvt_pk_fp8_f32 v184, v140, v141
	v_cvt_pk_fp8_f32 v185, v144, v145
	v_cvt_pk_fp8_f32 v186, v148, v149
	v_cvt_pk_fp8_f32 v187, v152, v153
	v_cvt_pk_fp8_f32 v188, v156, v157
	v_cvt_pk_fp8_f32 v189, v160, v161
	v_pk_mul_f32 v[104:105], v[104:105], s[4:5] op_sel_hi:[1,0]
	s_nop 0
	v_med3_f32 v192, v104, s24, v72
	v_med3_f32 v193, v105, s24, v72
	v_pk_mul_f32 v[104:105], v[108:109], s[4:5] op_sel_hi:[1,0]
	v_pk_mul_f32 v[108:109], v[112:113], s[4:5] op_sel_hi:[1,0]
	v_pk_mul_f32 v[112:113], v[116:117], s[4:5] op_sel_hi:[1,0]
	v_pk_mul_f32 v[116:117], v[120:121], s[4:5] op_sel_hi:[1,0]
	v_pk_mul_f32 v[120:121], v[124:125], s[4:5] op_sel_hi:[1,0]
	v_pk_mul_f32 v[124:125], v[128:129], s[4:5] op_sel_hi:[1,0]
	v_pk_mul_f32 v[128:129], v[134:135], s[4:5] op_sel_hi:[1,0]
	v_pk_mul_f32 v[134:135], v[138:139], s[4:5] op_sel_hi:[1,0]
	v_pk_mul_f32 v[138:139], v[142:143], s[4:5] op_sel_hi:[1,0]
	v_pk_mul_f32 v[142:143], v[146:147], s[4:5] op_sel_hi:[1,0]
	v_pk_mul_f32 v[146:147], v[150:151], s[4:5] op_sel_hi:[1,0]
	v_pk_mul_f32 v[150:151], v[154:155], s[4:5] op_sel_hi:[1,0]
	v_pk_mul_f32 v[154:155], v[158:159], s[4:5] op_sel_hi:[1,0]
	v_pk_mul_f32 v[158:159], v[162:163], s[4:5] op_sel_hi:[1,0]
	v_pk_mul_f32 v[162:163], v[166:167], s[4:5] op_sel_hi:[1,0]
	v_med3_f32 v104, v104, s24, v72
	v_med3_f32 v105, v105, s24, v72
	v_med3_f32 v108, v108, s24, v72
	v_med3_f32 v109, v109, s24, v72
	v_med3_f32 v112, v112, s24, v72
	v_med3_f32 v113, v113, s24, v72
	v_med3_f32 v116, v116, s24, v72
	v_med3_f32 v117, v117, s24, v72
	v_med3_f32 v120, v120, s24, v72
	v_med3_f32 v121, v121, s24, v72
	v_med3_f32 v124, v124, s24, v72
	v_med3_f32 v125, v125, s24, v72
	v_med3_f32 v128, v128, s24, v72
	v_med3_f32 v129, v129, s24, v72
	v_med3_f32 v134, v134, s24, v72
	v_med3_f32 v135, v135, s24, v72
	v_med3_f32 v138, v138, s24, v72
	v_med3_f32 v139, v139, s24, v72
	v_med3_f32 v142, v142, s24, v72
	v_med3_f32 v143, v143, s24, v72
	v_med3_f32 v146, v146, s24, v72
	v_med3_f32 v147, v147, s24, v72
	v_med3_f32 v150, v150, s24, v72
	v_med3_f32 v151, v151, s24, v72
	v_med3_f32 v154, v154, s24, v72
	v_med3_f32 v155, v155, s24, v72
	v_med3_f32 v158, v158, s24, v72
	v_med3_f32 v159, v159, s24, v72
	v_med3_f32 v162, v162, s24, v72
	v_med3_f32 v163, v163, s24, v72
	v_cvt_pk_fp8_f32 v101, v192, v193 op_sel:[0,0,1]
	v_cvt_pk_fp8_f32 v169, v104, v105 op_sel:[0,0,1]
	v_cvt_pk_fp8_f32 v100, v108, v109 op_sel:[0,0,1]
	v_cvt_pk_fp8_f32 v171, v112, v113 op_sel:[0,0,1]
	v_cvt_pk_fp8_f32 v168, v116, v117 op_sel:[0,0,1]
	v_cvt_pk_fp8_f32 v173, v120, v121 op_sel:[0,0,1]
	v_cvt_pk_fp8_f32 v180, v124, v125 op_sel:[0,0,1]
	v_cvt_pk_fp8_f32 v181, v128, v129 op_sel:[0,0,1]
	v_cvt_pk_fp8_f32 v182, v134, v135 op_sel:[0,0,1]
	v_cvt_pk_fp8_f32 v183, v138, v139 op_sel:[0,0,1]
	v_cvt_pk_fp8_f32 v184, v142, v143 op_sel:[0,0,1]
	v_cvt_pk_fp8_f32 v185, v146, v147 op_sel:[0,0,1]
	v_cvt_pk_fp8_f32 v186, v150, v151 op_sel:[0,0,1]
	v_cvt_pk_fp8_f32 v187, v154, v155 op_sel:[0,0,1]
	v_cvt_pk_fp8_f32 v188, v158, v159 op_sel:[0,0,1]
	v_cvt_pk_fp8_f32 v189, v162, v163 op_sel:[0,0,1]
	v_perm_b32 v103, v169, v101, s25
	v_perm_b32 v101, v169, v101, s26
	v_perm_b32 v104, v171, v100, s25
	v_perm_b32 v105, v171, v100, s26
	v_perm_b32 v107, v173, v168, s25
	v_perm_b32 v109, v181, v180, s25
	v_perm_b32 v113, v183, v182, s25
	v_perm_b32 v117, v185, v184, s25
	v_perm_b32 v119, v187, v186, s25
	v_perm_b32 v121, v189, v188, s25
	v_perm_b32 v108, v173, v168, s26
	v_perm_b32 v112, v181, v180, s26
	v_perm_b32 v116, v183, v182, s26
	v_perm_b32 v118, v185, v184, s26
	v_perm_b32 v120, v187, v186, s26
	v_perm_b32 v122, v189, v188, s26
	v_perm_b32 v102, v104, v103, s27
	v_perm_b32 v106, v104, v103, s28
	v_perm_b32 v110, v105, v101, s27
	v_perm_b32 v114, v105, v101, s28
	v_perm_b32 v103, v109, v107, s27
	v_perm_b32 v104, v117, v113, s27
	v_perm_b32 v105, v121, v119, s27
	v_perm_b32 v107, v109, v107, s28
	v_perm_b32 v111, v112, v108, s27
	v_perm_b32 v115, v112, v108, s28
	v_perm_b32 v108, v117, v113, s28
	v_perm_b32 v112, v118, v116, s27
	v_perm_b32 v116, v118, v116, s28
	v_perm_b32 v109, v121, v119, s28
	v_perm_b32 v113, v122, v120, s27
	v_perm_b32 v117, v122, v120, s28
	global_store_dwordx4 v[174:175], v[102:105], off nt
	global_store_dwordx4 v[176:177], v[106:109], off nt
	global_store_dwordx4 v[178:179], v[110:113], off nt
	global_store_dwordx4 v[98:99], v[114:117], off nt
	s_cbranch_scc0 .LBB0_761
	s_mov_b64 s[6:7], 0

; template <int MODE> __device__ __forceinline__ int drow(int n) {
;     if (MODE == 1) { const int h = n / 192, nl = n - h * 192; return nl < 128 ? n : h * 192 + 128 + ((nl - 128) & 31) * 2 + ((nl - 128) >> 5); }
;     if (MODE == 2) { return n < FF ? ((n >> 7) * 256 + (n & 127)) : (((n - FF) >> 7) * 256 + 128 + ((n - FF) & 127)); }
; __device__ __forceinline__ void cv_load(const float* W, int N, int nblk, int item, int lane, f32x4 (&tv)[16]) {
;     const int kb = item / nblk, nb = item - kb * nblk; const float* p = W + (size_t)(64 * kb + 16 * (lane >> 4)) * N + 64 * nb + 4 * (lane & 15);
; #pragma unroll
;     for (int i = 0; i < 16; ++i) tv[i] = __builtin_nontemporal_load((const f32x4*)(p + (size_t)i * N));
; }
.LBB0_766:
	s_ashr_i32 s10, s2, 31
	s_lshr_b32 s10, s10, 26
	s_add_i32 s10, s2, s10
	s_ashr_i32 s41, s10, 6
	s_andn2_b32 s10, s10, 63
	v_or_b32_e32 v68, s10, v1
	v_ashrrev_i32_e32 v69, 31, v68
	s_lshl_b32 s10, s41, 12
	v_lshlrev_b64 v[2:3], 14, v[68:69]
	s_sub_i32 s10, s39, s10
	v_lshl_add_u64 v[2:3], s[6:7], 0, v[2:3]
	s_ashr_i32 s11, s10, 31
	v_lshl_add_u64 v[2:3], s[10:11], 2, v[2:3]
	v_lshl_add_u64 v[2:3], v[2:3], 0, v[66:67]
	v_add_co_u32_e32 v4, vcc, s1, v2
	v_add_u32_e32 v75, s10, v130
	s_nop 0
	v_addc_co_u32_e32 v5, vcc, 0, v3, vcc
	global_load_dwordx4 v[62:65], v[2:3], off nt
	global_load_dwordx4 v[58:61], v[4:5], off nt
	v_add_co_u32_e32 v4, vcc, s12, v2
	v_add_u32_e32 v70, s40, v73
	s_nop 0
	v_addc_co_u32_e32 v5, vcc, 0, v3, vcc
	v_add_co_u32_e32 v6, vcc, s14, v2
	s_lshl_b32 s10, s41, 13
	s_nop 0
	v_addc_co_u32_e32 v7, vcc, 0, v3, vcc
	global_load_dwordx4 v[54:57], v[4:5], off nt
	global_load_dwordx4 v[50:53], v[6:7], off nt
	v_add_co_u32_e32 v4, vcc, s16, v2
	v_subrev_u32_e32 v74, s10, v70
	s_nop 0
	v_addc_co_u32_e32 v5, vcc, 0, v3, vcc
	v_add_co_u32_e32 v6, vcc, s18, v2
	v_and_b32_e32 v71, 0x7c, v75
	s_nop 0
	v_addc_co_u32_e32 v7, vcc, 0, v3, vcc
	global_load_dwordx4 v[46:49], v[4:5], off nt
	global_load_dwordx4 v[42:45], v[6:7], off nt
	v_add_co_u32_e32 v4, vcc, s20, v2
	s_nop 1
	v_addc_co_u32_e32 v5, vcc, 0, v3, vcc
	v_add_co_u32_e32 v6, vcc, s22, v2
	s_nop 1
	v_addc_co_u32_e32 v7, vcc, 0, v3, vcc
	global_load_dwordx4 v[38:41], v[4:5], off nt
	global_load_dwordx4 v[34:37], v[6:7], off nt
	v_add_co_u32_e32 v4, vcc, s29, v2
	s_nop 1
	v_addc_co_u32_e32 v5, vcc, 0, v3, vcc
	v_add_co_u32_e32 v6, vcc, s30, v2
	s_nop 1
	v_addc_co_u32_e32 v7, vcc, 0, v3, vcc
	global_load_dwordx4 v[30:33], v[4:5], off nt
	global_load_dwordx4 v[26:29], v[6:7], off nt
	v_add_co_u32_e32 v4, vcc, s31, v2
	s_nop 1
	v_addc_co_u32_e32 v5, vcc, 0, v3, vcc
	v_add_co_u32_e32 v6, vcc, s33, v2
	s_nop 1
	v_addc_co_u32_e32 v7, vcc, 0, v3, vcc
	global_load_dwordx4 v[22:25], v[4:5], off nt
	global_load_dwordx4 v[18:21], v[6:7], off nt
	v_add_co_u32_e32 v4, vcc, s34, v2
	s_nop 1
	v_addc_co_u32_e32 v5, vcc, 0, v3, vcc
	v_add_co_u32_e32 v6, vcc, s35, v2
	s_nop 1
	v_addc_co_u32_e32 v7, vcc, 0, v3, vcc
	global_load_dwordx4 v[14:17], v[4:5], off nt
	global_load_dwordx4 v[10:13], v[6:7], off nt
	v_add_co_u32_e32 v4, vcc, 0x38000, v2
	s_nop 1
	v_addc_co_u32_e32 v5, vcc, 0, v3, vcc
	v_add_co_u32_e32 v2, vcc, 0x3c000, v2
	s_nop 1
	v_addc_co_u32_e32 v3, vcc, 0, v3, vcc
	global_load_dwordx4 v[6:9], v[4:5], off nt
	s_nop 0
	global_load_dwordx4 v[2:5], v[2:3], off nt
	s_addk_i32 s40, 0x80
	s_add_i32 s39, s39, 64
	s_add_i32 s2, s2, 1
	s_ashr_i32 s10, s2, 31
	s_lshr_b32 s10, s10, 26
	s_add_i32 s10, s2, s10
	s_ashr_i32 s41, s10, 6
	s_andn2_b32 s10, s10, 63
	v_or_b32_e32 v148, s10, v1
	v_ashrrev_i32_e32 v149, 31, v148
	s_lshl_b32 s10, s41, 12
	v_lshlrev_b64 v[80:81], 14, v[148:149]
	s_sub_i32 s10, s39, s10
	v_lshl_add_u64 v[80:81], s[6:7], 0, v[80:81]
	s_ashr_i32 s11, s10, 31
	v_lshl_add_u64 v[80:81], s[10:11], 2, v[80:81]
	v_lshl_add_u64 v[80:81], v[80:81], 0, v[66:67]
	v_add_co_u32_e32 v82, vcc, s1, v80
	v_add_u32_e32 v129, s10, v130
	s_nop 0
	v_addc_co_u32_e32 v83, vcc, 0, v81, vcc
	global_load_dwordx4 v[144:147], v[80:81], off nt
	global_load_dwordx4 v[140:143], v[82:83], off nt
	v_add_co_u32_e32 v82, vcc, s12, v80
	v_add_u32_e32 v150, s40, v73
	s_nop 0
	v_addc_co_u32_e32 v83, vcc, 0, v81, vcc
	v_add_co_u32_e32 v84, vcc, s14, v80
	s_lshl_b32 s10, s41, 13
	s_nop 0
	v_addc_co_u32_e32 v85, vcc, 0, v81, vcc
	global_load_dwordx4 v[136:139], v[82:83], off nt
	global_load_dwordx4 v[132:135], v[84:85], off nt
	v_add_co_u32_e32 v82, vcc, s16, v80
	v_subrev_u32_e32 v128, s10, v150
	s_nop 0
	v_addc_co_u32_e32 v83, vcc, 0, v81, vcc
	v_add_co_u32_e32 v84, vcc, s18, v80
	v_and_b32_e32 v151, 0x7c, v129
	s_nop 0
	v_addc_co_u32_e32 v85, vcc, 0, v81, vcc
	global_load_dwordx4 v[124:127], v[82:83], off nt
	global_load_dwordx4 v[120:123], v[84:85], off nt
	v_add_co_u32_e32 v82, vcc, s20, v80
	s_nop 1
	v_addc_co_u32_e32 v83, vcc, 0, v81, vcc
	v_add_co_u32_e32 v84, vcc, s22, v80
	s_nop 1
	v_addc_co_u32_e32 v85, vcc, 0, v81, vcc
	global_load_dwordx4 v[116:119], v[82:83], off nt
	global_load_dwordx4 v[112:115], v[84:85], off nt
	v_add_co_u32_e32 v82, vcc, s29, v80
	s_nop 1
	v_addc_co_u32_e32 v83, vcc, 0, v81, vcc
	v_add_co_u32_e32 v84, vcc, s30, v80
	s_nop 1
	v_addc_co_u32_e32 v85, vcc, 0, v81, vcc
	global_load_dwordx4 v[108:111], v[82:83], off nt
	global_load_dwordx4 v[104:107], v[84:85], off nt
	v_add_co_u32_e32 v82, vcc, s31, v80
	s_nop 1
	v_addc_co_u32_e32 v83, vcc, 0, v81, vcc
	v_add_co_u32_e32 v84, vcc, s33, v80
	s_nop 1
	v_addc_co_u32_e32 v85, vcc, 0, v81, vcc
	global_load_dwordx4 v[100:103], v[82:83], off nt
	global_load_dwordx4 v[96:99], v[84:85], off nt
	v_add_co_u32_e32 v82, vcc, s34, v80
	s_nop 1
	v_addc_co_u32_e32 v83, vcc, 0, v81, vcc
	v_add_co_u32_e32 v84, vcc, s35, v80
	s_nop 1
	v_addc_co_u32_e32 v85, vcc, 0, v81, vcc
	global_load_dwordx4 v[92:95], v[82:83], off nt
	global_load_dwordx4 v[88:91], v[84:85], off nt
	v_add_co_u32_e32 v82, vcc, 0x38000, v80
	s_nop 1
	v_addc_co_u32_e32 v83, vcc, 0, v81, vcc
	v_add_co_u32_e32 v80, vcc, 0x3c000, v80
	s_nop 1
	v_addc_co_u32_e32 v81, vcc, 0, v81, vcc
	global_load_dwordx4 v[84:87], v[82:83], off nt
	s_nop 0
	global_load_dwordx4 v[80:83], v[80:81], off nt
	s_addk_i32 s40, 0x80
	s_add_i32 s39, s39, 64
	s_add_i32 s2, s2, 1
	v_cmp_lt_i32_e32 vcc, s36, v75
	s_and_saveexec_b64 s[10:11], vcc
	s_xor_b64 s[10:11], exec, s[10:11]
	v_add_u32_e32 v70, 0x7ffff000, v74
	v_and_b32_e32 v70, 0x7fffff00, v70
	v_or3_b32 v70, v71, v70, s37
	s_andn2_saveexec_b64 s[10:11], s[10:11]
	v_and_or_b32 v70, v74, s38, v71
	s_or_b64 exec, exec, s[10:11]
	s_waitcnt vmcnt(31)
; template <int MODE> __device__ __forceinline__ void cv_finish(const f32x4 (&tv)[16], int K, int nblk, unsigned char* WT, int item, int lane) {
;     ...
;     for (int i = 0; i < 16; ++i) { const f32x2 a = (f32x2){tv[i].x, tv[i].y} * (f32x2){1024.f, 1024.f}, b = (f32x2){tv[i].z, tv[i].w} * (f32x2){1024.f, 1024.f};
;         D[i] = pk4_fp8(a.x, a.y, b.x, b.y); }
	v_pk_mul_f32 v[62:63], v[62:63], s[4:5] op_sel_hi:[1,0]
	v_pk_mul_f32 v[64:65], v[64:65], s[4:5] op_sel_hi:[1,0]
	v_med3_f32 v71, v62, s24, v72
	v_med3_f32 v63, v63, s24, v72
	v_mov_b32_e32 v62, v67
	v_cvt_pk_fp8_f32 v62, v71, v63
	v_med3_f32 v63, v64, s24, v72
	v_med3_f32 v64, v65, s24, v72
	s_waitcnt vmcnt(30)
	v_pk_mul_f32 v[58:59], v[58:59], s[4:5] op_sel_hi:[1,0]
	v_cvt_pk_fp8_f32 v62, v63, v64 op_sel:[0,0,1]
	v_med3_f32 v63, v58, s24, v72
	v_med3_f32 v59, v59, s24, v72
	v_mov_b32_e32 v58, v67
	v_cvt_pk_fp8_f32 v58, v63, v59
	v_pk_mul_f32 v[60:61], v[60:61], s[4:5] op_sel_hi:[1,0]
	s_waitcnt vmcnt(29)
	v_pk_mul_f32 v[54:55], v[54:55], s[4:5] op_sel_hi:[1,0]
	v_med3_f32 v59, v60, s24, v72
	v_med3_f32 v60, v61, s24, v72
	v_cvt_pk_fp8_f32 v58, v59, v60 op_sel:[0,0,1]
	v_med3_f32 v59, v54, s24, v72
	v_med3_f32 v55, v55, s24, v72
	v_mov_b32_e32 v54, v67
	v_cvt_pk_fp8_f32 v54, v59, v55
	v_pk_mul_f32 v[56:57], v[56:57], s[4:5] op_sel_hi:[1,0]
	s_waitcnt vmcnt(28)
	v_pk_mul_f32 v[50:51], v[50:51], s[4:5] op_sel_hi:[1,0]
	v_med3_f32 v55, v56, s24, v72
	v_med3_f32 v56, v57, s24, v72
	v_cvt_pk_fp8_f32 v54, v55, v56 op_sel:[0,0,1]
	v_med3_f32 v55, v50, s24, v72
	v_med3_f32 v51, v51, s24, v72
	v_mov_b32_e32 v50, v67
	v_cvt_pk_fp8_f32 v50, v55, v51
	v_pk_mul_f32 v[52:53], v[52:53], s[4:5] op_sel_hi:[1,0]
	s_waitcnt vmcnt(27)
	v_pk_mul_f32 v[46:47], v[46:47], s[4:5] op_sel_hi:[1,0]
	v_med3_f32 v51, v52, s24, v72
	v_med3_f32 v52, v53, s24, v72
	v_cvt_pk_fp8_f32 v50, v51, v52 op_sel:[0,0,1]
	v_med3_f32 v51, v46, s24, v72
	v_med3_f32 v47, v47, s24, v72
	v_mov_b32_e32 v46, v67
	v_cvt_pk_fp8_f32 v46, v51, v47
	v_pk_mul_f32 v[48:49], v[48:49], s[4:5] op_sel_hi:[1,0]
	s_waitcnt vmcnt(26)
	v_pk_mul_f32 v[42:43], v[42:43], s[4:5] op_sel_hi:[1,0]
	v_med3_f32 v47, v48, s24, v72
	v_med3_f32 v48, v49, s24, v72
	v_cvt_pk_fp8_f32 v46, v47, v48 op_sel:[0,0,1]
	v_med3_f32 v47, v42, s24, v72
	v_med3_f32 v43, v43, s24, v72
	v_mov_b32_e32 v42, v67
	v_cvt_pk_fp8_f32 v42, v47, v43
	v_pk_mul_f32 v[44:45], v[44:45], s[4:5] op_sel_hi:[1,0]
	s_waitcnt vmcnt(25)
	v_pk_mul_f32 v[38:39], v[38:39], s[4:5] op_sel_hi:[1,0]
	v_med3_f32 v43, v44, s24, v72
	v_med3_f32 v44, v45, s24, v72
	v_cvt_pk_fp8_f32 v42, v43, v44 op_sel:[0,0,1]
	v_med3_f32 v43, v38, s24, v72
	v_med3_f32 v39, v39, s24, v72
	v_mov_b32_e32 v38, v67
	v_cvt_pk_fp8_f32 v38, v43, v39
	v_pk_mul_f32 v[40:41], v[40:41], s[4:5] op_sel_hi:[1,0]
	s_waitcnt vmcnt(24)
	v_pk_mul_f32 v[34:35], v[34:35], s[4:5] op_sel_hi:[1,0]
	v_med3_f32 v39, v40, s24, v72
	v_med3_f32 v40, v41, s24, v72
	v_cvt_pk_fp8_f32 v38, v39, v40 op_sel:[0,0,1]
	v_med3_f32 v39, v34, s24, v72
	v_med3_f32 v35, v35, s24, v72
	v_mov_b32_e32 v34, v67
	v_cvt_pk_fp8_f32 v34, v39, v35
	v_pk_mul_f32 v[36:37], v[36:37], s[4:5] op_sel_hi:[1,0]
	s_waitcnt vmcnt(23)
	v_pk_mul_f32 v[30:31], v[30:31], s[4:5] op_sel_hi:[1,0]
	v_med3_f32 v35, v36, s24, v72
	v_med3_f32 v36, v37, s24, v72
	v_cvt_pk_fp8_f32 v34, v35, v36 op_sel:[0,0,1]
	v_med3_f32 v35, v30, s24, v72
	v_med3_f32 v31, v31, s24, v72
	v_mov_b32_e32 v30, v67
	v_cvt_pk_fp8_f32 v30, v35, v31
	v_pk_mul_f32 v[32:33], v[32:33], s[4:5] op_sel_hi:[1,0]
	s_waitcnt vmcnt(22)
	v_pk_mul_f32 v[26:27], v[26:27], s[4:5] op_sel_hi:[1,0]
	v_med3_f32 v31, v32, s24, v72
	v_med3_f32 v32, v33, s24, v72
	v_cvt_pk_fp8_f32 v30, v31, v32 op_sel:[0,0,1]
	v_med3_f32 v31, v26, s24, v72
	v_med3_f32 v27, v27, s24, v72
	v_mov_b32_e32 v26, v67
	v_cvt_pk_fp8_f32 v26, v31, v27
	v_pk_mul_f32 v[28:29], v[28:29], s[4:5] op_sel_hi:[1,0]
	s_waitcnt vmcnt(21)
	v_pk_mul_f32 v[22:23], v[22:23], s[4:5] op_sel_hi:[1,0]
	v_med3_f32 v27, v28, s24, v72
	v_med3_f32 v28, v29, s24, v72
	v_cvt_pk_fp8_f32 v26, v27, v28 op_sel:[0,0,1]
	v_med3_f32 v27, v22, s24, v72
	v_med3_f32 v23, v23, s24, v72
	v_mov_b32_e32 v22, v67
	v_cvt_pk_fp8_f32 v22, v27, v23
	v_pk_mul_f32 v[24:25], v[24:25], s[4:5] op_sel_hi:[1,0]
	s_waitcnt vmcnt(20)
	v_pk_mul_f32 v[18:19], v[18:19], s[4:5] op_sel_hi:[1,0]
	v_med3_f32 v23, v24, s24, v72
	v_med3_f32 v24, v25, s24, v72
	v_cvt_pk_fp8_f32 v22, v23, v24 op_sel:[0,0,1]
	v_med3_f32 v23, v18, s24, v72
	v_med3_f32 v19, v19, s24, v72
	v_mov_b32_e32 v18, v67
	v_cvt_pk_fp8_f32 v18, v23, v19
	v_pk_mul_f32 v[20:21], v[20:21], s[4:5] op_sel_hi:[1,0]
	s_waitcnt vmcnt(19)
	v_pk_mul_f32 v[14:15], v[14:15], s[4:5] op_sel_hi:[1,0]
	v_med3_f32 v19, v20, s24, v72
	v_med3_f32 v20, v21, s24, v72
	v_cvt_pk_fp8_f32 v18, v19, v20 op_sel:[0,0,1]
	v_med3_f32 v19, v14, s24, v72
	v_med3_f32 v15, v15, s24, v72
	v_mov_b32_e32 v14, v67
	v_cvt_pk_fp8_f32 v14, v19, v15
	v_pk_mul_f32 v[16:17], v[16:17], s[4:5] op_sel_hi:[1,0]
	s_waitcnt vmcnt(18)
	v_pk_mul_f32 v[10:11], v[10:11], s[4:5] op_sel_hi:[1,0]
	v_med3_f32 v15, v16, s24, v72
	v_med3_f32 v16, v17, s24, v72
	v_cvt_pk_fp8_f32 v14, v15, v16 op_sel:[0,0,1]
	v_med3_f32 v15, v10, s24, v72
	v_med3_f32 v11, v11, s24, v72
	v_mov_b32_e32 v10, v67
	v_cvt_pk_fp8_f32 v10, v15, v11
	v_pk_mul_f32 v[12:13], v[12:13], s[4:5] op_sel_hi:[1,0]
	s_waitcnt vmcnt(17)
	v_pk_mul_f32 v[6:7], v[6:7], s[4:5] op_sel_hi:[1,0]
	v_med3_f32 v11, v12, s24, v72
	v_med3_f32 v12, v13, s24, v72
	v_cvt_pk_fp8_f32 v10, v11, v12 op_sel:[0,0,1]
	v_med3_f32 v11, v6, s24, v72
	v_med3_f32 v7, v7, s24, v72
	v_mov_b32_e32 v6, v67
	v_cvt_pk_fp8_f32 v6, v11, v7
	v_pk_mul_f32 v[8:9], v[8:9], s[4:5] op_sel_hi:[1,0]
	s_waitcnt vmcnt(16)
; template <int MODE> __device__ __forceinline__ int drow(int n) {
;     if (MODE == 1) { const int h = n / 192, nl = n - h * 192; return nl < 128 ? n : h * 192 + 128 + ((nl - 128) & 31) * 2 + ((nl - 128) >> 5); }
;     if (MODE == 2) { return n < FF ? ((n >> 7) * 256 + (n & 127)) : (((n - FF) >> 7) * 256 + 128 + ((n - FF) & 127)); }
; template <int MODE> __device__ __forceinline__ void cv_finish(const f32x4 (&tv)[16], int K, int nblk, unsigned char* WT, int item, int lane) {
;     ...
;     unsigned O[4][4];
; #pragma unroll
;     for (int q = 0; q < 4; ++q) { const unsigned a = D[4 * q], b = D[4 * q + 1], c = D[4 * q + 2], d = D[4 * q + 3];
;         const unsigned t0 = __builtin_amdgcn_perm(b, a, 0x05010400u), t1 = __builtin_amdgcn_perm(b, a, 0x07030602u), u0 = __builtin_amdgcn_perm(d, c, 0x05010400u), u1 = __builtin_amdgcn_perm(d, c, 0x07030602u);
;         O[0][q] = __builtin_amdgcn_perm(u0, t0, 0x05040100u); O[1][q] = __builtin_amdgcn_perm(u0, t0, 0x07060302u); O[2][q] = __builtin_amdgcn_perm(u1, t1, 0x05040100u); O[3][q] = __builtin_amdgcn_perm(u1, t1, 0x07060302u); }
; #pragma unroll
;     for (int j = 0; j < 4; ++j) { u32x4 o; o.x = O[j][0]; o.y = O[j][1]; o.z = O[j][2]; o.w = O[j][3];
;         __builtin_nontemporal_store(o, (u32x4*)(WT + (size_t)drow<MODE>(n0 + j) * K + k0)); }
; }
	v_pk_mul_f32 v[2:3], v[2:3], s[4:5] op_sel_hi:[1,0]
	v_med3_f32 v7, v8, s24, v72
	v_med3_f32 v8, v9, s24, v72
	v_cvt_pk_fp8_f32 v6, v7, v8 op_sel:[0,0,1]
	v_med3_f32 v2, v2, s24, v72
	v_med3_f32 v3, v3, s24, v72
	v_mov_b32_e32 v7, v67
	v_cvt_pk_fp8_f32 v7, v2, v3
	v_pk_mul_f32 v[2:3], v[4:5], s[4:5] op_sel_hi:[1,0]
	v_ashrrev_i32_e32 v71, 31, v70
	v_med3_f32 v2, v2, s24, v72
	v_med3_f32 v3, v3, s24, v72
	v_cvt_pk_fp8_f32 v7, v2, v3 op_sel:[0,0,1]
	v_perm_b32 v5, v58, v62, s25
	v_perm_b32 v8, v50, v54, s25
	v_perm_b32 v9, v42, v46, s25
	v_perm_b32 v11, v34, v38, s25
	v_perm_b32 v12, v26, v30, s25
	v_perm_b32 v13, v18, v22, s25
	v_perm_b32 v15, v10, v14, s25
	v_perm_b32 v16, v7, v6, s25
	v_lshl_add_u64 v[2:3], s[8:9], 0, v[68:69]
	v_lshlrev_b64 v[20:21], 11, v[70:71]
	v_add_u32_e32 v4, 1, v75
	v_perm_b32 v76, v8, v5, s27
	v_perm_b32 v77, v11, v9, s27
	v_perm_b32 v78, v13, v12, s27
	v_perm_b32 v79, v16, v15, s27
	v_lshl_add_u64 v[20:21], v[2:3], 0, v[20:21]
	v_cmp_lt_i32_e32 vcc, s36, v4
	v_and_b32_e32 v17, 0x7d, v4
	global_store_dwordx4 v[20:21], v[76:79], off nt
	s_and_saveexec_b64 s[10:11], vcc
	s_xor_b64 s[10:11], exec, s[10:11]
	v_add_u32_e32 v4, 0x7ffff002, v74
	v_and_b32_e32 v4, 0x7fffff00, v4
	v_or3_b32 v4, v17, v4, s37
	s_andn2_saveexec_b64 s[10:11], s[10:11]
	v_add_u32_e32 v4, 2, v74
	v_and_or_b32 v4, v4, s38, v17
	s_or_b64 exec, exec, s[10:11]
	v_perm_b32 v68, v8, v5, s28
	v_ashrrev_i32_e32 v5, 31, v4
	v_lshlrev_b64 v[4:5], 11, v[4:5]
	v_perm_b32 v69, v11, v9, s28
	v_perm_b32 v70, v13, v12, s28
	v_perm_b32 v71, v16, v15, s28
	v_lshl_add_u64 v[4:5], v[2:3], 0, v[4:5]
	global_store_dwordx4 v[4:5], v[68:71], off nt
	v_add_u32_e32 v4, 2, v75
	v_cmp_lt_i32_e32 vcc, s36, v4
	v_and_b32_e32 v5, 0x7e, v4
	s_and_saveexec_b64 s[10:11], vcc
	s_xor_b64 s[10:11], exec, s[10:11]
	v_add_u32_e32 v4, 0x7ffff004, v74
	v_and_b32_e32 v4, 0x7fffff00, v4
	v_or3_b32 v4, v5, v4, s37
	s_andn2_saveexec_b64 s[10:11], s[10:11]
	v_add_u32_e32 v4, 4, v74
	v_and_or_b32 v4, v4, s38, v5
	s_or_b64 exec, exec, s[10:11]
	v_ashrrev_i32_e32 v5, 31, v4
	v_perm_b32 v8, v58, v62, s26
	v_perm_b32 v9, v50, v54, s26
	v_perm_b32 v11, v42, v46, s26
	v_perm_b32 v12, v34, v38, s26
	v_perm_b32 v13, v26, v30, s26
	v_perm_b32 v15, v18, v22, s26
	v_perm_b32 v10, v10, v14, s26
	v_perm_b32 v6, v7, v6, s26
	v_lshlrev_b64 v[4:5], 11, v[4:5]
	v_perm_b32 v16, v9, v8, s27
	v_perm_b32 v17, v12, v11, s27
	v_perm_b32 v18, v15, v13, s27
	v_perm_b32 v19, v6, v10, s27
	v_lshl_add_u64 v[4:5], v[2:3], 0, v[4:5]
	global_store_dwordx4 v[4:5], v[16:19], off nt
	v_add_u32_e32 v4, 3, v75
	v_cmp_lt_i32_e32 vcc, s36, v4
	v_and_b32_e32 v5, 0x7f, v4
	s_and_saveexec_b64 s[10:11], vcc
	s_xor_b64 s[10:11], exec, s[10:11]
	v_add_u32_e32 v4, 0x7ffff006, v74
	v_and_b32_e32 v4, 0x7fffff00, v4
	v_or3_b32 v4, v5, v4, s37
	s_andn2_saveexec_b64 s[10:11], s[10:11]
	v_add_u32_e32 v4, 6, v74
	v_and_or_b32 v4, v4, s38, v5
	s_or_b64 exec, exec, s[10:11]
	v_ashrrev_i32_e32 v5, 31, v4
	v_lshlrev_b64 v[4:5], 11, v[4:5]
	v_perm_b32 v16, v9, v8, s28
	v_perm_b32 v17, v12, v11, s28
	v_perm_b32 v18, v15, v13, s28
	v_perm_b32 v19, v6, v10, s28
	v_lshl_add_u64 v[2:3], v[2:3], 0, v[4:5]
	global_store_dwordx4 v[2:3], v[16:19], off nt
	v_cmp_lt_i32_e32 vcc, s36, v129
	s_and_saveexec_b64 s[10:11], vcc
	s_xor_b64 s[10:11], exec, s[10:11]
	v_add_u32_e32 v150, 0x7ffff000, v128
	v_and_b32_e32 v150, 0x7fffff00, v150
	v_or3_b32 v150, v151, v150, s37
	s_andn2_saveexec_b64 s[10:11], s[10:11]
	v_and_or_b32 v150, v128, s38, v151
	s_or_b64 exec, exec, s[10:11]
	s_waitcnt vmcnt(19)
	v_pk_mul_f32 v[144:145], v[144:145], s[4:5] op_sel_hi:[1,0]
	v_pk_mul_f32 v[146:147], v[146:147], s[4:5] op_sel_hi:[1,0]
	v_med3_f32 v151, v144, s24, v72
	v_med3_f32 v145, v145, s24, v72
	v_mov_b32_e32 v144, v67
	v_cvt_pk_fp8_f32 v144, v151, v145
	v_med3_f32 v145, v146, s24, v72
	v_med3_f32 v146, v147, s24, v72
	s_waitcnt vmcnt(18)
	v_pk_mul_f32 v[140:141], v[140:141], s[4:5] op_sel_hi:[1,0]
	v_cvt_pk_fp8_f32 v144, v145, v146 op_sel:[0,0,1]
	v_med3_f32 v145, v140, s24, v72
	v_med3_f32 v141, v141, s24, v72
	v_mov_b32_e32 v140, v67
	v_cvt_pk_fp8_f32 v140, v145, v141
	v_pk_mul_f32 v[142:143], v[142:143], s[4:5] op_sel_hi:[1,0]
	s_waitcnt vmcnt(17)
	v_pk_mul_f32 v[136:137], v[136:137], s[4:5] op_sel_hi:[1,0]
	v_med3_f32 v141, v142, s24, v72
	v_med3_f32 v142, v143, s24, v72
	v_cvt_pk_fp8_f32 v140, v141, v142 op_sel:[0,0,1]
	v_med3_f32 v141, v136, s24, v72
	v_med3_f32 v137, v137, s24, v72
	v_mov_b32_e32 v136, v67
	v_cvt_pk_fp8_f32 v136, v141, v137
	v_pk_mul_f32 v[138:139], v[138:139], s[4:5] op_sel_hi:[1,0]
	s_waitcnt vmcnt(16)
	v_pk_mul_f32 v[132:133], v[132:133], s[4:5] op_sel_hi:[1,0]
	v_med3_f32 v137, v138, s24, v72
	v_med3_f32 v138, v139, s24, v72
	v_cvt_pk_fp8_f32 v136, v137, v138 op_sel:[0,0,1]
	v_med3_f32 v137, v132, s24, v72
	v_med3_f32 v133, v133, s24, v72
	v_mov_b32_e32 v132, v67
	v_cvt_pk_fp8_f32 v132, v137, v133
	v_pk_mul_f32 v[134:135], v[134:135], s[4:5] op_sel_hi:[1,0]
	s_waitcnt vmcnt(15)
	v_pk_mul_f32 v[124:125], v[124:125], s[4:5] op_sel_hi:[1,0]
	v_med3_f32 v133, v134, s24, v72
	v_med3_f32 v134, v135, s24, v72
	v_cvt_pk_fp8_f32 v132, v133, v134 op_sel:[0,0,1]
	v_med3_f32 v133, v124, s24, v72
	v_med3_f32 v125, v125, s24, v72
	v_mov_b32_e32 v124, v67
	v_cvt_pk_fp8_f32 v124, v133, v125
	v_pk_mul_f32 v[126:127], v[126:127], s[4:5] op_sel_hi:[1,0]
	s_waitcnt vmcnt(14)
	v_pk_mul_f32 v[120:121], v[120:121], s[4:5] op_sel_hi:[1,0]
	v_med3_f32 v125, v126, s24, v72
	v_med3_f32 v126, v127, s24, v72
	v_cvt_pk_fp8_f32 v124, v125, v126 op_sel:[0,0,1]
	v_med3_f32 v125, v120, s24, v72
	v_med3_f32 v121, v121, s24, v72
	v_mov_b32_e32 v120, v67
	v_cvt_pk_fp8_f32 v120, v125, v121
	v_pk_mul_f32 v[122:123], v[122:123], s[4:5] op_sel_hi:[1,0]
	s_waitcnt vmcnt(13)
; template <int MODE> __device__ __forceinline__ int drow(int n) {
;     if (MODE == 1) { const int h = n / 192, nl = n - h * 192; return nl < 128 ? n : h * 192 + 128 + ((nl - 128) & 31) * 2 + ((nl - 128) >> 5); }
;     if (MODE == 2) { return n < FF ? ((n >> 7) * 256 + (n & 127)) : (((n - FF) >> 7) * 256 + 128 + ((n - FF) & 127)); }
; template <int MODE> __device__ __forceinline__ void cv_finish(const f32x4 (&tv)[16], int K, int nblk, unsigned char* WT, int item, int lane) {
;     ...
;     for (int i = 0; i < 16; ++i) { const f32x2 a = (f32x2){tv[i].x, tv[i].y} * (f32x2){1024.f, 1024.f}, b = (f32x2){tv[i].z, tv[i].w} * (f32x2){1024.f, 1024.f};
;         D[i] = pk4_fp8(a.x, a.y, b.x, b.y); }
;     unsigned O[4][4];
; #pragma unroll
;     for (int q = 0; q < 4; ++q) { const unsigned a = D[4 * q], b = D[4 * q + 1], c = D[4 * q + 2], d = D[4 * q + 3];
;         const unsigned t0 = __builtin_amdgcn_perm(b, a, 0x05010400u), t1 = __builtin_amdgcn_perm(b, a, 0x07030602u), u0 = __builtin_amdgcn_perm(d, c, 0x05010400u), u1 = __builtin_amdgcn_perm(d, c, 0x07030602u);
;         O[0][q] = __builtin_amdgcn_perm(u0, t0, 0x05040100u); O[1][q] = __builtin_amdgcn_perm(u0, t0, 0x07060302u); O[2][q] = __builtin_amdgcn_perm(u1, t1, 0x05040100u); O[3][q] = __builtin_amdgcn_perm(u1, t1, 0x07060302u); }
; #pragma unroll
;     for (int j = 0; j < 4; ++j) { u32x4 o; o.x = O[j][0]; o.y = O[j][1]; o.z = O[j][2]; o.w = O[j][3];
;         __builtin_nontemporal_store(o, (u32x4*)(WT + (size_t)drow<MODE>(n0 + j) * K + k0)); }
; }
	v_pk_mul_f32 v[116:117], v[116:117], s[4:5] op_sel_hi:[1,0]
	v_med3_f32 v121, v122, s24, v72
	v_med3_f32 v122, v123, s24, v72
	v_cvt_pk_fp8_f32 v120, v121, v122 op_sel:[0,0,1]
	v_med3_f32 v121, v116, s24, v72
	v_med3_f32 v117, v117, s24, v72
	v_mov_b32_e32 v116, v67
	v_cvt_pk_fp8_f32 v116, v121, v117
	v_pk_mul_f32 v[118:119], v[118:119], s[4:5] op_sel_hi:[1,0]
	s_waitcnt vmcnt(12)
	v_pk_mul_f32 v[112:113], v[112:113], s[4:5] op_sel_hi:[1,0]
	v_med3_f32 v117, v118, s24, v72
	v_med3_f32 v118, v119, s24, v72
	v_cvt_pk_fp8_f32 v116, v117, v118 op_sel:[0,0,1]
	v_med3_f32 v117, v112, s24, v72
	v_med3_f32 v113, v113, s24, v72
	v_mov_b32_e32 v112, v67
	v_cvt_pk_fp8_f32 v112, v117, v113
	v_pk_mul_f32 v[114:115], v[114:115], s[4:5] op_sel_hi:[1,0]
	s_waitcnt vmcnt(11)
	v_pk_mul_f32 v[108:109], v[108:109], s[4:5] op_sel_hi:[1,0]
	v_med3_f32 v113, v114, s24, v72
	v_med3_f32 v114, v115, s24, v72
	v_cvt_pk_fp8_f32 v112, v113, v114 op_sel:[0,0,1]
	v_med3_f32 v113, v108, s24, v72
	v_med3_f32 v109, v109, s24, v72
	v_mov_b32_e32 v108, v67
	v_cvt_pk_fp8_f32 v108, v113, v109
	v_pk_mul_f32 v[110:111], v[110:111], s[4:5] op_sel_hi:[1,0]
	s_waitcnt vmcnt(10)
	v_pk_mul_f32 v[104:105], v[104:105], s[4:5] op_sel_hi:[1,0]
	v_med3_f32 v109, v110, s24, v72
	v_med3_f32 v110, v111, s24, v72
	v_cvt_pk_fp8_f32 v108, v109, v110 op_sel:[0,0,1]
	v_med3_f32 v109, v104, s24, v72
	v_med3_f32 v105, v105, s24, v72
	v_mov_b32_e32 v104, v67
	v_cvt_pk_fp8_f32 v104, v109, v105
	v_pk_mul_f32 v[106:107], v[106:107], s[4:5] op_sel_hi:[1,0]
	s_waitcnt vmcnt(9)
	v_pk_mul_f32 v[100:101], v[100:101], s[4:5] op_sel_hi:[1,0]
	v_med3_f32 v105, v106, s24, v72
	v_med3_f32 v106, v107, s24, v72
	v_cvt_pk_fp8_f32 v104, v105, v106 op_sel:[0,0,1]
	v_med3_f32 v105, v100, s24, v72
	v_med3_f32 v101, v101, s24, v72
	v_mov_b32_e32 v100, v67
	v_cvt_pk_fp8_f32 v100, v105, v101
	v_pk_mul_f32 v[102:103], v[102:103], s[4:5] op_sel_hi:[1,0]
	s_waitcnt vmcnt(8)
	v_pk_mul_f32 v[96:97], v[96:97], s[4:5] op_sel_hi:[1,0]
	v_med3_f32 v101, v102, s24, v72
	v_med3_f32 v102, v103, s24, v72
	v_cvt_pk_fp8_f32 v100, v101, v102 op_sel:[0,0,1]
	v_med3_f32 v101, v96, s24, v72
	v_med3_f32 v97, v97, s24, v72
	v_mov_b32_e32 v96, v67
	v_cvt_pk_fp8_f32 v96, v101, v97
	v_pk_mul_f32 v[98:99], v[98:99], s[4:5] op_sel_hi:[1,0]
	s_waitcnt vmcnt(7)
	v_pk_mul_f32 v[92:93], v[92:93], s[4:5] op_sel_hi:[1,0]
	v_med3_f32 v97, v98, s24, v72
	v_med3_f32 v98, v99, s24, v72
	v_cvt_pk_fp8_f32 v96, v97, v98 op_sel:[0,0,1]
	v_med3_f32 v97, v92, s24, v72
	v_med3_f32 v93, v93, s24, v72
	v_mov_b32_e32 v92, v67
	v_cvt_pk_fp8_f32 v92, v97, v93
	v_pk_mul_f32 v[94:95], v[94:95], s[4:5] op_sel_hi:[1,0]
	s_waitcnt vmcnt(6)
	v_pk_mul_f32 v[88:89], v[88:89], s[4:5] op_sel_hi:[1,0]
	v_med3_f32 v93, v94, s24, v72
	v_med3_f32 v94, v95, s24, v72
	v_cvt_pk_fp8_f32 v92, v93, v94 op_sel:[0,0,1]
	v_med3_f32 v93, v88, s24, v72
	v_med3_f32 v89, v89, s24, v72
	v_mov_b32_e32 v88, v67
	v_cvt_pk_fp8_f32 v88, v93, v89
	v_pk_mul_f32 v[90:91], v[90:91], s[4:5] op_sel_hi:[1,0]
	s_waitcnt vmcnt(5)
	v_pk_mul_f32 v[84:85], v[84:85], s[4:5] op_sel_hi:[1,0]
	v_med3_f32 v89, v90, s24, v72
	v_med3_f32 v90, v91, s24, v72
	v_cvt_pk_fp8_f32 v88, v89, v90 op_sel:[0,0,1]
	v_med3_f32 v89, v84, s24, v72
	v_med3_f32 v85, v85, s24, v72
	v_mov_b32_e32 v84, v67
	v_cvt_pk_fp8_f32 v84, v89, v85
	v_pk_mul_f32 v[86:87], v[86:87], s[4:5] op_sel_hi:[1,0]
	s_waitcnt vmcnt(4)
	v_pk_mul_f32 v[80:81], v[80:81], s[4:5] op_sel_hi:[1,0]
	v_med3_f32 v85, v86, s24, v72
	v_med3_f32 v86, v87, s24, v72
	v_cvt_pk_fp8_f32 v84, v85, v86 op_sel:[0,0,1]
	v_med3_f32 v80, v80, s24, v72
	v_med3_f32 v81, v81, s24, v72
	v_mov_b32_e32 v85, v67
	v_cvt_pk_fp8_f32 v85, v80, v81
	v_pk_mul_f32 v[80:81], v[82:83], s[4:5] op_sel_hi:[1,0]
	v_ashrrev_i32_e32 v151, 31, v150
	v_med3_f32 v80, v80, s24, v72
	v_med3_f32 v81, v81, s24, v72
	v_cvt_pk_fp8_f32 v85, v80, v81 op_sel:[0,0,1]
	v_perm_b32 v83, v140, v144, s25
	v_perm_b32 v86, v132, v136, s25
	v_perm_b32 v87, v120, v124, s25
	v_perm_b32 v89, v112, v116, s25
	v_perm_b32 v90, v104, v108, s25
	v_perm_b32 v91, v96, v100, s25
	v_perm_b32 v93, v88, v92, s25
	v_perm_b32 v94, v85, v84, s25
	v_lshl_add_u64 v[80:81], s[8:9], 0, v[148:149]
	v_lshlrev_b64 v[98:99], 11, v[150:151]
	v_add_u32_e32 v82, 1, v129
	v_perm_b32 v152, v86, v83, s27
	v_perm_b32 v153, v89, v87, s27
	v_perm_b32 v154, v91, v90, s27
	v_perm_b32 v155, v94, v93, s27
	v_lshl_add_u64 v[98:99], v[80:81], 0, v[98:99]
	v_cmp_lt_i32_e32 vcc, s36, v82
	v_and_b32_e32 v95, 0x7d, v82
	global_store_dwordx4 v[98:99], v[152:155], off nt
	s_and_saveexec_b64 s[10:11], vcc
	s_xor_b64 s[10:11], exec, s[10:11]
	v_add_u32_e32 v82, 0x7ffff002, v128
	v_and_b32_e32 v82, 0x7fffff00, v82
	v_or3_b32 v82, v95, v82, s37
	s_andn2_saveexec_b64 s[10:11], s[10:11]
	v_add_u32_e32 v82, 2, v128
	v_and_or_b32 v82, v82, s38, v95
	s_or_b64 exec, exec, s[10:11]
	v_perm_b32 v148, v86, v83, s28
	v_ashrrev_i32_e32 v83, 31, v82
	v_lshlrev_b64 v[82:83], 11, v[82:83]
	v_perm_b32 v149, v89, v87, s28
	v_perm_b32 v150, v91, v90, s28
	v_perm_b32 v151, v94, v93, s28
	v_lshl_add_u64 v[82:83], v[80:81], 0, v[82:83]
	global_store_dwordx4 v[82:83], v[148:151], off nt
	v_add_u32_e32 v82, 2, v129
	v_cmp_lt_i32_e32 vcc, s36, v82
	v_and_b32_e32 v83, 0x7e, v82
	s_and_saveexec_b64 s[10:11], vcc
	s_xor_b64 s[10:11], exec, s[10:11]
	v_add_u32_e32 v82, 0x7ffff004, v128
	v_and_b32_e32 v82, 0x7fffff00, v82
	v_or3_b32 v82, v83, v82, s37
	s_andn2_saveexec_b64 s[10:11], s[10:11]
	v_add_u32_e32 v82, 4, v128
	v_and_or_b32 v82, v82, s38, v83
	s_or_b64 exec, exec, s[10:11]
	v_ashrrev_i32_e32 v83, 31, v82
	v_perm_b32 v86, v140, v144, s26
	v_perm_b32 v87, v132, v136, s26
	v_perm_b32 v89, v120, v124, s26
	v_perm_b32 v90, v112, v116, s26
	v_perm_b32 v91, v104, v108, s26
	v_perm_b32 v93, v96, v100, s26
	v_perm_b32 v88, v88, v92, s26
	v_perm_b32 v84, v85, v84, s26
	v_lshlrev_b64 v[82:83], 11, v[82:83]
	v_perm_b32 v94, v87, v86, s27
	v_perm_b32 v95, v90, v89, s27
	v_perm_b32 v96, v93, v91, s27
	v_perm_b32 v97, v84, v88, s27
	v_lshl_add_u64 v[82:83], v[80:81], 0, v[82:83]
	global_store_dwordx4 v[82:83], v[94:97], off nt
	v_add_u32_e32 v82, 3, v129
	v_cmp_lt_i32_e32 vcc, s36, v82
	v_and_b32_e32 v83, 0x7f, v82
	s_and_saveexec_b64 s[10:11], vcc
	s_xor_b64 s[10:11], exec, s[10:11]
	v_add_u32_e32 v82, 0x7ffff006, v128
	v_and_b32_e32 v82, 0x7fffff00, v82
	v_or3_b32 v82, v83, v82, s37
	s_andn2_saveexec_b64 s[10:11], s[10:11]
	v_add_u32_e32 v82, 6, v128
	v_and_or_b32 v82, v82, s38, v83
	s_or_b64 exec, exec, s[10:11]
	v_ashrrev_i32_e32 v83, 31, v82
	v_lshlrev_b64 v[82:83], 11, v[82:83]
	v_perm_b32 v94, v87, v86, s28
	v_perm_b32 v95, v90, v89, s28
	v_perm_b32 v96, v93, v91, s28
	v_perm_b32 v97, v84, v88, s28
	v_lshl_add_u64 v[80:81], v[80:81], 0, v[82:83]
	global_store_dwordx4 v[80:81], v[94:97], off nt
	s_cmpk_eq_i32 s40, 0x200
	s_cbranch_scc0 .LBB0_766
	s_branch .LBB0_752

; __device__ __forceinline__ void cv_load(const float* W, int N, int nblk, int item, int lane, f32x4 (&tv)[16]) {
;     const int kb = item / nblk, nb = item - kb * nblk; const float* p = W + (size_t)(64 * kb + 16 * (lane >> 4)) * N + 64 * nb + 4 * (lane & 15);
; #pragma unroll
;     for (int i = 0; i < 16; ++i) tv[i] = __builtin_nontemporal_load((const f32x4*)(p + (size_t)i * N));
; }
; template <int MODE> __device__ __forceinline__ void cv_run4(const float* W, int K, int N, unsigned char* WT, int item0, int lane) {
;     const int nblk = N / 64; f32x4 ta[16];
; #pragma unroll 1
;     for (int j = 0; j < 4; ++j) { cv_load(W, N, nblk, item0 + j, lane, ta); cv_finish<MODE>(ta, K, nblk, WT, item0 + j, lane); }
.LBB0_979:
	s_lshr_b32 s49, s4, 5
	s_lshl_b32 s50, s49, 11
	v_mov_b32_e32 v3, v69
	v_lshl_or_b32 v2, s49, 6, v1
	s_sub_i32 s49, s47, s50
	s_waitcnt lgkmcnt(1)
	v_subrev_u32_e32 v8, s50, v4
	s_waitcnt lgkmcnt(0)
	v_lshlrev_b64 v[6:7], 13, v[2:3]
	s_add_i32 s50, s48, s49
	v_lshl_add_u64 v[6:7], s[8:9], 0, v[6:7]
	s_ashr_i32 s51, s50, 31
	v_lshl_add_u64 v[6:7], s[50:51], 2, v[6:7]
	v_lshl_add_u64 v[16:17], v[6:7], 0, v[68:69]
	v_add_co_u32_e32 v18, vcc, s17, v16
	v_add_u32_e32 v8, s48, v8
	s_nop 0
	v_addc_co_u32_e32 v19, vcc, 0, v17, vcc
	v_add_co_u32_e32 v20, vcc, s18, v16
	v_ashrrev_i32_e32 v9, 31, v8
	s_nop 0
	v_addc_co_u32_e32 v21, vcc, 0, v17, vcc
	v_add_co_u32_e32 v22, vcc, s19, v16
	v_add_u32_e32 v10, 1, v8
	s_nop 0
	v_addc_co_u32_e32 v23, vcc, 0, v17, vcc
	v_add_co_u32_e32 v24, vcc, s20, v16
	s_waitcnt vmcnt(2)
	v_add_u32_e32 v12, 2, v8
	v_addc_co_u32_e32 v25, vcc, 0, v17, vcc
	v_add_co_u32_e32 v26, vcc, s21, v16
	v_add_u32_e32 v14, 3, v8
	s_nop 0
	v_addc_co_u32_e32 v27, vcc, 0, v17, vcc
	v_add_co_u32_e32 v30, vcc, s22, v16
	v_lshl_add_u64 v[2:3], s[10:11], 0, v[2:3]
	s_nop 0
	v_addc_co_u32_e32 v31, vcc, 0, v17, vcc
	v_add_co_u32_e32 v34, vcc, s23, v16
	v_lshlrev_b64 v[8:9], 11, v[8:9]
	s_nop 0
	v_addc_co_u32_e32 v35, vcc, 0, v17, vcc
	v_add_co_u32_e32 v38, vcc, s24, v16
	v_ashrrev_i32_e32 v11, 31, v10
	s_nop 0
	v_addc_co_u32_e32 v39, vcc, 0, v17, vcc
	v_add_co_u32_e32 v42, vcc, s25, v16
	v_ashrrev_i32_e32 v13, 31, v12
	s_nop 0
	v_addc_co_u32_e32 v43, vcc, 0, v17, vcc
	v_add_co_u32_e32 v46, vcc, s26, v16
	v_ashrrev_i32_e32 v15, 31, v14
	s_nop 0
	v_addc_co_u32_e32 v47, vcc, 0, v17, vcc
	v_add_co_u32_e32 v50, vcc, s27, v16
	v_lshl_add_u64 v[76:77], v[2:3], 0, v[8:9]
	s_nop 0
	v_addc_co_u32_e32 v51, vcc, 0, v17, vcc
	v_add_co_u32_e32 v54, vcc, s28, v16
	v_lshlrev_b64 v[10:11], 11, v[10:11]
	s_nop 0
	v_addc_co_u32_e32 v55, vcc, 0, v17, vcc
	v_add_co_u32_e32 v58, vcc, s29, v16
	v_lshlrev_b64 v[12:13], 11, v[12:13]
	s_nop 0
	v_addc_co_u32_e32 v59, vcc, 0, v17, vcc
	v_add_co_u32_e32 v62, vcc, s30, v16
	v_lshlrev_b64 v[14:15], 11, v[14:15]
	s_nop 0
	v_addc_co_u32_e32 v63, vcc, 0, v17, vcc
	v_add_co_u32_e32 v70, vcc, s31, v16
	global_load_dwordx4 v[6:9], v[16:17], off nt
	s_nop 0
	v_addc_co_u32_e32 v71, vcc, 0, v17, vcc
	v_lshl_add_u64 v[78:79], v[2:3], 0, v[10:11]
	v_lshl_add_u64 v[80:81], v[2:3], 0, v[12:13]
	v_lshl_add_u64 v[2:3], v[2:3], 0, v[14:15]
	global_load_dwordx4 v[10:13], v[18:19], off nt
	global_load_dwordx4 v[14:17], v[20:21], off nt
	s_nop 0
	global_load_dwordx4 v[18:21], v[22:23], off nt
	s_nop 0
	global_load_dwordx4 v[22:25], v[24:25], off nt
	s_nop 0
	global_load_dwordx4 v[26:29], v[26:27], off nt
	s_nop 0
	global_load_dwordx4 v[30:33], v[30:31], off nt
	s_nop 0
	global_load_dwordx4 v[34:37], v[34:35], off nt
	s_nop 0
	global_load_dwordx4 v[38:41], v[38:39], off nt
	s_nop 0
	global_load_dwordx4 v[42:45], v[42:43], off nt
	s_nop 0
	global_load_dwordx4 v[46:49], v[46:47], off nt
	s_nop 0
	global_load_dwordx4 v[50:53], v[50:51], off nt
	s_nop 0
	global_load_dwordx4 v[54:57], v[54:55], off nt
	s_nop 0
	global_load_dwordx4 v[58:61], v[58:59], off nt
	s_nop 0
	global_load_dwordx4 v[62:65], v[62:63], off nt
	s_nop 0
	global_load_dwordx4 v[70:73], v[70:71], off nt
	v_mov_b32_e32 v5, v69
	v_mov_b32_e32 v75, v69
	v_mov_b32_e32 v82, v69
	v_mov_b32_e32 v83, v69
	v_mov_b32_e32 v84, v69
	v_mov_b32_e32 v85, v69
	v_mov_b32_e32 v86, v69
	v_mov_b32_e32 v87, v69
	v_mov_b32_e32 v88, v69
	v_mov_b32_e32 v89, v69
	v_mov_b32_e32 v90, v69
	v_mov_b32_e32 v91, v69
	v_mov_b32_e32 v92, v69
	v_mov_b32_e32 v93, v69
	v_mov_b32_e32 v94, v69
	v_mov_b32_e32 v95, v69
	s_add_i32 s4, s4, 1
	s_add_i32 s48, s48, 64
	s_lshr_b32 s49, s4, 5
	s_lshl_b32 s50, s49, 11
	v_mov_b32_e32 v101, v69
	v_lshl_or_b32 v100, s49, 6, v1
	s_sub_i32 s49, s47, s50
	s_waitcnt lgkmcnt(1)
	v_subrev_u32_e32 v106, s50, v4
	s_waitcnt lgkmcnt(0)
	v_lshlrev_b64 v[104:105], 13, v[100:101]
	s_add_i32 s50, s48, s49
	v_lshl_add_u64 v[104:105], s[8:9], 0, v[104:105]
	s_ashr_i32 s51, s50, 31
	v_lshl_add_u64 v[104:105], s[50:51], 2, v[104:105]
	v_lshl_add_u64 v[114:115], v[104:105], 0, v[68:69]
	v_add_co_u32_e32 v116, vcc, s17, v114
	v_add_u32_e32 v106, s48, v106
	s_nop 0
	v_addc_co_u32_e32 v117, vcc, 0, v115, vcc
	v_add_co_u32_e32 v118, vcc, s18, v114
	v_ashrrev_i32_e32 v107, 31, v106
	s_nop 0
	v_addc_co_u32_e32 v119, vcc, 0, v115, vcc
	v_add_co_u32_e32 v120, vcc, s19, v114
	v_add_u32_e32 v108, 1, v106
	s_nop 0
	v_addc_co_u32_e32 v121, vcc, 0, v115, vcc
	v_add_co_u32_e32 v122, vcc, s20, v114
	s_waitcnt vmcnt(2)
; __device__ __forceinline__ void cv_load(const float* W, int N, int nblk, int item, int lane, f32x4 (&tv)[16]) {
;     const int kb = item / nblk, nb = item - kb * nblk; const float* p = W + (size_t)(64 * kb + 16 * (lane >> 4)) * N + 64 * nb + 4 * (lane & 15);
; #pragma unroll
;     for (int i = 0; i < 16; ++i) tv[i] = __builtin_nontemporal_load((const f32x4*)(p + (size_t)i * N));
; }
; template <int MODE> __device__ __forceinline__ void cv_finish(const f32x4 (&tv)[16], int K, int nblk, unsigned char* WT, int item, int lane) {
;     const int kb = item / nblk, nb = item - kb * nblk, k0 = 64 * kb + 16 * (lane >> 4), n0 = 64 * nb + 4 * (lane & 15);
;     unsigned D[16];
; #pragma unroll
;     for (int i = 0; i < 16; ++i) { const f32x2 a = (f32x2){tv[i].x, tv[i].y} * (f32x2){1024.f, 1024.f}, b = (f32x2){tv[i].z, tv[i].w} * (f32x2){1024.f, 1024.f};
;         D[i] = pk4_fp8(a.x, a.y, b.x, b.y); }
	v_add_u32_e32 v110, 2, v106
	v_addc_co_u32_e32 v123, vcc, 0, v115, vcc
	v_add_co_u32_e32 v124, vcc, s21, v114
	v_add_u32_e32 v112, 3, v106
	s_nop 0
	v_addc_co_u32_e32 v125, vcc, 0, v115, vcc
	v_add_co_u32_e32 v128, vcc, s22, v114
	v_lshl_add_u64 v[100:101], s[10:11], 0, v[100:101]
	s_nop 0
	v_addc_co_u32_e32 v129, vcc, 0, v115, vcc
	v_add_co_u32_e32 v132, vcc, s23, v114
	v_lshlrev_b64 v[106:107], 11, v[106:107]
	s_nop 0
	v_addc_co_u32_e32 v133, vcc, 0, v115, vcc
	v_add_co_u32_e32 v136, vcc, s24, v114
	v_ashrrev_i32_e32 v109, 31, v108
	s_nop 0
	v_addc_co_u32_e32 v137, vcc, 0, v115, vcc
	v_add_co_u32_e32 v140, vcc, s25, v114
	v_ashrrev_i32_e32 v111, 31, v110
	s_nop 0
	v_addc_co_u32_e32 v141, vcc, 0, v115, vcc
	v_add_co_u32_e32 v144, vcc, s26, v114
	v_ashrrev_i32_e32 v113, 31, v112
	s_nop 0
	v_addc_co_u32_e32 v145, vcc, 0, v115, vcc
	v_add_co_u32_e32 v148, vcc, s27, v114
	v_lshl_add_u64 v[170:171], v[100:101], 0, v[106:107]
	s_nop 0
	v_addc_co_u32_e32 v149, vcc, 0, v115, vcc
	v_add_co_u32_e32 v152, vcc, s28, v114
	v_lshlrev_b64 v[108:109], 11, v[108:109]
	s_nop 0
	v_addc_co_u32_e32 v153, vcc, 0, v115, vcc
	v_add_co_u32_e32 v156, vcc, s29, v114
	v_lshlrev_b64 v[110:111], 11, v[110:111]
	s_nop 0
	v_addc_co_u32_e32 v157, vcc, 0, v115, vcc
	v_add_co_u32_e32 v160, vcc, s30, v114
	v_lshlrev_b64 v[112:113], 11, v[112:113]
	s_nop 0
	v_addc_co_u32_e32 v161, vcc, 0, v115, vcc
	v_add_co_u32_e32 v164, vcc, s31, v114
	global_load_dwordx4 v[104:107], v[114:115], off nt
	s_nop 0
	v_addc_co_u32_e32 v165, vcc, 0, v115, vcc
	v_lshl_add_u64 v[172:173], v[100:101], 0, v[108:109]
	v_lshl_add_u64 v[174:175], v[100:101], 0, v[110:111]
	v_lshl_add_u64 v[100:101], v[100:101], 0, v[112:113]
	global_load_dwordx4 v[108:111], v[116:117], off nt
	global_load_dwordx4 v[112:115], v[118:119], off nt
	s_nop 0
	global_load_dwordx4 v[116:119], v[120:121], off nt
	s_nop 0
	global_load_dwordx4 v[120:123], v[122:123], off nt
	s_nop 0
	global_load_dwordx4 v[124:127], v[124:125], off nt
	s_nop 0
	global_load_dwordx4 v[128:131], v[128:129], off nt
	s_nop 0
	global_load_dwordx4 v[132:135], v[132:133], off nt
	s_nop 0
	global_load_dwordx4 v[136:139], v[136:137], off nt
	s_nop 0
	global_load_dwordx4 v[140:143], v[140:141], off nt
	s_nop 0
	global_load_dwordx4 v[144:147], v[144:145], off nt
	s_nop 0
	global_load_dwordx4 v[148:151], v[148:149], off nt
	s_nop 0
	global_load_dwordx4 v[152:155], v[152:153], off nt
	s_nop 0
	global_load_dwordx4 v[156:159], v[156:157], off nt
	s_nop 0
	global_load_dwordx4 v[160:163], v[160:161], off nt
	s_nop 0
	global_load_dwordx4 v[164:167], v[164:165], off nt
	v_mov_b32_e32 v103, v69
	v_mov_b32_e32 v169, v69
	v_mov_b32_e32 v102, v69
	v_mov_b32_e32 v177, v69
	v_mov_b32_e32 v168, v69
	v_mov_b32_e32 v179, v69
	v_mov_b32_e32 v176, v69
	v_mov_b32_e32 v181, v69
	v_mov_b32_e32 v178, v69
	v_mov_b32_e32 v183, v69
	v_mov_b32_e32 v180, v69
	v_mov_b32_e32 v185, v69
	v_mov_b32_e32 v182, v69
	v_mov_b32_e32 v187, v69
	v_mov_b32_e32 v184, v69
	v_mov_b32_e32 v189, v69
	s_add_i32 s4, s4, 1
	s_add_i32 s48, s48, 64
	s_cmpk_eq_i32 s48, 0x100
	s_waitcnt vmcnt(31)
	v_pk_mul_f32 v[6:7], v[6:7], s[6:7] op_sel_hi:[1,0]
	s_nop 0
	v_med3_f32 v96, v6, s33, v74
	v_med3_f32 v97, v7, s33, v74
	s_waitcnt vmcnt(30)
	v_pk_mul_f32 v[6:7], v[10:11], s[6:7] op_sel_hi:[1,0]
	s_waitcnt vmcnt(29)
	v_pk_mul_f32 v[10:11], v[14:15], s[6:7] op_sel_hi:[1,0]
	s_waitcnt vmcnt(28)
	v_pk_mul_f32 v[14:15], v[18:19], s[6:7] op_sel_hi:[1,0]
	s_waitcnt vmcnt(27)
	v_pk_mul_f32 v[18:19], v[22:23], s[6:7] op_sel_hi:[1,0]
	s_waitcnt vmcnt(26)
	v_pk_mul_f32 v[22:23], v[26:27], s[6:7] op_sel_hi:[1,0]
	s_waitcnt vmcnt(25)
	v_pk_mul_f32 v[26:27], v[30:31], s[6:7] op_sel_hi:[1,0]
	s_waitcnt vmcnt(24)
	v_pk_mul_f32 v[30:31], v[34:35], s[6:7] op_sel_hi:[1,0]
	s_waitcnt vmcnt(23)
	v_pk_mul_f32 v[34:35], v[38:39], s[6:7] op_sel_hi:[1,0]
	s_waitcnt vmcnt(22)
	v_pk_mul_f32 v[38:39], v[42:43], s[6:7] op_sel_hi:[1,0]
	s_waitcnt vmcnt(21)
	v_pk_mul_f32 v[42:43], v[46:47], s[6:7] op_sel_hi:[1,0]
	s_waitcnt vmcnt(20)
	v_pk_mul_f32 v[46:47], v[50:51], s[6:7] op_sel_hi:[1,0]
	s_waitcnt vmcnt(19)
	v_pk_mul_f32 v[50:51], v[54:55], s[6:7] op_sel_hi:[1,0]
	s_waitcnt vmcnt(18)
	v_pk_mul_f32 v[54:55], v[58:59], s[6:7] op_sel_hi:[1,0]
	s_waitcnt vmcnt(17)
	v_pk_mul_f32 v[58:59], v[62:63], s[6:7] op_sel_hi:[1,0]
	s_waitcnt vmcnt(16)
; template <int MODE> __device__ __forceinline__ void cv_finish(const f32x4 (&tv)[16], int K, int nblk, unsigned char* WT, int item, int lane) {
;     const int kb = item / nblk, nb = item - kb * nblk, k0 = 64 * kb + 16 * (lane >> 4), n0 = 64 * nb + 4 * (lane & 15);
;     unsigned D[16];
; #pragma unroll
;     for (int i = 0; i < 16; ++i) { const f32x2 a = (f32x2){tv[i].x, tv[i].y} * (f32x2){1024.f, 1024.f}, b = (f32x2){tv[i].z, tv[i].w} * (f32x2){1024.f, 1024.f};
;         D[i] = pk4_fp8(a.x, a.y, b.x, b.y); }
;     unsigned O[4][4];
; #pragma unroll
;     for (int q = 0; q < 4; ++q) { const unsigned a = D[4 * q], b = D[4 * q + 1], c = D[4 * q + 2], d = D[4 * q + 3];
;         const unsigned t0 = __builtin_amdgcn_perm(b, a, 0x05010400u), t1 = __builtin_amdgcn_perm(b, a, 0x07030602u), u0 = __builtin_amdgcn_perm(d, c, 0x05010400u), u1 = __builtin_amdgcn_perm(d, c, 0x07030602u);
;         O[0][q] = __builtin_amdgcn_perm(u0, t0, 0x05040100u); O[1][q] = __builtin_amdgcn_perm(u0, t0, 0x07060302u); O[2][q] = __builtin_amdgcn_perm(u1, t1, 0x05040100u); O[3][q] = __builtin_amdgcn_perm(u1, t1, 0x07060302u); }
; #pragma unroll
;     for (int j = 0; j < 4; ++j) { u32x4 o; o.x = O[j][0]; o.y = O[j][1]; o.z = O[j][2]; o.w = O[j][3];
;         __builtin_nontemporal_store(o, (u32x4*)(WT + (size_t)drow<MODE>(n0 + j) * K + k0)); }
; }
	v_pk_mul_f32 v[62:63], v[70:71], s[6:7] op_sel_hi:[1,0]
	v_med3_f32 v6, v6, s33, v74
	v_med3_f32 v7, v7, s33, v74
	v_med3_f32 v10, v10, s33, v74
	v_med3_f32 v11, v11, s33, v74
	v_med3_f32 v14, v14, s33, v74
	v_med3_f32 v15, v15, s33, v74
	v_med3_f32 v18, v18, s33, v74
	v_med3_f32 v19, v19, s33, v74
	v_med3_f32 v22, v22, s33, v74
	v_med3_f32 v23, v23, s33, v74
	v_med3_f32 v26, v26, s33, v74
	v_med3_f32 v27, v27, s33, v74
	v_med3_f32 v30, v30, s33, v74
	v_med3_f32 v31, v31, s33, v74
	v_med3_f32 v34, v34, s33, v74
	v_med3_f32 v35, v35, s33, v74
	v_med3_f32 v38, v38, s33, v74
	v_med3_f32 v39, v39, s33, v74
	v_med3_f32 v42, v42, s33, v74
	v_med3_f32 v43, v43, s33, v74
	v_med3_f32 v46, v46, s33, v74
	v_med3_f32 v47, v47, s33, v74
	v_med3_f32 v50, v50, s33, v74
	v_med3_f32 v51, v51, s33, v74
	v_med3_f32 v54, v54, s33, v74
	v_med3_f32 v55, v55, s33, v74
	v_med3_f32 v58, v58, s33, v74
	v_med3_f32 v59, v59, s33, v74
	v_med3_f32 v62, v62, s33, v74
	v_med3_f32 v63, v63, s33, v74
	v_cvt_pk_fp8_f32 v5, v96, v97
	v_cvt_pk_fp8_f32 v75, v6, v7
	v_cvt_pk_fp8_f32 v82, v10, v11
	v_cvt_pk_fp8_f32 v83, v14, v15
	v_cvt_pk_fp8_f32 v84, v18, v19
	v_cvt_pk_fp8_f32 v85, v22, v23
	v_cvt_pk_fp8_f32 v86, v26, v27
	v_cvt_pk_fp8_f32 v87, v30, v31
	v_cvt_pk_fp8_f32 v88, v34, v35
	v_cvt_pk_fp8_f32 v89, v38, v39
	v_cvt_pk_fp8_f32 v90, v42, v43
	v_cvt_pk_fp8_f32 v91, v46, v47
	v_cvt_pk_fp8_f32 v92, v50, v51
	v_cvt_pk_fp8_f32 v93, v54, v55
	v_cvt_pk_fp8_f32 v94, v58, v59
	v_cvt_pk_fp8_f32 v95, v62, v63
	v_pk_mul_f32 v[8:9], v[8:9], s[6:7] op_sel_hi:[1,0]
	s_nop 0
	v_med3_f32 v98, v8, s33, v74
	v_med3_f32 v99, v9, s33, v74
	v_pk_mul_f32 v[8:9], v[12:13], s[6:7] op_sel_hi:[1,0]
	v_pk_mul_f32 v[12:13], v[16:17], s[6:7] op_sel_hi:[1,0]
	v_pk_mul_f32 v[16:17], v[20:21], s[6:7] op_sel_hi:[1,0]
	v_pk_mul_f32 v[20:21], v[24:25], s[6:7] op_sel_hi:[1,0]
	v_pk_mul_f32 v[24:25], v[28:29], s[6:7] op_sel_hi:[1,0]
	v_pk_mul_f32 v[28:29], v[32:33], s[6:7] op_sel_hi:[1,0]
	v_pk_mul_f32 v[32:33], v[36:37], s[6:7] op_sel_hi:[1,0]
	v_pk_mul_f32 v[36:37], v[40:41], s[6:7] op_sel_hi:[1,0]
	v_pk_mul_f32 v[40:41], v[44:45], s[6:7] op_sel_hi:[1,0]
	v_pk_mul_f32 v[44:45], v[48:49], s[6:7] op_sel_hi:[1,0]
	v_pk_mul_f32 v[48:49], v[52:53], s[6:7] op_sel_hi:[1,0]
	v_pk_mul_f32 v[52:53], v[56:57], s[6:7] op_sel_hi:[1,0]
	v_pk_mul_f32 v[56:57], v[60:61], s[6:7] op_sel_hi:[1,0]
	v_pk_mul_f32 v[60:61], v[64:65], s[6:7] op_sel_hi:[1,0]
	v_pk_mul_f32 v[64:65], v[72:73], s[6:7] op_sel_hi:[1,0]
	v_med3_f32 v8, v8, s33, v74
	v_med3_f32 v9, v9, s33, v74
	v_med3_f32 v12, v12, s33, v74
	v_med3_f32 v13, v13, s33, v74
	v_med3_f32 v16, v16, s33, v74
	v_med3_f32 v17, v17, s33, v74
	v_med3_f32 v20, v20, s33, v74
	v_med3_f32 v21, v21, s33, v74
	v_med3_f32 v24, v24, s33, v74
	v_med3_f32 v25, v25, s33, v74
	v_med3_f32 v28, v28, s33, v74
	v_med3_f32 v29, v29, s33, v74
	v_med3_f32 v32, v32, s33, v74
	v_med3_f32 v33, v33, s33, v74
	v_med3_f32 v36, v36, s33, v74
	v_med3_f32 v37, v37, s33, v74
	v_med3_f32 v40, v40, s33, v74
	v_med3_f32 v41, v41, s33, v74
	v_med3_f32 v44, v44, s33, v74
	v_med3_f32 v45, v45, s33, v74
	v_med3_f32 v48, v48, s33, v74
	v_med3_f32 v49, v49, s33, v74
	v_med3_f32 v52, v52, s33, v74
	v_med3_f32 v53, v53, s33, v74
	v_med3_f32 v56, v56, s33, v74
	v_med3_f32 v57, v57, s33, v74
	v_med3_f32 v60, v60, s33, v74
	v_med3_f32 v61, v61, s33, v74
	v_med3_f32 v64, v64, s33, v74
	v_med3_f32 v65, v65, s33, v74
	v_cvt_pk_fp8_f32 v5, v98, v99 op_sel:[0,0,1]
	v_cvt_pk_fp8_f32 v75, v8, v9 op_sel:[0,0,1]
	v_cvt_pk_fp8_f32 v82, v12, v13 op_sel:[0,0,1]
	v_cvt_pk_fp8_f32 v83, v16, v17 op_sel:[0,0,1]
	v_cvt_pk_fp8_f32 v84, v20, v21 op_sel:[0,0,1]
	v_cvt_pk_fp8_f32 v85, v24, v25 op_sel:[0,0,1]
	v_cvt_pk_fp8_f32 v86, v28, v29 op_sel:[0,0,1]
	v_cvt_pk_fp8_f32 v87, v32, v33 op_sel:[0,0,1]
	v_cvt_pk_fp8_f32 v88, v36, v37 op_sel:[0,0,1]
	v_cvt_pk_fp8_f32 v89, v40, v41 op_sel:[0,0,1]
	v_cvt_pk_fp8_f32 v90, v44, v45 op_sel:[0,0,1]
	v_cvt_pk_fp8_f32 v91, v48, v49 op_sel:[0,0,1]
	v_cvt_pk_fp8_f32 v92, v52, v53 op_sel:[0,0,1]
	v_cvt_pk_fp8_f32 v93, v56, v57 op_sel:[0,0,1]
	v_cvt_pk_fp8_f32 v94, v60, v61 op_sel:[0,0,1]
	v_cvt_pk_fp8_f32 v95, v64, v65 op_sel:[0,0,1]
	v_perm_b32 v7, v75, v5, s34
	v_perm_b32 v5, v75, v5, s35
	v_perm_b32 v8, v83, v82, s34
	v_perm_b32 v9, v83, v82, s35
	v_perm_b32 v11, v85, v84, s34
	v_perm_b32 v13, v87, v86, s34
	v_perm_b32 v17, v89, v88, s34
	v_perm_b32 v21, v91, v90, s34
	v_perm_b32 v23, v93, v92, s34
	v_perm_b32 v25, v95, v94, s34
	v_perm_b32 v12, v85, v84, s35
	v_perm_b32 v16, v87, v86, s35
	v_perm_b32 v20, v89, v88, s35
	v_perm_b32 v22, v91, v90, s35
	v_perm_b32 v24, v93, v92, s35
	v_perm_b32 v26, v95, v94, s35
	v_perm_b32 v6, v8, v7, s36
	v_perm_b32 v10, v8, v7, s37
	v_perm_b32 v14, v9, v5, s36
	v_perm_b32 v18, v9, v5, s37
	v_perm_b32 v7, v13, v11, s36
	v_perm_b32 v8, v21, v17, s36
	v_perm_b32 v9, v25, v23, s36
	v_perm_b32 v11, v13, v11, s37
	v_perm_b32 v15, v16, v12, s36
	v_perm_b32 v19, v16, v12, s37
	v_perm_b32 v12, v21, v17, s37
	v_perm_b32 v16, v22, v20, s36
	v_perm_b32 v20, v22, v20, s37
	v_perm_b32 v13, v25, v23, s37
	v_perm_b32 v17, v26, v24, s36
	v_perm_b32 v21, v26, v24, s37
	global_store_dwordx4 v[76:77], v[6:9], off nt
	global_store_dwordx4 v[78:79], v[10:13], off nt
	global_store_dwordx4 v[80:81], v[14:17], off nt
	global_store_dwordx4 v[2:3], v[18:21], off nt
	s_waitcnt vmcnt(19)
	v_pk_mul_f32 v[104:105], v[104:105], s[6:7] op_sel_hi:[1,0]
	s_nop 0
	v_med3_f32 v186, v104, s33, v74
	v_med3_f32 v191, v105, s33, v74
	s_waitcnt vmcnt(18)
	v_pk_mul_f32 v[104:105], v[108:109], s[6:7] op_sel_hi:[1,0]
	s_waitcnt vmcnt(17)
	v_pk_mul_f32 v[108:109], v[112:113], s[6:7] op_sel_hi:[1,0]
	s_waitcnt vmcnt(16)
; template <int MODE> __device__ __forceinline__ void cv_finish(const f32x4 (&tv)[16], int K, int nblk, unsigned char* WT, int item, int lane) {
;     const int kb = item / nblk, nb = item - kb * nblk, k0 = 64 * kb + 16 * (lane >> 4), n0 = 64 * nb + 4 * (lane & 15);
;     unsigned D[16];
; #pragma unroll
;     for (int i = 0; i < 16; ++i) { const f32x2 a = (f32x2){tv[i].x, tv[i].y} * (f32x2){1024.f, 1024.f}, b = (f32x2){tv[i].z, tv[i].w} * (f32x2){1024.f, 1024.f};
;         D[i] = pk4_fp8(a.x, a.y, b.x, b.y); }
;     unsigned O[4][4];
; #pragma unroll
;     for (int q = 0; q < 4; ++q) { const unsigned a = D[4 * q], b = D[4 * q + 1], c = D[4 * q + 2], d = D[4 * q + 3];
;         const unsigned t0 = __builtin_amdgcn_perm(b, a, 0x05010400u), t1 = __builtin_amdgcn_perm(b, a, 0x07030602u), u0 = __builtin_amdgcn_perm(d, c, 0x05010400u), u1 = __builtin_amdgcn_perm(d, c, 0x07030602u);
;         O[0][q] = __builtin_amdgcn_perm(u0, t0, 0x05040100u); O[1][q] = __builtin_amdgcn_perm(u0, t0, 0x07060302u); O[2][q] = __builtin_amdgcn_perm(u1, t1, 0x05040100u); O[3][q] = __builtin_amdgcn_perm(u1, t1, 0x07060302u); }
; #pragma unroll
;     for (int j = 0; j < 4; ++j) { u32x4 o; o.x = O[j][0]; o.y = O[j][1]; o.z = O[j][2]; o.w = O[j][3];
;         __builtin_nontemporal_store(o, (u32x4*)(WT + (size_t)drow<MODE>(n0 + j) * K + k0)); }
; }
	v_pk_mul_f32 v[112:113], v[116:117], s[6:7] op_sel_hi:[1,0]
	s_waitcnt vmcnt(15)
	v_pk_mul_f32 v[116:117], v[120:121], s[6:7] op_sel_hi:[1,0]
	s_waitcnt vmcnt(14)
	v_pk_mul_f32 v[120:121], v[124:125], s[6:7] op_sel_hi:[1,0]
	s_waitcnt vmcnt(13)
	v_pk_mul_f32 v[124:125], v[128:129], s[6:7] op_sel_hi:[1,0]
	s_waitcnt vmcnt(12)
	v_pk_mul_f32 v[128:129], v[132:133], s[6:7] op_sel_hi:[1,0]
	s_waitcnt vmcnt(11)
	v_pk_mul_f32 v[132:133], v[136:137], s[6:7] op_sel_hi:[1,0]
	s_waitcnt vmcnt(10)
	v_pk_mul_f32 v[136:137], v[140:141], s[6:7] op_sel_hi:[1,0]
	s_waitcnt vmcnt(9)
	v_pk_mul_f32 v[140:141], v[144:145], s[6:7] op_sel_hi:[1,0]
	s_waitcnt vmcnt(8)
	v_pk_mul_f32 v[144:145], v[148:149], s[6:7] op_sel_hi:[1,0]
	s_waitcnt vmcnt(7)
	v_pk_mul_f32 v[148:149], v[152:153], s[6:7] op_sel_hi:[1,0]
	s_waitcnt vmcnt(6)
	v_pk_mul_f32 v[152:153], v[156:157], s[6:7] op_sel_hi:[1,0]
	s_waitcnt vmcnt(5)
	v_pk_mul_f32 v[156:157], v[160:161], s[6:7] op_sel_hi:[1,0]
	s_waitcnt vmcnt(4)
	v_pk_mul_f32 v[160:161], v[164:165], s[6:7] op_sel_hi:[1,0]
	v_med3_f32 v104, v104, s33, v74
	v_med3_f32 v105, v105, s33, v74
	v_med3_f32 v108, v108, s33, v74
	v_med3_f32 v109, v109, s33, v74
	v_med3_f32 v112, v112, s33, v74
	v_med3_f32 v113, v113, s33, v74
	v_med3_f32 v116, v116, s33, v74
	v_med3_f32 v117, v117, s33, v74
	v_med3_f32 v120, v120, s33, v74
	v_med3_f32 v121, v121, s33, v74
	v_med3_f32 v124, v124, s33, v74
	v_med3_f32 v125, v125, s33, v74
	v_med3_f32 v128, v128, s33, v74
	v_med3_f32 v129, v129, s33, v74
	v_med3_f32 v132, v132, s33, v74
	v_med3_f32 v133, v133, s33, v74
	v_med3_f32 v136, v136, s33, v74
	v_med3_f32 v137, v137, s33, v74
	v_med3_f32 v140, v140, s33, v74
	v_med3_f32 v141, v141, s33, v74
	v_med3_f32 v144, v144, s33, v74
	v_med3_f32 v145, v145, s33, v74
	v_med3_f32 v148, v148, s33, v74
	v_med3_f32 v149, v149, s33, v74
	v_med3_f32 v152, v152, s33, v74
	v_med3_f32 v153, v153, s33, v74
	v_med3_f32 v156, v156, s33, v74
	v_med3_f32 v157, v157, s33, v74
	v_med3_f32 v160, v160, s33, v74
	v_med3_f32 v161, v161, s33, v74
	v_cvt_pk_fp8_f32 v103, v186, v191
	v_cvt_pk_fp8_f32 v169, v104, v105
	v_cvt_pk_fp8_f32 v102, v108, v109
	v_cvt_pk_fp8_f32 v177, v112, v113
	v_cvt_pk_fp8_f32 v168, v116, v117
	v_cvt_pk_fp8_f32 v179, v120, v121
	v_cvt_pk_fp8_f32 v176, v124, v125
	v_cvt_pk_fp8_f32 v181, v128, v129
	v_cvt_pk_fp8_f32 v178, v132, v133
	v_cvt_pk_fp8_f32 v183, v136, v137
	v_cvt_pk_fp8_f32 v180, v140, v141
	v_cvt_pk_fp8_f32 v185, v144, v145
	v_cvt_pk_fp8_f32 v182, v148, v149
	v_cvt_pk_fp8_f32 v187, v152, v153
	v_cvt_pk_fp8_f32 v184, v156, v157
	v_cvt_pk_fp8_f32 v189, v160, v161
	v_pk_mul_f32 v[106:107], v[106:107], s[6:7] op_sel_hi:[1,0]
	s_nop 0
	v_med3_f32 v188, v106, s33, v74
	v_med3_f32 v193, v107, s33, v74
	v_pk_mul_f32 v[106:107], v[110:111], s[6:7] op_sel_hi:[1,0]
	v_pk_mul_f32 v[110:111], v[114:115], s[6:7] op_sel_hi:[1,0]
	v_pk_mul_f32 v[114:115], v[118:119], s[6:7] op_sel_hi:[1,0]
	v_pk_mul_f32 v[118:119], v[122:123], s[6:7] op_sel_hi:[1,0]
	v_pk_mul_f32 v[122:123], v[126:127], s[6:7] op_sel_hi:[1,0]
	v_pk_mul_f32 v[126:127], v[130:131], s[6:7] op_sel_hi:[1,0]
	v_pk_mul_f32 v[130:131], v[134:135], s[6:7] op_sel_hi:[1,0]
	v_pk_mul_f32 v[134:135], v[138:139], s[6:7] op_sel_hi:[1,0]
	v_pk_mul_f32 v[138:139], v[142:143], s[6:7] op_sel_hi:[1,0]
	v_pk_mul_f32 v[142:143], v[146:147], s[6:7] op_sel_hi:[1,0]
	v_pk_mul_f32 v[146:147], v[150:151], s[6:7] op_sel_hi:[1,0]
	v_pk_mul_f32 v[150:151], v[154:155], s[6:7] op_sel_hi:[1,0]
	v_pk_mul_f32 v[154:155], v[158:159], s[6:7] op_sel_hi:[1,0]
	v_pk_mul_f32 v[158:159], v[162:163], s[6:7] op_sel_hi:[1,0]
	v_pk_mul_f32 v[162:163], v[166:167], s[6:7] op_sel_hi:[1,0]
	v_med3_f32 v106, v106, s33, v74
	v_med3_f32 v107, v107, s33, v74
	v_med3_f32 v110, v110, s33, v74
	v_med3_f32 v111, v111, s33, v74
	v_med3_f32 v114, v114, s33, v74
	v_med3_f32 v115, v115, s33, v74
	v_med3_f32 v118, v118, s33, v74
	v_med3_f32 v119, v119, s33, v74
	v_med3_f32 v122, v122, s33, v74
	v_med3_f32 v123, v123, s33, v74
	v_med3_f32 v126, v126, s33, v74
	v_med3_f32 v127, v127, s33, v74
	v_med3_f32 v130, v130, s33, v74
	v_med3_f32 v131, v131, s33, v74
	v_med3_f32 v134, v134, s33, v74
	v_med3_f32 v135, v135, s33, v74
	v_med3_f32 v138, v138, s33, v74
	v_med3_f32 v139, v139, s33, v74
	v_med3_f32 v142, v142, s33, v74
	v_med3_f32 v143, v143, s33, v74
	v_med3_f32 v146, v146, s33, v74
	v_med3_f32 v147, v147, s33, v74
	v_med3_f32 v150, v150, s33, v74
	v_med3_f32 v151, v151, s33, v74
	v_med3_f32 v154, v154, s33, v74
	v_med3_f32 v155, v155, s33, v74
	v_med3_f32 v158, v158, s33, v74
	v_med3_f32 v159, v159, s33, v74
	v_med3_f32 v162, v162, s33, v74
	v_med3_f32 v163, v163, s33, v74
	v_cvt_pk_fp8_f32 v103, v188, v193 op_sel:[0,0,1]
	v_cvt_pk_fp8_f32 v169, v106, v107 op_sel:[0,0,1]
	v_cvt_pk_fp8_f32 v102, v110, v111 op_sel:[0,0,1]
	v_cvt_pk_fp8_f32 v177, v114, v115 op_sel:[0,0,1]
	v_cvt_pk_fp8_f32 v168, v118, v119 op_sel:[0,0,1]
	v_cvt_pk_fp8_f32 v179, v122, v123 op_sel:[0,0,1]
	v_cvt_pk_fp8_f32 v176, v126, v127 op_sel:[0,0,1]
	v_cvt_pk_fp8_f32 v181, v130, v131 op_sel:[0,0,1]
	v_cvt_pk_fp8_f32 v178, v134, v135 op_sel:[0,0,1]
	v_cvt_pk_fp8_f32 v183, v138, v139 op_sel:[0,0,1]
	v_cvt_pk_fp8_f32 v180, v142, v143 op_sel:[0,0,1]
	v_cvt_pk_fp8_f32 v185, v146, v147 op_sel:[0,0,1]
	v_cvt_pk_fp8_f32 v182, v150, v151 op_sel:[0,0,1]
	v_cvt_pk_fp8_f32 v187, v154, v155 op_sel:[0,0,1]
	v_cvt_pk_fp8_f32 v184, v158, v159 op_sel:[0,0,1]
	v_cvt_pk_fp8_f32 v189, v162, v163 op_sel:[0,0,1]
	v_perm_b32 v105, v169, v103, s34
	v_perm_b32 v103, v169, v103, s35
	v_perm_b32 v106, v177, v102, s34
	v_perm_b32 v107, v177, v102, s35
	v_perm_b32 v109, v179, v168, s34
	v_perm_b32 v111, v181, v176, s34
	v_perm_b32 v115, v183, v178, s34
	v_perm_b32 v119, v185, v180, s34
	v_perm_b32 v121, v187, v182, s34
	v_perm_b32 v123, v189, v184, s34
	v_perm_b32 v110, v179, v168, s35
	v_perm_b32 v114, v181, v176, s35
	v_perm_b32 v118, v183, v178, s35
	v_perm_b32 v120, v185, v180, s35
	v_perm_b32 v122, v187, v182, s35
	v_perm_b32 v124, v189, v184, s35
	v_perm_b32 v104, v106, v105, s36
	v_perm_b32 v108, v106, v105, s37
	v_perm_b32 v112, v107, v103, s36
	v_perm_b32 v116, v107, v103, s37
	v_perm_b32 v105, v111, v109, s36
	v_perm_b32 v106, v119, v115, s36
	v_perm_b32 v107, v123, v121, s36
	v_perm_b32 v109, v111, v109, s37
	v_perm_b32 v113, v114, v110, s36
	v_perm_b32 v117, v114, v110, s37
	v_perm_b32 v110, v119, v115, s37
	v_perm_b32 v114, v120, v118, s36
	v_perm_b32 v118, v120, v118, s37
	v_perm_b32 v111, v123, v121, s37
	v_perm_b32 v115, v124, v122, s36
	v_perm_b32 v119, v124, v122, s37
	global_store_dwordx4 v[170:171], v[104:107], off nt
	global_store_dwordx4 v[172:173], v[108:111], off nt
	global_store_dwordx4 v[174:175], v[112:115], off nt
	global_store_dwordx4 v[100:101], v[116:119], off nt
	s_cbranch_scc0 .LBB0_979
	s_mov_b64 s[8:9], 0

; __device__ __forceinline__ void cv_load(const float* W, int N, int nblk, int item, int lane, f32x4 (&tv)[16]) {
;     const int kb = item / nblk, nb = item - kb * nblk; const float* p = W + (size_t)(64 * kb + 16 * (lane >> 4)) * N + 64 * nb + 4 * (lane & 15);
; #pragma unroll
;     for (int i = 0; i < 16; ++i) tv[i] = __builtin_nontemporal_load((const f32x4*)(p + (size_t)i * N));
; }
; template <int MODE> __device__ __forceinline__ void cv_run4(const float* W, int K, int N, unsigned char* WT, int item0, int lane) {
;     const int nblk = N / 64; f32x4 ta[16];
; #pragma unroll 1
;     for (int j = 0; j < 4; ++j) { cv_load(W, N, nblk, item0 + j, lane, ta); cv_finish<MODE>(ta, K, nblk, WT, item0 + j, lane); }
; }
.LBB0_984:
	s_ashr_i32 s12, s4, 31
	s_lshr_b32 s12, s12, 26
	s_add_i32 s12, s4, s12
	s_ashr_i32 s49, s12, 6
	s_andn2_b32 s12, s12, 63
	v_or_b32_e32 v70, s12, v1
	v_ashrrev_i32_e32 v71, 31, v70
	s_lshl_b32 s12, s49, 12
	v_lshlrev_b64 v[2:3], 14, v[70:71]
	s_sub_i32 s12, s47, s12
	v_lshl_add_u64 v[2:3], s[8:9], 0, v[2:3]
	s_ashr_i32 s13, s12, 31
	v_lshl_add_u64 v[2:3], s[12:13], 2, v[2:3]
	v_lshl_add_u64 v[2:3], v[2:3], 0, v[68:69]
	v_add_co_u32_e32 v4, vcc, s18, v2
	v_add_u32_e32 v77, s12, v66
	s_nop 0
	v_addc_co_u32_e32 v5, vcc, 0, v3, vcc
	global_load_dwordx4 v[62:65], v[2:3], off nt
	global_load_dwordx4 v[58:61], v[4:5], off nt
	v_add_co_u32_e32 v4, vcc, s20, v2
	v_add_u32_e32 v72, s48, v75
	s_nop 0
	v_addc_co_u32_e32 v5, vcc, 0, v3, vcc
	s_waitcnt lgkmcnt(0)
	v_add_co_u32_e32 v6, vcc, s22, v2
	s_lshl_b32 s12, s49, 13
	s_nop 0
	v_addc_co_u32_e32 v7, vcc, 0, v3, vcc
	global_load_dwordx4 v[54:57], v[4:5], off nt
	global_load_dwordx4 v[50:53], v[6:7], off nt
	v_add_co_u32_e32 v4, vcc, s24, v2
	v_subrev_u32_e32 v76, s12, v72
	s_nop 0
	v_addc_co_u32_e32 v5, vcc, 0, v3, vcc
	v_add_co_u32_e32 v6, vcc, s26, v2
	v_and_b32_e32 v73, 0x7c, v77
	s_nop 0
	v_addc_co_u32_e32 v7, vcc, 0, v3, vcc
	global_load_dwordx4 v[46:49], v[4:5], off nt
	global_load_dwordx4 v[42:45], v[6:7], off nt
	v_add_co_u32_e32 v4, vcc, s28, v2
	s_nop 1
	v_addc_co_u32_e32 v5, vcc, 0, v3, vcc
	v_add_co_u32_e32 v6, vcc, s30, v2
	s_nop 1
	v_addc_co_u32_e32 v7, vcc, 0, v3, vcc
	global_load_dwordx4 v[38:41], v[4:5], off nt
	global_load_dwordx4 v[34:37], v[6:7], off nt
	v_add_co_u32_e32 v4, vcc, s38, v2
	s_nop 1
	v_addc_co_u32_e32 v5, vcc, 0, v3, vcc
	v_add_co_u32_e32 v6, vcc, s39, v2
	s_nop 1
	v_addc_co_u32_e32 v7, vcc, 0, v3, vcc
	global_load_dwordx4 v[30:33], v[4:5], off nt
	global_load_dwordx4 v[26:29], v[6:7], off nt
	v_add_co_u32_e32 v4, vcc, s40, v2
	s_nop 1
	v_addc_co_u32_e32 v5, vcc, 0, v3, vcc
	v_add_co_u32_e32 v6, vcc, s41, v2
	s_nop 1
	v_addc_co_u32_e32 v7, vcc, 0, v3, vcc
	global_load_dwordx4 v[22:25], v[4:5], off nt
	global_load_dwordx4 v[18:21], v[6:7], off nt
	v_add_co_u32_e32 v4, vcc, s42, v2
	s_nop 1
	v_addc_co_u32_e32 v5, vcc, 0, v3, vcc
	v_add_co_u32_e32 v6, vcc, s43, v2
	s_nop 1
	v_addc_co_u32_e32 v7, vcc, 0, v3, vcc
	global_load_dwordx4 v[14:17], v[4:5], off nt
	global_load_dwordx4 v[10:13], v[6:7], off nt
	v_add_co_u32_e32 v4, vcc, 0x38000, v2
	s_nop 1
	v_addc_co_u32_e32 v5, vcc, 0, v3, vcc
	v_add_co_u32_e32 v2, vcc, 0x3c000, v2
	s_nop 1
	v_addc_co_u32_e32 v3, vcc, 0, v3, vcc
	global_load_dwordx4 v[6:9], v[4:5], off nt
	s_nop 0
	global_load_dwordx4 v[2:5], v[2:3], off nt
	s_addk_i32 s48, 0x80
	s_add_i32 s47, s47, 64
	s_add_i32 s4, s4, 1
	s_ashr_i32 s12, s4, 31
	s_lshr_b32 s12, s12, 26
	s_add_i32 s12, s4, s12
	s_ashr_i32 s49, s12, 6
	s_andn2_b32 s12, s12, 63
	v_or_b32_e32 v146, s12, v1
	v_ashrrev_i32_e32 v147, 31, v146
	s_lshl_b32 s12, s49, 12
	v_lshlrev_b64 v[82:83], 14, v[146:147]
	s_sub_i32 s12, s47, s12
	v_lshl_add_u64 v[82:83], s[8:9], 0, v[82:83]
	s_ashr_i32 s13, s12, 31
	v_lshl_add_u64 v[82:83], s[12:13], 2, v[82:83]
	v_lshl_add_u64 v[82:83], v[82:83], 0, v[68:69]
	v_add_co_u32_e32 v84, vcc, s18, v82
	v_add_u32_e32 v151, s12, v66
	s_nop 0
	v_addc_co_u32_e32 v85, vcc, 0, v83, vcc
	global_load_dwordx4 v[142:145], v[82:83], off nt
	global_load_dwordx4 v[138:141], v[84:85], off nt
	v_add_co_u32_e32 v84, vcc, s20, v82
	v_add_u32_e32 v148, s48, v75
	s_nop 0
	v_addc_co_u32_e32 v85, vcc, 0, v83, vcc
	s_waitcnt lgkmcnt(0)
	v_add_co_u32_e32 v86, vcc, s22, v82
	s_lshl_b32 s12, s49, 13
	s_nop 0
	v_addc_co_u32_e32 v87, vcc, 0, v83, vcc
	global_load_dwordx4 v[134:137], v[84:85], off nt
	global_load_dwordx4 v[130:133], v[86:87], off nt
	v_add_co_u32_e32 v84, vcc, s24, v82
	v_subrev_u32_e32 v150, s12, v148
	s_nop 0
	v_addc_co_u32_e32 v85, vcc, 0, v83, vcc
	v_add_co_u32_e32 v86, vcc, s26, v82
	v_and_b32_e32 v149, 0x7c, v151
	s_nop 0
	v_addc_co_u32_e32 v87, vcc, 0, v83, vcc
	global_load_dwordx4 v[126:129], v[84:85], off nt
	global_load_dwordx4 v[122:125], v[86:87], off nt
	v_add_co_u32_e32 v84, vcc, s28, v82
	s_nop 1
	v_addc_co_u32_e32 v85, vcc, 0, v83, vcc
	v_add_co_u32_e32 v86, vcc, s30, v82
	s_nop 1
	v_addc_co_u32_e32 v87, vcc, 0, v83, vcc
	global_load_dwordx4 v[118:121], v[84:85], off nt
	global_load_dwordx4 v[114:117], v[86:87], off nt
	v_add_co_u32_e32 v84, vcc, s38, v82
	s_nop 1
	v_addc_co_u32_e32 v85, vcc, 0, v83, vcc
	v_add_co_u32_e32 v86, vcc, s39, v82
	s_nop 1
	v_addc_co_u32_e32 v87, vcc, 0, v83, vcc
	global_load_dwordx4 v[110:113], v[84:85], off nt
	global_load_dwordx4 v[106:109], v[86:87], off nt
	v_add_co_u32_e32 v84, vcc, s40, v82
	s_nop 1
	v_addc_co_u32_e32 v85, vcc, 0, v83, vcc
	v_add_co_u32_e32 v86, vcc, s41, v82
	s_nop 1
	v_addc_co_u32_e32 v87, vcc, 0, v83, vcc
	global_load_dwordx4 v[102:105], v[84:85], off nt
	global_load_dwordx4 v[98:101], v[86:87], off nt
	v_add_co_u32_e32 v84, vcc, s42, v82
	s_nop 1
	v_addc_co_u32_e32 v85, vcc, 0, v83, vcc
	v_add_co_u32_e32 v86, vcc, s43, v82
	s_nop 1
	v_addc_co_u32_e32 v87, vcc, 0, v83, vcc
	global_load_dwordx4 v[94:97], v[84:85], off nt
	global_load_dwordx4 v[90:93], v[86:87], off nt
	v_add_co_u32_e32 v84, vcc, 0x38000, v82
	s_nop 1
	v_addc_co_u32_e32 v85, vcc, 0, v83, vcc
	v_add_co_u32_e32 v82, vcc, 0x3c000, v82
	s_nop 1
	v_addc_co_u32_e32 v83, vcc, 0, v83, vcc
	global_load_dwordx4 v[86:89], v[84:85], off nt
	s_nop 0
	global_load_dwordx4 v[82:85], v[82:83], off nt
	s_addk_i32 s48, 0x80
	s_add_i32 s47, s47, 64
	s_add_i32 s4, s4, 1
	v_cmp_lt_i32_e32 vcc, s44, v77
	s_and_saveexec_b64 s[12:13], vcc
	s_xor_b64 s[12:13], exec, s[12:13]
	v_add_u32_e32 v72, 0x7ffff000, v76
	v_and_b32_e32 v72, 0x7fffff00, v72
	v_or3_b32 v72, v73, v72, s45
	s_andn2_saveexec_b64 s[12:13], s[12:13]
	v_and_or_b32 v72, v76, s46, v73
	s_or_b64 exec, exec, s[12:13]
	s_waitcnt vmcnt(31)
; template <int MODE> __device__ __forceinline__ void cv_finish(const f32x4 (&tv)[16], int K, int nblk, unsigned char* WT, int item, int lane) {
;     const int kb = item / nblk, nb = item - kb * nblk, k0 = 64 * kb + 16 * (lane >> 4), n0 = 64 * nb + 4 * (lane & 15);
;     unsigned D[16];
; #pragma unroll
;     for (int i = 0; i < 16; ++i) { const f32x2 a = (f32x2){tv[i].x, tv[i].y} * (f32x2){1024.f, 1024.f}, b = (f32x2){tv[i].z, tv[i].w} * (f32x2){1024.f, 1024.f};
;         D[i] = pk4_fp8(a.x, a.y, b.x, b.y); }
	v_pk_mul_f32 v[62:63], v[62:63], s[6:7] op_sel_hi:[1,0]
	v_pk_mul_f32 v[64:65], v[64:65], s[6:7] op_sel_hi:[1,0]
	v_med3_f32 v73, v62, s33, v74
	v_med3_f32 v63, v63, s33, v74
	v_mov_b32_e32 v62, v69
	v_cvt_pk_fp8_f32 v62, v73, v63
	v_med3_f32 v63, v64, s33, v74
	v_med3_f32 v64, v65, s33, v74
	s_waitcnt vmcnt(30)
	v_pk_mul_f32 v[58:59], v[58:59], s[6:7] op_sel_hi:[1,0]
	v_cvt_pk_fp8_f32 v62, v63, v64 op_sel:[0,0,1]
	v_med3_f32 v63, v58, s33, v74
	v_med3_f32 v59, v59, s33, v74
	v_mov_b32_e32 v58, v69
	v_cvt_pk_fp8_f32 v58, v63, v59
	v_pk_mul_f32 v[60:61], v[60:61], s[6:7] op_sel_hi:[1,0]
	s_waitcnt vmcnt(29)
	v_pk_mul_f32 v[54:55], v[54:55], s[6:7] op_sel_hi:[1,0]
	v_med3_f32 v59, v60, s33, v74
	v_med3_f32 v60, v61, s33, v74
	v_cvt_pk_fp8_f32 v58, v59, v60 op_sel:[0,0,1]
	v_med3_f32 v59, v54, s33, v74
	v_med3_f32 v55, v55, s33, v74
	v_mov_b32_e32 v54, v69
	v_cvt_pk_fp8_f32 v54, v59, v55
	v_pk_mul_f32 v[56:57], v[56:57], s[6:7] op_sel_hi:[1,0]
	s_waitcnt vmcnt(28)
	v_pk_mul_f32 v[50:51], v[50:51], s[6:7] op_sel_hi:[1,0]
	v_med3_f32 v55, v56, s33, v74
	v_med3_f32 v56, v57, s33, v74
	v_cvt_pk_fp8_f32 v54, v55, v56 op_sel:[0,0,1]
	v_med3_f32 v55, v50, s33, v74
	v_med3_f32 v51, v51, s33, v74
	v_mov_b32_e32 v50, v69
	v_cvt_pk_fp8_f32 v50, v55, v51
	v_pk_mul_f32 v[52:53], v[52:53], s[6:7] op_sel_hi:[1,0]
	s_waitcnt vmcnt(27)
	v_pk_mul_f32 v[46:47], v[46:47], s[6:7] op_sel_hi:[1,0]
	v_med3_f32 v51, v52, s33, v74
	v_med3_f32 v52, v53, s33, v74
	v_cvt_pk_fp8_f32 v50, v51, v52 op_sel:[0,0,1]
	v_med3_f32 v51, v46, s33, v74
	v_med3_f32 v47, v47, s33, v74
	v_mov_b32_e32 v46, v69
	v_cvt_pk_fp8_f32 v46, v51, v47
	v_pk_mul_f32 v[48:49], v[48:49], s[6:7] op_sel_hi:[1,0]
	s_waitcnt vmcnt(26)
	v_pk_mul_f32 v[42:43], v[42:43], s[6:7] op_sel_hi:[1,0]
	v_med3_f32 v47, v48, s33, v74
	v_med3_f32 v48, v49, s33, v74
	v_cvt_pk_fp8_f32 v46, v47, v48 op_sel:[0,0,1]
	v_med3_f32 v47, v42, s33, v74
	v_med3_f32 v43, v43, s33, v74
	v_mov_b32_e32 v42, v69
	v_cvt_pk_fp8_f32 v42, v47, v43
	v_pk_mul_f32 v[44:45], v[44:45], s[6:7] op_sel_hi:[1,0]
	s_waitcnt vmcnt(25)
	v_pk_mul_f32 v[38:39], v[38:39], s[6:7] op_sel_hi:[1,0]
	v_med3_f32 v43, v44, s33, v74
	v_med3_f32 v44, v45, s33, v74
	v_cvt_pk_fp8_f32 v42, v43, v44 op_sel:[0,0,1]
	v_med3_f32 v43, v38, s33, v74
	v_med3_f32 v39, v39, s33, v74
	v_mov_b32_e32 v38, v69
	v_cvt_pk_fp8_f32 v38, v43, v39
	v_pk_mul_f32 v[40:41], v[40:41], s[6:7] op_sel_hi:[1,0]
	s_waitcnt vmcnt(24)
	v_pk_mul_f32 v[34:35], v[34:35], s[6:7] op_sel_hi:[1,0]
	v_med3_f32 v39, v40, s33, v74
	v_med3_f32 v40, v41, s33, v74
	v_cvt_pk_fp8_f32 v38, v39, v40 op_sel:[0,0,1]
	v_med3_f32 v39, v34, s33, v74
	v_med3_f32 v35, v35, s33, v74
	v_mov_b32_e32 v34, v69
	v_cvt_pk_fp8_f32 v34, v39, v35
	v_pk_mul_f32 v[36:37], v[36:37], s[6:7] op_sel_hi:[1,0]
	s_waitcnt vmcnt(23)
	v_pk_mul_f32 v[30:31], v[30:31], s[6:7] op_sel_hi:[1,0]
	v_med3_f32 v35, v36, s33, v74
	v_med3_f32 v36, v37, s33, v74
	v_cvt_pk_fp8_f32 v34, v35, v36 op_sel:[0,0,1]
	v_med3_f32 v35, v30, s33, v74
	v_med3_f32 v31, v31, s33, v74
	v_mov_b32_e32 v30, v69
	v_cvt_pk_fp8_f32 v30, v35, v31
	v_pk_mul_f32 v[32:33], v[32:33], s[6:7] op_sel_hi:[1,0]
	s_waitcnt vmcnt(22)
	v_pk_mul_f32 v[26:27], v[26:27], s[6:7] op_sel_hi:[1,0]
	v_med3_f32 v31, v32, s33, v74
	v_med3_f32 v32, v33, s33, v74
	v_cvt_pk_fp8_f32 v30, v31, v32 op_sel:[0,0,1]
	v_med3_f32 v31, v26, s33, v74
	v_med3_f32 v27, v27, s33, v74
	v_mov_b32_e32 v26, v69
	v_cvt_pk_fp8_f32 v26, v31, v27
	v_pk_mul_f32 v[28:29], v[28:29], s[6:7] op_sel_hi:[1,0]
	s_waitcnt vmcnt(21)
	v_pk_mul_f32 v[22:23], v[22:23], s[6:7] op_sel_hi:[1,0]
	v_med3_f32 v27, v28, s33, v74
	v_med3_f32 v28, v29, s33, v74
	v_cvt_pk_fp8_f32 v26, v27, v28 op_sel:[0,0,1]
	v_med3_f32 v27, v22, s33, v74
	v_med3_f32 v23, v23, s33, v74
	v_mov_b32_e32 v22, v69
	v_cvt_pk_fp8_f32 v22, v27, v23
	v_pk_mul_f32 v[24:25], v[24:25], s[6:7] op_sel_hi:[1,0]
	s_waitcnt vmcnt(20)
	v_pk_mul_f32 v[18:19], v[18:19], s[6:7] op_sel_hi:[1,0]
	v_med3_f32 v23, v24, s33, v74
	v_med3_f32 v24, v25, s33, v74
	v_cvt_pk_fp8_f32 v22, v23, v24 op_sel:[0,0,1]
	v_med3_f32 v23, v18, s33, v74
	v_med3_f32 v19, v19, s33, v74
	v_mov_b32_e32 v18, v69
	v_cvt_pk_fp8_f32 v18, v23, v19
	v_pk_mul_f32 v[20:21], v[20:21], s[6:7] op_sel_hi:[1,0]
	s_waitcnt vmcnt(19)
	v_pk_mul_f32 v[14:15], v[14:15], s[6:7] op_sel_hi:[1,0]
	v_med3_f32 v19, v20, s33, v74
	v_med3_f32 v20, v21, s33, v74
	v_cvt_pk_fp8_f32 v18, v19, v20 op_sel:[0,0,1]
	v_med3_f32 v19, v14, s33, v74
	v_med3_f32 v15, v15, s33, v74
	v_mov_b32_e32 v14, v69
	v_cvt_pk_fp8_f32 v14, v19, v15
	v_pk_mul_f32 v[16:17], v[16:17], s[6:7] op_sel_hi:[1,0]
	s_waitcnt vmcnt(18)
	v_pk_mul_f32 v[10:11], v[10:11], s[6:7] op_sel_hi:[1,0]
	v_med3_f32 v15, v16, s33, v74
	v_med3_f32 v16, v17, s33, v74
	v_cvt_pk_fp8_f32 v14, v15, v16 op_sel:[0,0,1]
	v_med3_f32 v15, v10, s33, v74
	v_med3_f32 v11, v11, s33, v74
	v_mov_b32_e32 v10, v69
	v_cvt_pk_fp8_f32 v10, v15, v11
	v_pk_mul_f32 v[12:13], v[12:13], s[6:7] op_sel_hi:[1,0]
	s_waitcnt vmcnt(17)
	v_pk_mul_f32 v[6:7], v[6:7], s[6:7] op_sel_hi:[1,0]
	v_med3_f32 v11, v12, s33, v74
	v_med3_f32 v12, v13, s33, v74
	v_cvt_pk_fp8_f32 v10, v11, v12 op_sel:[0,0,1]
	v_med3_f32 v11, v6, s33, v74
	v_med3_f32 v7, v7, s33, v74
	v_mov_b32_e32 v6, v69
	v_cvt_pk_fp8_f32 v6, v11, v7
	v_pk_mul_f32 v[8:9], v[8:9], s[6:7] op_sel_hi:[1,0]
	s_waitcnt vmcnt(16)
; template <int MODE> __device__ __forceinline__ int drow(int n) {
;     if (MODE == 1) { const int h = n / 192, nl = n - h * 192; return nl < 128 ? n : h * 192 + 128 + ((nl - 128) & 31) * 2 + ((nl - 128) >> 5); }
;     if (MODE == 2) { return n < FF ? ((n >> 7) * 256 + (n & 127)) : (((n - FF) >> 7) * 256 + 128 + ((n - FF) & 127)); }
;     return n;
; }
; template <int MODE> __device__ __forceinline__ void cv_finish(const f32x4 (&tv)[16], int K, int nblk, unsigned char* WT, int item, int lane) {
;     const int kb = item / nblk, nb = item - kb * nblk, k0 = 64 * kb + 16 * (lane >> 4), n0 = 64 * nb + 4 * (lane & 15);
;     unsigned D[16];
; #pragma unroll
;     for (int i = 0; i < 16; ++i) { const f32x2 a = (f32x2){tv[i].x, tv[i].y} * (f32x2){1024.f, 1024.f}, b = (f32x2){tv[i].z, tv[i].w} * (f32x2){1024.f, 1024.f};
;         D[i] = pk4_fp8(a.x, a.y, b.x, b.y); }
;     unsigned O[4][4];
; #pragma unroll
;     for (int q = 0; q < 4; ++q) { const unsigned a = D[4 * q], b = D[4 * q + 1], c = D[4 * q + 2], d = D[4 * q + 3];
;         const unsigned t0 = __builtin_amdgcn_perm(b, a, 0x05010400u), t1 = __builtin_amdgcn_perm(b, a, 0x07030602u), u0 = __builtin_amdgcn_perm(d, c, 0x05010400u), u1 = __builtin_amdgcn_perm(d, c, 0x07030602u);
;         O[0][q] = __builtin_amdgcn_perm(u0, t0, 0x05040100u); O[1][q] = __builtin_amdgcn_perm(u0, t0, 0x07060302u); O[2][q] = __builtin_amdgcn_perm(u1, t1, 0x05040100u); O[3][q] = __builtin_amdgcn_perm(u1, t1, 0x07060302u); }
; #pragma unroll
;     for (int j = 0; j < 4; ++j) { u32x4 o; o.x = O[j][0]; o.y = O[j][1]; o.z = O[j][2]; o.w = O[j][3];
;         __builtin_nontemporal_store(o, (u32x4*)(WT + (size_t)drow<MODE>(n0 + j) * K + k0)); }
; }
	v_pk_mul_f32 v[2:3], v[2:3], s[6:7] op_sel_hi:[1,0]
	v_med3_f32 v7, v8, s33, v74
	v_med3_f32 v8, v9, s33, v74
	v_cvt_pk_fp8_f32 v6, v7, v8 op_sel:[0,0,1]
	v_med3_f32 v2, v2, s33, v74
	v_med3_f32 v3, v3, s33, v74
	v_mov_b32_e32 v7, v69
	v_cvt_pk_fp8_f32 v7, v2, v3
	v_pk_mul_f32 v[2:3], v[4:5], s[6:7] op_sel_hi:[1,0]
	v_ashrrev_i32_e32 v73, 31, v72
	v_med3_f32 v2, v2, s33, v74
	v_med3_f32 v3, v3, s33, v74
	v_cvt_pk_fp8_f32 v7, v2, v3 op_sel:[0,0,1]
	v_perm_b32 v5, v58, v62, s34
	v_perm_b32 v8, v50, v54, s34
	v_perm_b32 v9, v42, v46, s34
	v_perm_b32 v11, v34, v38, s34
	v_perm_b32 v12, v26, v30, s34
	v_perm_b32 v13, v18, v22, s34
	v_perm_b32 v15, v10, v14, s34
	v_perm_b32 v16, v7, v6, s34
	v_lshl_add_u64 v[2:3], s[10:11], 0, v[70:71]
	v_lshlrev_b64 v[20:21], 11, v[72:73]
	v_add_u32_e32 v4, 1, v77
	v_perm_b32 v78, v8, v5, s36
	v_perm_b32 v79, v11, v9, s36
	v_perm_b32 v80, v13, v12, s36
	v_perm_b32 v81, v16, v15, s36
	v_lshl_add_u64 v[20:21], v[2:3], 0, v[20:21]
	v_cmp_lt_i32_e32 vcc, s44, v4
	v_and_b32_e32 v17, 0x7d, v4
	global_store_dwordx4 v[20:21], v[78:81], off nt
	s_and_saveexec_b64 s[12:13], vcc
	s_xor_b64 s[12:13], exec, s[12:13]
	v_add_u32_e32 v4, 0x7ffff002, v76
	v_and_b32_e32 v4, 0x7fffff00, v4
	v_or3_b32 v4, v17, v4, s45
	s_andn2_saveexec_b64 s[12:13], s[12:13]
	v_add_u32_e32 v4, 2, v76
	v_and_or_b32 v4, v4, s46, v17
	s_or_b64 exec, exec, s[12:13]
	v_perm_b32 v70, v8, v5, s37
	v_ashrrev_i32_e32 v5, 31, v4
	v_lshlrev_b64 v[4:5], 11, v[4:5]
	v_perm_b32 v71, v11, v9, s37
	v_perm_b32 v72, v13, v12, s37
	v_perm_b32 v73, v16, v15, s37
	v_lshl_add_u64 v[4:5], v[2:3], 0, v[4:5]
	global_store_dwordx4 v[4:5], v[70:73], off nt
	v_add_u32_e32 v4, 2, v77
	v_cmp_lt_i32_e32 vcc, s44, v4
	v_and_b32_e32 v5, 0x7e, v4
	s_and_saveexec_b64 s[12:13], vcc
	s_xor_b64 s[12:13], exec, s[12:13]
	v_add_u32_e32 v4, 0x7ffff004, v76
	v_and_b32_e32 v4, 0x7fffff00, v4
	v_or3_b32 v4, v5, v4, s45
	s_andn2_saveexec_b64 s[12:13], s[12:13]
	v_add_u32_e32 v4, 4, v76
	v_and_or_b32 v4, v4, s46, v5
	s_or_b64 exec, exec, s[12:13]
	v_ashrrev_i32_e32 v5, 31, v4
	v_perm_b32 v8, v58, v62, s35
	v_perm_b32 v9, v50, v54, s35
	v_perm_b32 v11, v42, v46, s35
	v_perm_b32 v12, v34, v38, s35
	v_perm_b32 v13, v26, v30, s35
	v_perm_b32 v15, v18, v22, s35
	v_perm_b32 v10, v10, v14, s35
	v_perm_b32 v6, v7, v6, s35
	v_lshlrev_b64 v[4:5], 11, v[4:5]
	v_perm_b32 v16, v9, v8, s36
	v_perm_b32 v17, v12, v11, s36
	v_perm_b32 v18, v15, v13, s36
	v_perm_b32 v19, v6, v10, s36
	v_lshl_add_u64 v[4:5], v[2:3], 0, v[4:5]
	global_store_dwordx4 v[4:5], v[16:19], off nt
	v_add_u32_e32 v4, 3, v77
	v_cmp_lt_i32_e32 vcc, s44, v4
	v_and_b32_e32 v5, 0x7f, v4
	s_and_saveexec_b64 s[12:13], vcc
	s_xor_b64 s[12:13], exec, s[12:13]
	v_add_u32_e32 v4, 0x7ffff006, v76
	v_and_b32_e32 v4, 0x7fffff00, v4
	v_or3_b32 v4, v5, v4, s45
	s_andn2_saveexec_b64 s[12:13], s[12:13]
	v_add_u32_e32 v4, 6, v76
	v_and_or_b32 v4, v4, s46, v5
	s_or_b64 exec, exec, s[12:13]
	v_ashrrev_i32_e32 v5, 31, v4
	v_lshlrev_b64 v[4:5], 11, v[4:5]
	v_perm_b32 v16, v9, v8, s37
	v_perm_b32 v17, v12, v11, s37
	v_perm_b32 v18, v15, v13, s37
	v_perm_b32 v19, v6, v10, s37
	v_lshl_add_u64 v[2:3], v[2:3], 0, v[4:5]
	global_store_dwordx4 v[2:3], v[16:19], off nt
	v_cmp_lt_i32_e32 vcc, s44, v151
	s_and_saveexec_b64 s[12:13], vcc
	s_xor_b64 s[12:13], exec, s[12:13]
	v_add_u32_e32 v148, 0x7ffff000, v150
	v_and_b32_e32 v148, 0x7fffff00, v148
	v_or3_b32 v148, v149, v148, s45
	s_andn2_saveexec_b64 s[12:13], s[12:13]
	v_and_or_b32 v148, v150, s46, v149
	s_or_b64 exec, exec, s[12:13]
	s_waitcnt vmcnt(19)
	v_pk_mul_f32 v[142:143], v[142:143], s[6:7] op_sel_hi:[1,0]
	v_pk_mul_f32 v[144:145], v[144:145], s[6:7] op_sel_hi:[1,0]
	v_med3_f32 v149, v142, s33, v74
	v_med3_f32 v143, v143, s33, v74
	v_mov_b32_e32 v142, v69
	v_cvt_pk_fp8_f32 v142, v149, v143
	v_med3_f32 v143, v144, s33, v74
	v_med3_f32 v144, v145, s33, v74
	s_waitcnt vmcnt(18)
	v_pk_mul_f32 v[138:139], v[138:139], s[6:7] op_sel_hi:[1,0]
	v_cvt_pk_fp8_f32 v142, v143, v144 op_sel:[0,0,1]
	v_med3_f32 v143, v138, s33, v74
	v_med3_f32 v139, v139, s33, v74
	v_mov_b32_e32 v138, v69
	v_cvt_pk_fp8_f32 v138, v143, v139
	v_pk_mul_f32 v[140:141], v[140:141], s[6:7] op_sel_hi:[1,0]
	s_waitcnt vmcnt(17)
	v_pk_mul_f32 v[134:135], v[134:135], s[6:7] op_sel_hi:[1,0]
	v_med3_f32 v139, v140, s33, v74
	v_med3_f32 v140, v141, s33, v74
	v_cvt_pk_fp8_f32 v138, v139, v140 op_sel:[0,0,1]
	v_med3_f32 v139, v134, s33, v74
	v_med3_f32 v135, v135, s33, v74
	v_mov_b32_e32 v134, v69
	v_cvt_pk_fp8_f32 v134, v139, v135
	v_pk_mul_f32 v[136:137], v[136:137], s[6:7] op_sel_hi:[1,0]
	s_waitcnt vmcnt(16)
	v_pk_mul_f32 v[130:131], v[130:131], s[6:7] op_sel_hi:[1,0]
	v_med3_f32 v135, v136, s33, v74
	v_med3_f32 v136, v137, s33, v74
	v_cvt_pk_fp8_f32 v134, v135, v136 op_sel:[0,0,1]
	v_med3_f32 v135, v130, s33, v74
	v_med3_f32 v131, v131, s33, v74
	v_mov_b32_e32 v130, v69
	v_cvt_pk_fp8_f32 v130, v135, v131
	v_pk_mul_f32 v[132:133], v[132:133], s[6:7] op_sel_hi:[1,0]
	s_waitcnt vmcnt(15)
	v_pk_mul_f32 v[126:127], v[126:127], s[6:7] op_sel_hi:[1,0]
	v_med3_f32 v131, v132, s33, v74
	v_med3_f32 v132, v133, s33, v74
	v_cvt_pk_fp8_f32 v130, v131, v132 op_sel:[0,0,1]
	v_med3_f32 v131, v126, s33, v74
	v_med3_f32 v127, v127, s33, v74
	v_mov_b32_e32 v126, v69
	v_cvt_pk_fp8_f32 v126, v131, v127
	v_pk_mul_f32 v[128:129], v[128:129], s[6:7] op_sel_hi:[1,0]
	s_waitcnt vmcnt(14)
	v_pk_mul_f32 v[122:123], v[122:123], s[6:7] op_sel_hi:[1,0]
	v_med3_f32 v127, v128, s33, v74
	v_med3_f32 v128, v129, s33, v74
	v_cvt_pk_fp8_f32 v126, v127, v128 op_sel:[0,0,1]
	v_med3_f32 v127, v122, s33, v74
	v_med3_f32 v123, v123, s33, v74
	v_mov_b32_e32 v122, v69
	v_cvt_pk_fp8_f32 v122, v127, v123
	v_pk_mul_f32 v[124:125], v[124:125], s[6:7] op_sel_hi:[1,0]
	s_waitcnt vmcnt(13)
; template <int MODE> __device__ __forceinline__ void cv_finish(const f32x4 (&tv)[16], int K, int nblk, unsigned char* WT, int item, int lane) {
;     const int kb = item / nblk, nb = item - kb * nblk, k0 = 64 * kb + 16 * (lane >> 4), n0 = 64 * nb + 4 * (lane & 15);
;     unsigned D[16];
; #pragma unroll
;     for (int i = 0; i < 16; ++i) { const f32x2 a = (f32x2){tv[i].x, tv[i].y} * (f32x2){1024.f, 1024.f}, b = (f32x2){tv[i].z, tv[i].w} * (f32x2){1024.f, 1024.f};
;         D[i] = pk4_fp8(a.x, a.y, b.x, b.y); }
;     unsigned O[4][4];
; #pragma unroll
;     for (int q = 0; q < 4; ++q) { const unsigned a = D[4 * q], b = D[4 * q + 1], c = D[4 * q + 2], d = D[4 * q + 3];
;         const unsigned t0 = __builtin_amdgcn_perm(b, a, 0x05010400u), t1 = __builtin_amdgcn_perm(b, a, 0x07030602u), u0 = __builtin_amdgcn_perm(d, c, 0x05010400u), u1 = __builtin_amdgcn_perm(d, c, 0x07030602u);
;         O[0][q] = __builtin_amdgcn_perm(u0, t0, 0x05040100u); O[1][q] = __builtin_amdgcn_perm(u0, t0, 0x07060302u); O[2][q] = __builtin_amdgcn_perm(u1, t1, 0x05040100u); O[3][q] = __builtin_amdgcn_perm(u1, t1, 0x07060302u); }
; #pragma unroll
;     for (int j = 0; j < 4; ++j) { u32x4 o; o.x = O[j][0]; o.y = O[j][1]; o.z = O[j][2]; o.w = O[j][3];
;         __builtin_nontemporal_store(o, (u32x4*)(WT + (size_t)drow<MODE>(n0 + j) * K + k0)); }
; }
	v_pk_mul_f32 v[118:119], v[118:119], s[6:7] op_sel_hi:[1,0]
	v_med3_f32 v123, v124, s33, v74
	v_med3_f32 v124, v125, s33, v74
	v_cvt_pk_fp8_f32 v122, v123, v124 op_sel:[0,0,1]
	v_med3_f32 v123, v118, s33, v74
	v_med3_f32 v119, v119, s33, v74
	v_mov_b32_e32 v118, v69
	v_cvt_pk_fp8_f32 v118, v123, v119
	v_pk_mul_f32 v[120:121], v[120:121], s[6:7] op_sel_hi:[1,0]
	s_waitcnt vmcnt(12)
	v_pk_mul_f32 v[114:115], v[114:115], s[6:7] op_sel_hi:[1,0]
	v_med3_f32 v119, v120, s33, v74
	v_med3_f32 v120, v121, s33, v74
	v_cvt_pk_fp8_f32 v118, v119, v120 op_sel:[0,0,1]
	v_med3_f32 v119, v114, s33, v74
	v_med3_f32 v115, v115, s33, v74
	v_mov_b32_e32 v114, v69
	v_cvt_pk_fp8_f32 v114, v119, v115
	v_pk_mul_f32 v[116:117], v[116:117], s[6:7] op_sel_hi:[1,0]
	s_waitcnt vmcnt(11)
	v_pk_mul_f32 v[110:111], v[110:111], s[6:7] op_sel_hi:[1,0]
	v_med3_f32 v115, v116, s33, v74
	v_med3_f32 v116, v117, s33, v74
	v_cvt_pk_fp8_f32 v114, v115, v116 op_sel:[0,0,1]
	v_med3_f32 v115, v110, s33, v74
	v_med3_f32 v111, v111, s33, v74
	v_mov_b32_e32 v110, v69
	v_cvt_pk_fp8_f32 v110, v115, v111
	v_pk_mul_f32 v[112:113], v[112:113], s[6:7] op_sel_hi:[1,0]
	s_waitcnt vmcnt(10)
	v_pk_mul_f32 v[106:107], v[106:107], s[6:7] op_sel_hi:[1,0]
	v_med3_f32 v111, v112, s33, v74
	v_med3_f32 v112, v113, s33, v74
	v_cvt_pk_fp8_f32 v110, v111, v112 op_sel:[0,0,1]
	v_med3_f32 v111, v106, s33, v74
	v_med3_f32 v107, v107, s33, v74
	v_mov_b32_e32 v106, v69
	v_cvt_pk_fp8_f32 v106, v111, v107
	v_pk_mul_f32 v[108:109], v[108:109], s[6:7] op_sel_hi:[1,0]
	s_waitcnt vmcnt(9)
	v_pk_mul_f32 v[102:103], v[102:103], s[6:7] op_sel_hi:[1,0]
	v_med3_f32 v107, v108, s33, v74
	v_med3_f32 v108, v109, s33, v74
	v_cvt_pk_fp8_f32 v106, v107, v108 op_sel:[0,0,1]
	v_med3_f32 v107, v102, s33, v74
	v_med3_f32 v103, v103, s33, v74
	v_mov_b32_e32 v102, v69
	v_cvt_pk_fp8_f32 v102, v107, v103
	v_pk_mul_f32 v[104:105], v[104:105], s[6:7] op_sel_hi:[1,0]
	s_waitcnt vmcnt(8)
	v_pk_mul_f32 v[98:99], v[98:99], s[6:7] op_sel_hi:[1,0]
	v_med3_f32 v103, v104, s33, v74
	v_med3_f32 v104, v105, s33, v74
	v_cvt_pk_fp8_f32 v102, v103, v104 op_sel:[0,0,1]
	v_med3_f32 v103, v98, s33, v74
	v_med3_f32 v99, v99, s33, v74
	v_mov_b32_e32 v98, v69
	v_cvt_pk_fp8_f32 v98, v103, v99
	v_pk_mul_f32 v[100:101], v[100:101], s[6:7] op_sel_hi:[1,0]
	s_waitcnt vmcnt(7)
	v_pk_mul_f32 v[94:95], v[94:95], s[6:7] op_sel_hi:[1,0]
	v_med3_f32 v99, v100, s33, v74
	v_med3_f32 v100, v101, s33, v74
	v_cvt_pk_fp8_f32 v98, v99, v100 op_sel:[0,0,1]
	v_med3_f32 v99, v94, s33, v74
	v_med3_f32 v95, v95, s33, v74
	v_mov_b32_e32 v94, v69
	v_cvt_pk_fp8_f32 v94, v99, v95
	v_pk_mul_f32 v[96:97], v[96:97], s[6:7] op_sel_hi:[1,0]
	s_waitcnt vmcnt(6)
	v_pk_mul_f32 v[90:91], v[90:91], s[6:7] op_sel_hi:[1,0]
	v_med3_f32 v95, v96, s33, v74
	v_med3_f32 v96, v97, s33, v74
	v_cvt_pk_fp8_f32 v94, v95, v96 op_sel:[0,0,1]
	v_med3_f32 v95, v90, s33, v74
	v_med3_f32 v91, v91, s33, v74
	v_mov_b32_e32 v90, v69
	v_cvt_pk_fp8_f32 v90, v95, v91
	v_pk_mul_f32 v[92:93], v[92:93], s[6:7] op_sel_hi:[1,0]
	s_waitcnt vmcnt(5)
	v_pk_mul_f32 v[86:87], v[86:87], s[6:7] op_sel_hi:[1,0]
	v_med3_f32 v91, v92, s33, v74
	v_med3_f32 v92, v93, s33, v74
	v_cvt_pk_fp8_f32 v90, v91, v92 op_sel:[0,0,1]
	v_med3_f32 v91, v86, s33, v74
	v_med3_f32 v87, v87, s33, v74
	v_mov_b32_e32 v86, v69
	v_cvt_pk_fp8_f32 v86, v91, v87
	v_pk_mul_f32 v[88:89], v[88:89], s[6:7] op_sel_hi:[1,0]
	s_waitcnt vmcnt(4)
	v_pk_mul_f32 v[82:83], v[82:83], s[6:7] op_sel_hi:[1,0]
	v_med3_f32 v87, v88, s33, v74
	v_med3_f32 v88, v89, s33, v74
	v_cvt_pk_fp8_f32 v86, v87, v88 op_sel:[0,0,1]
	v_med3_f32 v82, v82, s33, v74
	v_med3_f32 v83, v83, s33, v74
	v_mov_b32_e32 v87, v69
	v_cvt_pk_fp8_f32 v87, v82, v83
	v_pk_mul_f32 v[82:83], v[84:85], s[6:7] op_sel_hi:[1,0]
	v_ashrrev_i32_e32 v149, 31, v148
	v_med3_f32 v82, v82, s33, v74
	v_med3_f32 v83, v83, s33, v74
	v_cvt_pk_fp8_f32 v87, v82, v83 op_sel:[0,0,1]
	v_perm_b32 v85, v138, v142, s34
	v_perm_b32 v88, v130, v134, s34
	v_perm_b32 v89, v122, v126, s34
	v_perm_b32 v91, v114, v118, s34
	v_perm_b32 v92, v106, v110, s34
	v_perm_b32 v93, v98, v102, s34
	v_perm_b32 v95, v90, v94, s34
	v_perm_b32 v96, v87, v86, s34
	v_lshl_add_u64 v[82:83], s[10:11], 0, v[146:147]
	v_lshlrev_b64 v[100:101], 11, v[148:149]
	v_add_u32_e32 v84, 1, v151
	v_perm_b32 v152, v88, v85, s36
	v_perm_b32 v153, v91, v89, s36
	v_perm_b32 v154, v93, v92, s36
	v_perm_b32 v155, v96, v95, s36
	v_lshl_add_u64 v[100:101], v[82:83], 0, v[100:101]
	v_cmp_lt_i32_e32 vcc, s44, v84
	v_and_b32_e32 v97, 0x7d, v84
	global_store_dwordx4 v[100:101], v[152:155], off nt
	s_and_saveexec_b64 s[12:13], vcc
	s_xor_b64 s[12:13], exec, s[12:13]
	v_add_u32_e32 v84, 0x7ffff002, v150
	v_and_b32_e32 v84, 0x7fffff00, v84
	v_or3_b32 v84, v97, v84, s45
	s_andn2_saveexec_b64 s[12:13], s[12:13]
	v_add_u32_e32 v84, 2, v150
	v_and_or_b32 v84, v84, s46, v97
	s_or_b64 exec, exec, s[12:13]
	v_perm_b32 v146, v88, v85, s37
	v_ashrrev_i32_e32 v85, 31, v84
	v_lshlrev_b64 v[84:85], 11, v[84:85]
	v_perm_b32 v147, v91, v89, s37
	v_perm_b32 v148, v93, v92, s37
	v_perm_b32 v149, v96, v95, s37
	v_lshl_add_u64 v[84:85], v[82:83], 0, v[84:85]
	global_store_dwordx4 v[84:85], v[146:149], off nt
	v_add_u32_e32 v84, 2, v151
	v_cmp_lt_i32_e32 vcc, s44, v84
	v_and_b32_e32 v85, 0x7e, v84
	s_and_saveexec_b64 s[12:13], vcc
	s_xor_b64 s[12:13], exec, s[12:13]
	v_add_u32_e32 v84, 0x7ffff004, v150
	v_and_b32_e32 v84, 0x7fffff00, v84
	v_or3_b32 v84, v85, v84, s45
	s_andn2_saveexec_b64 s[12:13], s[12:13]
	v_add_u32_e32 v84, 4, v150
	v_and_or_b32 v84, v84, s46, v85
	s_or_b64 exec, exec, s[12:13]
	v_ashrrev_i32_e32 v85, 31, v84
	v_perm_b32 v88, v138, v142, s35
	v_perm_b32 v89, v130, v134, s35
	v_perm_b32 v91, v122, v126, s35
	v_perm_b32 v92, v114, v118, s35
	v_perm_b32 v93, v106, v110, s35
	v_perm_b32 v95, v98, v102, s35
	v_perm_b32 v90, v90, v94, s35
	v_perm_b32 v86, v87, v86, s35
	v_lshlrev_b64 v[84:85], 11, v[84:85]
	v_perm_b32 v96, v89, v88, s36
	v_perm_b32 v97, v92, v91, s36
	v_perm_b32 v98, v95, v93, s36
	v_perm_b32 v99, v86, v90, s36
	v_lshl_add_u64 v[84:85], v[82:83], 0, v[84:85]
	global_store_dwordx4 v[84:85], v[96:99], off nt
	v_add_u32_e32 v84, 3, v151
	v_cmp_lt_i32_e32 vcc, s44, v84
	v_and_b32_e32 v85, 0x7f, v84
	s_and_saveexec_b64 s[12:13], vcc
	s_xor_b64 s[12:13], exec, s[12:13]
	v_add_u32_e32 v84, 0x7ffff006, v150
	v_and_b32_e32 v84, 0x7fffff00, v84
	v_or3_b32 v84, v85, v84, s45
	s_andn2_saveexec_b64 s[12:13], s[12:13]
	v_add_u32_e32 v84, 6, v150
	v_and_or_b32 v84, v84, s46, v85
	s_or_b64 exec, exec, s[12:13]
	v_ashrrev_i32_e32 v85, 31, v84
	v_lshlrev_b64 v[84:85], 11, v[84:85]
	v_perm_b32 v96, v89, v88, s37
	v_perm_b32 v97, v92, v91, s37
	v_perm_b32 v98, v95, v93, s37
	v_perm_b32 v99, v86, v90, s37
	v_lshl_add_u64 v[82:83], v[82:83], 0, v[84:85]
	global_store_dwordx4 v[82:83], v[96:99], off nt
	s_cmpk_eq_i32 s48, 0x200
	s_cbranch_scc0 .LBB0_984
	s_branch .LBB0_970
